# RWKV output store issues unconditionally and the chunk-load wait no longer covers its acknowledgement; RWKV workgroups convert 8 rows per wave of the layer-0 u table after the recurrence
# speedup vs baseline: 1.0108x; 1.0077x over previous
; __device__ __forceinline__ void peer_row_load(f32x4 (&v)[16], const float* const (&in)[34], int it, int layer, int lane) {
;     const int tbl = it >= NEXP, r = it - tbl * NEXP + layer * NEXP;
;     const f32x4* src = (const f32x4*)((tbl ? in[33] : in[32]) + (size_t)r * D) + lane;
; #pragma unroll
;     for (int j = 0; j < 16; ++j) v[j] = src[64 * j];
; }
;     f32x4 va[16], vb[16];
;     if (it_lo + gw >= it_hi) return;
;     peer_row_load(va, in, it_lo + gw, only_layer, lane);
; #pragma unroll 1
;     for (int it = it_lo + gw; it < it_hi; it += 2 * NGW) {
;         const int it1 = it + NGW, it2 = it + 2 * NGW;
;         peer_row_load(vb, in, it1 < it_hi ? it1 : it, only_layer, lane);
.LBB0_618:
	v_mov_b32_e32 v1, v0
	s_nop 0
	v_readfirstlane_b32 s0, v1
	s_ashr_i32 s16, s0, 6
	s_lshl_b32 s0, s35, 3
	s_add_i32 s4, s16, s0
	v_and_b32_e32 v134, 63, v1
	s_cmpk_gt_i32 s4, 0x1fff
	v_lshlrev_b32_e32 v136, 2, v134
	v_cmp_eq_u32_e64 s[0:1], 0, v134
	s_cbranch_scc1 .LBB0_627
	s_ashr_i32 s5, s4, 31
	s_lshl_b64 s[6:7], s[4:5], 14
	s_add_u32 s6, s84, s6
	s_addc_u32 s7, s85, s7
	v_mov_b32_e32 v131, 0
	v_lshlrev_b32_e32 v130, 4, v134
	v_lshl_add_u64 v[2:3], s[6:7], 0, v[130:131]
	v_add_co_u32_e32 v4, vcc, 0x1000, v2
	global_load_dwordx4 v[86:89], v130, s[6:7]
	global_load_dwordx4 v[62:65], v130, s[6:7] offset:1024
	global_load_dwordx4 v[50:53], v130, s[6:7] offset:2048
	global_load_dwordx4 v[54:57], v130, s[6:7] offset:3072
	v_addc_co_u32_e32 v5, vcc, 0, v3, vcc
	global_load_dwordx4 v[46:49], v[4:5], off
	global_load_dwordx4 v[42:45], v[4:5], off offset:1024
	global_load_dwordx4 v[38:41], v[4:5], off offset:2048
	global_load_dwordx4 v[34:37], v[4:5], off offset:3072
	v_add_co_u32_e32 v4, vcc, 0x2000, v2
	v_mov_b32_e32 v137, v131
	s_nop 0
	v_addc_co_u32_e32 v5, vcc, 0, v3, vcc
	v_add_co_u32_e32 v2, vcc, 0x3000, v2
	global_load_dwordx4 v[30:33], v[4:5], off
	global_load_dwordx4 v[26:29], v[4:5], off offset:1024
	global_load_dwordx4 v[22:25], v[4:5], off offset:2048
	global_load_dwordx4 v[14:17], v[4:5], off offset:3072
	v_addc_co_u32_e32 v3, vcc, 0, v3, vcc
	global_load_dwordx4 v[18:21], v[2:3], off
	global_load_dwordx4 v[10:13], v[2:3], off offset:1024
	global_load_dwordx4 v[6:9], v[2:3], off offset:2048
	s_nop 0
	global_load_dwordx4 v[2:5], v[2:3], off offset:3072
	v_lshl_add_u64 v[58:59], s[90:91], 0, v[136:137]
	s_mov_b64 s[6:7], 0xba00000
	s_add_u32 s17, s90, 0x1ba00000
	v_lshl_add_u64 v[132:133], v[58:59], 0, s[6:7]
	s_addc_u32 s18, s91, 0
	s_lshl_b32 s6, s2, 3
	s_lshl_b32 s29, s34, 4
	s_lshl_b32 s30, s34, 3
	s_movk_i32 s5, 0x1000
	s_movk_i32 s14, 0x2000
	s_movk_i32 s15, 0x3000
	s_add_i32 s19, s16, s6
	s_add_i32 s28, s29, 0xfffff800
	s_addk_i32 s29, 0xf400
	s_addk_i32 s30, 0xf800
	s_mov_b32 s31, 0x43800000
	s_branch .LBB0_622

; __device__ __forceinline__ void peer_row_load(f32x4 (&v)[16], const float* const (&in)[34], int it, int layer, int lane) {
;     const int tbl = it >= NEXP, r = it - tbl * NEXP + layer * NEXP;
;     const f32x4* src = (const f32x4*)((tbl ? in[33] : in[32]) + (size_t)r * D) + lane;
; #pragma unroll
;     for (int j = 0; j < 16; ++j) v[j] = src[64 * j];
; }
; __device__ __forceinline__ void peer_row_store(const f32x4 (&v)[16], unsigned char* ws, int it, int layer, int lane) {
;     const int tbl = it >= NEXP, r = it - tbl * NEXP + layer * NEXP;
;     float am = 0.f;
; #pragma unroll
;     for (int j = 0; j < 16; ++j) am = fmaxf(fmaxf(am, fmaxf(fabsf(v[j][0]), fabsf(v[j][1]))), fmaxf(fabsf(v[j][2]), fabsf(v[j][3])));
;     am = __uint_as_float(max64u(__float_as_uint(am)));
;     ...
;     for (int it = it_lo + gw; it < it_hi; it += 2 * NGW) {
;         const int it1 = it + NGW, it2 = it + 2 * NGW;
;         peer_row_load(vb, in, it1 < it_hi ? it1 : it, only_layer, lane);
.LBB0_621:
	s_add_i32 s19, s19, s28
	s_add_i32 s6, s19, 0xfffffc00
	s_cmpk_lt_i32 s6, 0x2000
	s_cbranch_scc0 .LBB0_627
.LBB0_622:
	s_add_i32 s10, s19, 0xfffffc00
	s_add_i32 s6, s30, s19
	s_cmpk_lt_i32 s6, 0x2000
	s_cselect_b64 s[8:9], -1, 0
	s_and_b64 s[12:13], s[8:9], exec
	s_cselect_b32 s7, s6, s10
	s_cmpk_gt_i32 s7, 0x3fff
	s_cselect_b32 s11, 0xffffc000, 0
	s_cselect_b32 s20, s86, s84
	s_cselect_b32 s21, s87, s85
	s_add_i32 s12, s11, s7
	s_ashr_i32 s13, s12, 31
	s_lshl_b64 s[12:13], s[12:13], 14
	s_add_u32 s12, s20, s12
	s_addc_u32 s13, s21, s13
	v_lshlrev_b32_e32 v130, 4, v134
	s_waitcnt vmcnt(32)
	v_lshl_add_u64 v[58:59], s[12:13], 0, v[130:131]
	v_add_co_u32_e32 v60, vcc, s5, v58
	global_load_dwordx4 v[122:125], v130, s[12:13] offset:1024
	global_load_dwordx4 v[118:121], v130, s[12:13] offset:2048
	v_addc_co_u32_e32 v61, vcc, 0, v59, vcc
	v_add_co_u32_e32 v66, vcc, s14, v58
	s_nop 1
	v_addc_co_u32_e32 v67, vcc, 0, v59, vcc
	global_load_dwordx4 v[114:117], v130, s[12:13] offset:3072
	global_load_dwordx4 v[110:113], v[66:67], off offset:-4096
	global_load_dwordx4 v[106:109], v[60:61], off offset:1024
	global_load_dwordx4 v[102:105], v[60:61], off offset:2048
	global_load_dwordx4 v[94:97], v[66:67], off
	global_load_dwordx4 v[90:93], v[66:67], off offset:1024
	global_load_dwordx4 v[82:85], v[66:67], off offset:2048
	global_load_dwordx4 v[78:81], v[66:67], off offset:3072
	v_add_co_u32_e32 v58, vcc, s15, v58
	s_nop 1
	v_addc_co_u32_e32 v59, vcc, 0, v59, vcc
	global_load_dwordx4 v[98:101], v[60:61], off offset:3072
	global_load_dwordx4 v[74:77], v[58:59], off
	global_load_dwordx4 v[70:73], v[58:59], off offset:1024
	global_load_dwordx4 v[66:69], v[58:59], off offset:2048
	global_load_dwordx4 v[126:129], v130, s[12:13]
	s_nop 0
	global_load_dwordx4 v[58:61], v[58:59], off offset:3072
	s_waitcnt vmcnt(17)
	v_max_f32_e64 v135, |v87|, |v87|
	v_max_f32_e64 v137, |v86|, |v86|
	v_max_f32_e32 v135, v137, v135
	v_max_f32_e64 v137, |v89|, |v89|
	v_max_f32_e64 v138, |v88|, |v88|
	v_max_f32_e32 v137, v138, v137
	v_max3_f32 v135, v135, 0, v137
	s_waitcnt vmcnt(30)
	v_max_f32_e64 v137, |v63|, |v63|
	v_max_f32_e64 v138, |v62|, |v62|
	v_max_f32_e32 v137, v138, v137
	v_max_f32_e64 v138, |v65|, |v65|
	v_max_f32_e64 v139, |v64|, |v64|
	v_max_f32_e32 v138, v139, v138
	v_max3_f32 v135, v135, v137, v138
	s_waitcnt vmcnt(29)
	v_max_f32_e64 v137, |v51|, |v51|
	v_max_f32_e64 v138, |v50|, |v50|
	v_max_f32_e32 v137, v138, v137
	v_max_f32_e64 v138, |v53|, |v53|
	v_max_f32_e64 v139, |v52|, |v52|
	v_max_f32_e32 v138, v139, v138
	v_max3_f32 v135, v135, v137, v138
	s_waitcnt vmcnt(28)
	v_max_f32_e64 v137, |v55|, |v55|
	v_max_f32_e64 v138, |v54|, |v54|
	v_max_f32_e32 v137, v138, v137
	v_max_f32_e64 v138, |v57|, |v57|
	v_max_f32_e64 v139, |v56|, |v56|
	v_max_f32_e32 v138, v139, v138
	v_max3_f32 v135, v135, v137, v138
	s_waitcnt vmcnt(27)
	v_max_f32_e64 v137, |v47|, |v47|
	v_max_f32_e64 v138, |v46|, |v46|
	v_max_f32_e32 v137, v138, v137
	v_max_f32_e64 v138, |v49|, |v49|
	v_max_f32_e64 v139, |v48|, |v48|
	v_max_f32_e32 v138, v139, v138
	v_max3_f32 v135, v135, v137, v138
	s_waitcnt vmcnt(26)
	v_max_f32_e64 v137, |v43|, |v43|
	v_max_f32_e64 v138, |v42|, |v42|
	v_max_f32_e32 v137, v138, v137
	v_max_f32_e64 v138, |v45|, |v45|
	v_max_f32_e64 v139, |v44|, |v44|
	v_max_f32_e32 v138, v139, v138
	v_max3_f32 v135, v135, v137, v138
	s_waitcnt vmcnt(25)
	v_max_f32_e64 v137, |v39|, |v39|
	v_max_f32_e64 v138, |v38|, |v38|
	v_max_f32_e32 v137, v138, v137
	v_max_f32_e64 v138, |v41|, |v41|
	v_max_f32_e64 v139, |v40|, |v40|
	v_max_f32_e32 v138, v139, v138
	v_max3_f32 v135, v135, v137, v138
	s_waitcnt vmcnt(24)
	v_max_f32_e64 v137, |v35|, |v35|
	v_max_f32_e64 v138, |v34|, |v34|
	v_max_f32_e32 v137, v138, v137
	v_max_f32_e64 v138, |v37|, |v37|
	v_max_f32_e64 v139, |v36|, |v36|
	v_max_f32_e32 v138, v139, v138
	v_max3_f32 v135, v135, v137, v138
	s_waitcnt vmcnt(23)
	v_max_f32_e64 v137, |v31|, |v31|
	v_max_f32_e64 v138, |v30|, |v30|
	v_max_f32_e32 v137, v138, v137
	v_max_f32_e64 v138, |v33|, |v33|
	v_max_f32_e64 v139, |v32|, |v32|
	v_max_f32_e32 v138, v139, v138
	v_max3_f32 v135, v135, v137, v138
	s_waitcnt vmcnt(22)
	v_max_f32_e64 v137, |v27|, |v27|
	v_max_f32_e64 v138, |v26|, |v26|
	v_max_f32_e32 v137, v138, v137
	v_max_f32_e64 v138, |v29|, |v29|
	v_max_f32_e64 v139, |v28|, |v28|
	v_max_f32_e32 v138, v139, v138
	v_max3_f32 v135, v135, v137, v138
	s_waitcnt vmcnt(21)
	v_max_f32_e64 v137, |v23|, |v23|
	v_max_f32_e64 v138, |v22|, |v22|
	v_max_f32_e32 v137, v138, v137
	v_max_f32_e64 v138, |v25|, |v25|
	v_max_f32_e64 v139, |v24|, |v24|
	v_max_f32_e32 v138, v139, v138
	v_max3_f32 v135, v135, v137, v138
	s_waitcnt vmcnt(20)
	v_max_f32_e64 v137, |v15|, |v15|
	v_max_f32_e64 v138, |v14|, |v14|
	v_max_f32_e32 v137, v138, v137
	v_max_f32_e64 v138, |v17|, |v17|
	v_max_f32_e64 v139, |v16|, |v16|
	v_max_f32_e32 v138, v139, v138
	v_max3_f32 v135, v135, v137, v138
	s_waitcnt vmcnt(19)
	v_max_f32_e64 v137, |v19|, |v19|
	v_max_f32_e64 v138, |v18|, |v18|
	v_max_f32_e32 v137, v138, v137
	v_max_f32_e64 v138, |v21|, |v21|
	v_max_f32_e64 v139, |v20|, |v20|
	v_max_f32_e32 v138, v139, v138
	v_max3_f32 v135, v135, v137, v138
	s_waitcnt vmcnt(18)
	v_max_f32_e64 v137, |v11|, |v11|
	v_max_f32_e64 v138, |v10|, |v10|
	v_max_f32_e32 v137, v138, v137
	v_max_f32_e64 v138, |v13|, |v13|
	v_max_f32_e64 v139, |v12|, |v12|
	v_max_f32_e32 v138, v139, v138
	v_max3_f32 v135, v135, v137, v138
	s_waitcnt vmcnt(17)
	v_max_f32_e64 v137, |v7|, |v7|
	v_max_f32_e64 v138, |v6|, |v6|
	v_max_f32_e32 v137, v138, v137
	v_max_f32_e64 v138, |v9|, |v9|
	v_max_f32_e64 v139, |v8|, |v8|
	v_max_f32_e32 v138, v139, v138
	v_max3_f32 v135, v135, v137, v138
	s_waitcnt vmcnt(16)
; __device__ __forceinline__ void peer_row_store(const f32x4 (&v)[16], unsigned char* ws, int it, int layer, int lane) {
;     ...
; #pragma unroll
;     for (int j = 0; j < 16; ++j) am = fmaxf(fmaxf(am, fmaxf(fabsf(v[j][0]), fabsf(v[j][1]))), fmaxf(fabsf(v[j][2]), fabsf(v[j][3])));
;     am = __uint_as_float(max64u(__float_as_uint(am)));
;     const float q = am > 0.f ? 256.0f / am : 0.f;
;     unsigned* dst = (unsigned*)(ws + (tbl ? WS_PV : WS_PU) + (size_t)r * D) + lane;
;     if (tbl) {
;         const int rl = it - NEXP;
;         unsigned char* pvl = ws + WS_PV + (size_t)layer * NEXP * D + (size_t)rl * 8 + (lane & 1) * 4;
;         unsigned char* pvg = ws + WS_PV + (size_t)layer * NEXP * D + (size_t)NEXP * 2048 + (size_t)rl * 2048 + 4 * lane;
; #pragma unroll
;         for (int j = 0; j < 16; ++j) { int w = __builtin_amdgcn_cvt_pk_bf8_f32(v[j][0] * q, v[j][1] * q, 0, false); w = __builtin_amdgcn_cvt_pk_bf8_f32(v[j][2] * q, v[j][3] * q, w, true);
;             if (j < 8) *(unsigned*)(pvl + (size_t)((lane >> 1) + 32 * j) * (NEXP * 8)) = (unsigned)w;
;             else *(unsigned*)(pvg + 256 * (j - 8)) = (unsigned)w; }
;     } else {
; #pragma unroll
;         for (int j = 0; j < 16; ++j) { int w = __builtin_amdgcn_cvt_pk_fp8_f32(v[j][0] * q, v[j][1] * q, 0, false); w = __builtin_amdgcn_cvt_pk_fp8_f32(v[j][2] * q, v[j][3] * q, w, true); dst[64 * j] = (unsigned)w; }
;     }
;     if (lane == 0) ((float*)(ws + (tbl ? WS_SV : WS_SU)))[r] = am * (1.0f / 256.0f);
	v_max_f32_e64 v137, |v3|, |v3|
	v_max_f32_e64 v138, |v2|, |v2|
	v_max_f32_e32 v137, v138, v137
	v_max_f32_e64 v138, |v5|, |v5|
	v_max_f32_e64 v139, |v4|, |v4|
	v_max_f32_e32 v138, v139, v138
	v_max3_f32 v135, v135, v137, v138
	s_ashr_i32 s11, s10, 31
	s_nop 0
	v_max_u32_dpp v135, v135, v135 quad_perm:[1,0,3,2] row_mask:0xf bank_mask:0xf bound_ctrl:1
	s_nop 1
	v_max_u32_dpp v135, v135, v135 quad_perm:[2,3,0,1] row_mask:0xf bank_mask:0xf bound_ctrl:1
	s_nop 1
	v_max_u32_dpp v135, v135, v135 row_half_mirror row_mask:0xf bank_mask:0xf bound_ctrl:1
	s_nop 1
	v_max_u32_dpp v135, v135, v135 row_mirror row_mask:0xf bank_mask:0xf bound_ctrl:1
	v_mov_b32_e32 v137, v135
	s_nop 1
	v_permlane16_swap_b32_e32 v135, v137
	v_max_u32_e32 v135, v135, v137
	v_mov_b32_e32 v137, v135
	s_nop 1
	v_permlane32_swap_b32_e32 v135, v137
	v_max_u32_e32 v135, v135, v137
	v_div_scale_f32 v137, s[12:13], v135, v135, s31
	v_rcp_f32_e32 v138, v137
	s_lshl_b64 s[12:13], s[10:11], 12
	v_fma_f32 v139, -v137, v138, 1.0
	v_fmac_f32_e32 v138, v139, v138
	v_div_scale_f32 v139, vcc, s31, v135, s31
	v_mul_f32_e32 v140, v139, v138
	v_fma_f32 v141, -v137, v140, v139
	v_fmac_f32_e32 v140, v141, v138
	v_fma_f32 v137, -v137, v140, v139
	v_div_fmas_f32 v137, v137, v138, v140
	v_div_fixup_f32 v137, v137, v135, s31
	v_cmp_lt_f32_e32 vcc, 0, v135
	v_mov_b32_e32 v140, v131
	v_lshl_add_u64 v[138:139], v[132:133], 0, s[12:13]
	v_cndmask_b32_e32 v137, 0, v137, vcc
	v_mul_f32_e32 v86, v86, v137
	v_mul_f32_e32 v87, v87, v137
	v_cvt_pk_fp8_f32 v140, v86, v87
	v_mul_f32_e32 v86, v88, v137
	v_mul_f32_e32 v62, v62, v137
	v_mul_f32_e32 v63, v63, v137
	v_mov_b32_e32 v88, v131
	v_cvt_pk_fp8_f32 v88, v62, v63
	v_mul_f32_e32 v62, v64, v137
	v_mul_f32_e32 v63, v65, v137
	v_mul_f32_e32 v50, v50, v137
	v_cvt_pk_fp8_f32 v88, v62, v63 op_sel:[0,0,1]
	v_mul_f32_e32 v51, v51, v137
	v_mov_b32_e32 v62, v131
	v_cvt_pk_fp8_f32 v62, v50, v51
	v_mul_f32_e32 v50, v52, v137
	v_mul_f32_e32 v51, v53, v137
	v_mul_f32_e32 v52, v54, v137
	v_mul_f32_e32 v53, v55, v137
	v_mov_b32_e32 v54, v131
	v_cvt_pk_fp8_f32 v54, v52, v53
	v_cvt_pk_fp8_f32 v62, v50, v51 op_sel:[0,0,1]
	v_mul_f32_e32 v50, v56, v137
	v_mul_f32_e32 v51, v57, v137
	v_cvt_pk_fp8_f32 v54, v50, v51 op_sel:[0,0,1]
	v_mul_f32_e32 v46, v46, v137
	v_mul_f32_e32 v47, v47, v137
	v_mov_b32_e32 v50, v131
	v_cvt_pk_fp8_f32 v50, v46, v47
	v_mul_f32_e32 v46, v48, v137
	v_mul_f32_e32 v42, v42, v137
	v_mul_f32_e32 v43, v43, v137
	v_mov_b32_e32 v48, v131
	v_cvt_pk_fp8_f32 v48, v42, v43
	v_mul_f32_e32 v42, v44, v137
	v_mul_f32_e32 v43, v45, v137
	v_mul_f32_e32 v38, v38, v137
	v_cvt_pk_fp8_f32 v48, v42, v43 op_sel:[0,0,1]
	v_mul_f32_e32 v39, v39, v137
	v_mov_b32_e32 v42, v131
	v_cvt_pk_fp8_f32 v42, v38, v39
	v_mul_f32_e32 v38, v40, v137
	v_mul_f32_e32 v34, v34, v137
	v_mul_f32_e32 v35, v35, v137
	v_mov_b32_e32 v40, v131
	v_cvt_pk_fp8_f32 v40, v34, v35
	v_mul_f32_e32 v34, v36, v137
	v_mul_f32_e32 v35, v37, v137
	v_mul_f32_e32 v30, v30, v137
	v_cvt_pk_fp8_f32 v40, v34, v35 op_sel:[0,0,1]
	v_mul_f32_e32 v31, v31, v137
	v_mov_b32_e32 v34, v131
	v_cvt_pk_fp8_f32 v34, v30, v31
	v_mul_f32_e32 v30, v32, v137
	v_mul_f32_e32 v26, v26, v137
	v_mul_f32_e32 v27, v27, v137
	v_mov_b32_e32 v32, v131
	v_cvt_pk_fp8_f32 v32, v26, v27
	v_mul_f32_e32 v26, v28, v137
	v_mul_f32_e32 v27, v29, v137
	v_mul_f32_e32 v22, v22, v137
	v_cvt_pk_fp8_f32 v32, v26, v27 op_sel:[0,0,1]
	v_mul_f32_e32 v23, v23, v137
	v_mov_b32_e32 v26, v131
	v_cvt_pk_fp8_f32 v26, v22, v23
	v_mul_f32_e32 v22, v24, v137
	v_mul_f32_e32 v14, v14, v137
	v_mul_f32_e32 v15, v15, v137
	v_mov_b32_e32 v24, v131
	v_cvt_pk_fp8_f32 v24, v14, v15
	v_mul_f32_e32 v15, v17, v137
	v_mul_f32_e32 v10, v10, v137
	v_mul_f32_e32 v11, v11, v137
	v_mov_b32_e32 v17, v131
	v_cvt_pk_fp8_f32 v17, v10, v11
	v_mul_f32_e32 v14, v16, v137
	v_cvt_pk_fp8_f32 v24, v14, v15 op_sel:[0,0,1]
	v_mul_f32_e32 v14, v18, v137
	v_mul_f32_e32 v15, v19, v137
	v_mov_b32_e32 v16, v131
	v_cvt_pk_fp8_f32 v16, v14, v15
	v_mul_f32_e32 v10, v12, v137
	v_mul_f32_e32 v11, v13, v137
	v_cvt_pk_fp8_f32 v17, v10, v11 op_sel:[0,0,1]
	v_mul_f32_e32 v6, v6, v137
	v_mul_f32_e32 v7, v7, v137
	v_mov_b32_e32 v10, v131
	v_cvt_pk_fp8_f32 v10, v6, v7
	v_mul_f32_e32 v6, v8, v137
	v_mul_f32_e32 v2, v2, v137
	v_mul_f32_e32 v3, v3, v137
	v_mov_b32_e32 v8, v131
	v_mul_f32_e32 v87, v89, v137
	v_mul_f32_e32 v47, v49, v137
	v_mul_f32_e32 v31, v33, v137
	v_mul_f32_e32 v14, v20, v137
	v_mul_f32_e32 v15, v21, v137
	v_cvt_pk_fp8_f32 v8, v2, v3
	v_cvt_pk_fp8_f32 v140, v86, v87 op_sel:[0,0,1]
	v_cvt_pk_fp8_f32 v50, v46, v47 op_sel:[0,0,1]
	v_cvt_pk_fp8_f32 v34, v30, v31 op_sel:[0,0,1]
	v_cvt_pk_fp8_f32 v16, v14, v15 op_sel:[0,0,1]
	v_mul_f32_e32 v39, v41, v137
	v_mul_f32_e32 v23, v25, v137
	v_mul_f32_e32 v7, v9, v137
	v_cvt_pk_fp8_f32 v42, v38, v39 op_sel:[0,0,1]
	v_cvt_pk_fp8_f32 v26, v22, v23 op_sel:[0,0,1]
	v_cvt_pk_fp8_f32 v10, v6, v7 op_sel:[0,0,1]
	v_mul_f32_e32 v2, v4, v137
	v_mul_f32_e32 v3, v5, v137
	v_cvt_pk_fp8_f32 v8, v2, v3 op_sel:[0,0,1]
	global_store_dword v[138:139], v140, off
	global_store_dword v[138:139], v88, off offset:256
	global_store_dword v[138:139], v62, off offset:512
	global_store_dword v[138:139], v54, off offset:768
	global_store_dword v[138:139], v50, off offset:1024
	global_store_dword v[138:139], v48, off offset:1280
	global_store_dword v[138:139], v42, off offset:1536
	global_store_dword v[138:139], v40, off offset:1792
	global_store_dword v[138:139], v34, off offset:2048
	global_store_dword v[138:139], v32, off offset:2304
	global_store_dword v[138:139], v26, off offset:2560
	global_store_dword v[138:139], v24, off offset:2816
	global_store_dword v[138:139], v16, off offset:3072
	global_store_dword v[138:139], v17, off offset:3328
	global_store_dword v[138:139], v10, off offset:3584
	global_store_dword v[138:139], v8, off offset:3840
	s_and_saveexec_b64 s[12:13], s[0:1]
	s_cbranch_execz .LBB0_624
	s_lshl_b64 s[20:21], s[10:11], 2
	s_add_u32 s20, s17, s20
	s_addc_u32 s21, s18, s21
	v_mul_f32_e32 v2, 0x3b800000, v135
	global_store_dword v131, v2, s[20:21]
; __device__ __forceinline__ void peer_row_load(f32x4 (&v)[16], const float* const (&in)[34], int it, int layer, int lane) {
;     const int tbl = it >= NEXP, r = it - tbl * NEXP + layer * NEXP;
;     const f32x4* src = (const f32x4*)((tbl ? in[33] : in[32]) + (size_t)r * D) + lane;
; #pragma unroll
;     for (int j = 0; j < 16; ++j) v[j] = src[64 * j];
; }
; __device__ __forceinline__ void peer_row_store(const f32x4 (&v)[16], unsigned char* ws, int it, int layer, int lane) {
;     const int tbl = it >= NEXP, r = it - tbl * NEXP + layer * NEXP;
;     float am = 0.f;
; #pragma unroll
;     for (int j = 0; j < 16; ++j) am = fmaxf(fmaxf(am, fmaxf(fabsf(v[j][0]), fabsf(v[j][1]))), fmaxf(fabsf(v[j][2]), fabsf(v[j][3])));
;     am = __uint_as_float(max64u(__float_as_uint(am)));
;     ...
;         peer_row_load(va, in, it2 < it_hi ? it2 : it, only_layer, lane);
;         __builtin_amdgcn_sched_barrier(0);
;         if (it1 < it_hi) peer_row_store(vb, ws, it1, only_layer, lane);
.LBB0_624:
	s_or_b64 exec, exec, s[12:13]
	s_add_i32 s7, s29, s19
	s_cmpk_lt_i32 s7, 0x2000
	s_cselect_b32 s7, s7, s10
	s_cmpk_gt_i32 s7, 0x3fff
	s_cselect_b64 s[10:11], -1, 0
	s_and_b64 s[12:13], s[10:11], exec
	s_cselect_b32 s12, 0xffffc000, 0
	s_add_i32 s12, s12, s7
	s_and_b64 s[10:11], s[10:11], exec
	s_cselect_b32 s7, s87, s85
	s_cselect_b32 s20, s86, s84
	s_ashr_i32 s13, s12, 31
	s_lshl_b64 s[10:11], s[12:13], 14
	s_add_u32 s10, s20, s10
	s_addc_u32 s11, s7, s11
	v_lshl_add_u64 v[2:3], s[10:11], 0, v[130:131]
	v_add_co_u32_e32 v4, vcc, s5, v2
	global_load_dwordx4 v[62:65], v130, s[10:11] offset:1024
	global_load_dwordx4 v[50:53], v130, s[10:11] offset:2048
	v_addc_co_u32_e32 v5, vcc, 0, v3, vcc
	v_add_co_u32_e32 v6, vcc, s14, v2
	s_nop 1
	v_addc_co_u32_e32 v7, vcc, 0, v3, vcc
	global_load_dwordx4 v[54:57], v130, s[10:11] offset:3072
	global_load_dwordx4 v[46:49], v[6:7], off offset:-4096
	global_load_dwordx4 v[42:45], v[4:5], off offset:1024
	global_load_dwordx4 v[38:41], v[4:5], off offset:2048
	global_load_dwordx4 v[30:33], v[6:7], off
	global_load_dwordx4 v[26:29], v[6:7], off offset:1024
	global_load_dwordx4 v[22:25], v[6:7], off offset:2048
	global_load_dwordx4 v[14:17], v[6:7], off offset:3072
	v_add_co_u32_e32 v2, vcc, 0x3000, v2
	s_nop 1
	v_addc_co_u32_e32 v3, vcc, 0, v3, vcc
	global_load_dwordx4 v[34:37], v[4:5], off offset:3072
	global_load_dwordx4 v[18:21], v[2:3], off
	global_load_dwordx4 v[10:13], v[2:3], off offset:1024
	global_load_dwordx4 v[6:9], v[2:3], off offset:2048
	global_load_dwordx4 v[86:89], v130, s[10:11]
	s_nop 0
	global_load_dwordx4 v[2:5], v[2:3], off offset:3072
	s_andn2_b64 vcc, exec, s[8:9]
	s_cbranch_vccnz .LBB0_621
	s_waitcnt vmcnt(33)
	v_max_f32_e64 v130, |v127|, |v127|
	v_max_f32_e64 v135, |v126|, |v126|
	v_max_f32_e32 v130, v135, v130
	v_max_f32_e64 v135, |v129|, |v129|
	v_max_f32_e64 v137, |v128|, |v128|
	v_max_f32_e32 v135, v137, v135
	v_max3_f32 v130, v130, 0, v135
	v_max_f32_e64 v135, |v123|, |v123|
	v_max_f32_e64 v137, |v122|, |v122|
	v_max_f32_e32 v135, v137, v135
	v_max_f32_e64 v137, |v125|, |v125|
	v_max_f32_e64 v138, |v124|, |v124|
	v_max_f32_e32 v137, v138, v137
	v_max3_f32 v130, v130, v135, v137
	v_max_f32_e64 v135, |v119|, |v119|
	v_max_f32_e64 v137, |v118|, |v118|
	v_max_f32_e32 v135, v137, v135
	v_max_f32_e64 v137, |v121|, |v121|
	v_max_f32_e64 v138, |v120|, |v120|
	v_max_f32_e32 v137, v138, v137
	v_max3_f32 v130, v130, v135, v137
	v_max_f32_e64 v135, |v115|, |v115|
	v_max_f32_e64 v137, |v114|, |v114|
	v_max_f32_e32 v135, v137, v135
	v_max_f32_e64 v137, |v117|, |v117|
	v_max_f32_e64 v138, |v116|, |v116|
	v_max_f32_e32 v137, v138, v137
	v_max3_f32 v130, v130, v135, v137
	v_max_f32_e64 v135, |v111|, |v111|
	v_max_f32_e64 v137, |v110|, |v110|
	v_max_f32_e32 v135, v137, v135
	v_max_f32_e64 v137, |v113|, |v113|
	v_max_f32_e64 v138, |v112|, |v112|
	v_max_f32_e32 v137, v138, v137
	v_max3_f32 v130, v130, v135, v137
	v_max_f32_e64 v135, |v107|, |v107|
	v_max_f32_e64 v137, |v106|, |v106|
	v_max_f32_e32 v135, v137, v135
	v_max_f32_e64 v137, |v109|, |v109|
	v_max_f32_e64 v138, |v108|, |v108|
	v_max_f32_e32 v137, v138, v137
	v_max3_f32 v130, v130, v135, v137
	v_max_f32_e64 v135, |v103|, |v103|
	v_max_f32_e64 v137, |v102|, |v102|
	v_max_f32_e32 v135, v137, v135
	v_max_f32_e64 v137, |v105|, |v105|
	v_max_f32_e64 v138, |v104|, |v104|
	v_max_f32_e32 v137, v138, v137
	v_max3_f32 v130, v130, v135, v137
	v_max_f32_e64 v135, |v99|, |v99|
	v_max_f32_e64 v137, |v98|, |v98|
	v_max_f32_e32 v135, v137, v135
	v_max_f32_e64 v137, |v101|, |v101|
	v_max_f32_e64 v138, |v100|, |v100|
	v_max_f32_e32 v137, v138, v137
	v_max3_f32 v130, v130, v135, v137
	v_max_f32_e64 v135, |v95|, |v95|
	v_max_f32_e64 v137, |v94|, |v94|
	v_max_f32_e32 v135, v137, v135
	v_max_f32_e64 v137, |v97|, |v97|
	v_max_f32_e64 v138, |v96|, |v96|
	v_max_f32_e32 v137, v138, v137
	v_max3_f32 v130, v130, v135, v137
	v_max_f32_e64 v135, |v91|, |v91|
	v_max_f32_e64 v137, |v90|, |v90|
	v_max_f32_e32 v135, v137, v135
	v_max_f32_e64 v137, |v93|, |v93|
	v_max_f32_e64 v138, |v92|, |v92|
	v_max_f32_e32 v137, v138, v137
	v_max3_f32 v130, v130, v135, v137
	v_max_f32_e64 v135, |v83|, |v83|
	v_max_f32_e64 v137, |v82|, |v82|
	v_max_f32_e32 v135, v137, v135
	v_max_f32_e64 v137, |v85|, |v85|
	v_max_f32_e64 v138, |v84|, |v84|
	v_max_f32_e32 v137, v138, v137
	v_max3_f32 v130, v130, v135, v137
	v_max_f32_e64 v135, |v79|, |v79|
	v_max_f32_e64 v137, |v78|, |v78|
	v_max_f32_e32 v135, v137, v135
	v_max_f32_e64 v137, |v81|, |v81|
	v_max_f32_e64 v138, |v80|, |v80|
	v_max_f32_e32 v137, v138, v137
	v_max3_f32 v130, v130, v135, v137
	v_max_f32_e64 v135, |v75|, |v75|
	v_max_f32_e64 v137, |v74|, |v74|
	v_max_f32_e32 v135, v137, v135
	v_max_f32_e64 v137, |v77|, |v77|
	v_max_f32_e64 v138, |v76|, |v76|
	v_max_f32_e32 v137, v138, v137
	v_max3_f32 v130, v130, v135, v137
	v_max_f32_e64 v135, |v71|, |v71|
	v_max_f32_e64 v137, |v70|, |v70|
	v_max_f32_e32 v135, v137, v135
	v_max_f32_e64 v137, |v73|, |v73|
	v_max_f32_e64 v138, |v72|, |v72|
	v_max_f32_e32 v137, v138, v137
	v_max3_f32 v130, v130, v135, v137
	v_max_f32_e64 v135, |v67|, |v67|
	v_max_f32_e64 v137, |v66|, |v66|
	v_max_f32_e32 v135, v137, v135
	v_max_f32_e64 v137, |v69|, |v69|
	v_max_f32_e64 v138, |v68|, |v68|
	v_max_f32_e32 v137, v138, v137
	v_max3_f32 v130, v130, v135, v137
	s_waitcnt vmcnt(32)
; __device__ __forceinline__ void peer_row_store(const f32x4 (&v)[16], unsigned char* ws, int it, int layer, int lane) {
;     const int tbl = it >= NEXP, r = it - tbl * NEXP + layer * NEXP;
;     float am = 0.f;
; #pragma unroll
;     for (int j = 0; j < 16; ++j) am = fmaxf(fmaxf(am, fmaxf(fabsf(v[j][0]), fabsf(v[j][1]))), fmaxf(fabsf(v[j][2]), fabsf(v[j][3])));
;     am = __uint_as_float(max64u(__float_as_uint(am)));
;     const float q = am > 0.f ? 256.0f / am : 0.f;
;     unsigned* dst = (unsigned*)(ws + (tbl ? WS_PV : WS_PU) + (size_t)r * D) + lane;
;     if (tbl) {
;         const int rl = it - NEXP;
;         unsigned char* pvl = ws + WS_PV + (size_t)layer * NEXP * D + (size_t)rl * 8 + (lane & 1) * 4;
;         unsigned char* pvg = ws + WS_PV + (size_t)layer * NEXP * D + (size_t)NEXP * 2048 + (size_t)rl * 2048 + 4 * lane;
; #pragma unroll
;         for (int j = 0; j < 16; ++j) { int w = __builtin_amdgcn_cvt_pk_bf8_f32(v[j][0] * q, v[j][1] * q, 0, false); w = __builtin_amdgcn_cvt_pk_bf8_f32(v[j][2] * q, v[j][3] * q, w, true);
;             if (j < 8) *(unsigned*)(pvl + (size_t)((lane >> 1) + 32 * j) * (NEXP * 8)) = (unsigned)w;
;             else *(unsigned*)(pvg + 256 * (j - 8)) = (unsigned)w; }
;     } else {
; #pragma unroll
;         for (int j = 0; j < 16; ++j) { int w = __builtin_amdgcn_cvt_pk_fp8_f32(v[j][0] * q, v[j][1] * q, 0, false); w = __builtin_amdgcn_cvt_pk_fp8_f32(v[j][2] * q, v[j][3] * q, w, true); dst[64 * j] = (unsigned)w; }
;     }
;     if (lane == 0) ((float*)(ws + (tbl ? WS_SV : WS_SU)))[r] = am * (1.0f / 256.0f);
	v_max_f32_e64 v135, |v59|, |v59|
	v_max_f32_e64 v137, |v58|, |v58|
	v_max_f32_e32 v135, v137, v135
	v_max_f32_e64 v137, |v61|, |v61|
	v_max_f32_e64 v138, |v60|, |v60|
	v_max_f32_e32 v137, v138, v137
	v_max3_f32 v130, v130, v135, v137
	s_ashr_i32 s7, s6, 31
	s_nop 0
	v_max_u32_dpp v130, v130, v130 quad_perm:[1,0,3,2] row_mask:0xf bank_mask:0xf bound_ctrl:1
	s_nop 1
	v_max_u32_dpp v130, v130, v130 quad_perm:[2,3,0,1] row_mask:0xf bank_mask:0xf bound_ctrl:1
	s_nop 1
	v_max_u32_dpp v130, v130, v130 row_half_mirror row_mask:0xf bank_mask:0xf bound_ctrl:1
	s_nop 1
	v_max_u32_dpp v130, v130, v130 row_mirror row_mask:0xf bank_mask:0xf bound_ctrl:1
	v_mov_b32_e32 v135, v130
	s_nop 1
	v_permlane16_swap_b32_e32 v130, v135
	v_max_u32_e32 v130, v130, v135
	v_mov_b32_e32 v135, v130
	s_nop 1
	v_permlane32_swap_b32_e32 v130, v135
	v_max_u32_e32 v130, v130, v135
	v_div_scale_f32 v135, s[8:9], v130, v130, s31
	v_rcp_f32_e32 v137, v135
	s_lshl_b64 s[8:9], s[6:7], 12
	v_fma_f32 v138, -v135, v137, 1.0
	v_fmac_f32_e32 v137, v138, v137
	v_div_scale_f32 v138, vcc, s31, v130, s31
	v_mul_f32_e32 v139, v138, v137
	v_fma_f32 v140, -v135, v139, v138
	v_fmac_f32_e32 v139, v140, v137
	v_fma_f32 v135, -v135, v139, v138
	v_div_fmas_f32 v135, v135, v137, v139
	v_div_fixup_f32 v135, v135, v130, s31
	v_cmp_lt_f32_e32 vcc, 0, v130
	v_mov_b32_e32 v137, v131
	v_lshl_add_u64 v[138:139], v[132:133], 0, s[8:9]
	v_cndmask_b32_e32 v135, 0, v135, vcc
	v_mul_f32_e32 v126, v126, v135
	v_mul_f32_e32 v127, v127, v135
	v_cvt_pk_fp8_f32 v137, v126, v127
	v_mul_f32_e32 v126, v128, v135
	v_mul_f32_e32 v122, v122, v135
	v_mul_f32_e32 v123, v123, v135
	v_mov_b32_e32 v128, v131
	v_cvt_pk_fp8_f32 v128, v122, v123
	v_mul_f32_e32 v122, v124, v135
	v_mul_f32_e32 v123, v125, v135
	v_mul_f32_e32 v118, v118, v135
	v_cvt_pk_fp8_f32 v128, v122, v123 op_sel:[0,0,1]
	v_mul_f32_e32 v119, v119, v135
	v_mov_b32_e32 v122, v131
	v_cvt_pk_fp8_f32 v122, v118, v119
	v_mul_f32_e32 v118, v120, v135
	v_mul_f32_e32 v114, v114, v135
	v_mul_f32_e32 v115, v115, v135
	v_mov_b32_e32 v120, v131
	v_cvt_pk_fp8_f32 v120, v114, v115
	v_mul_f32_e32 v114, v116, v135
	v_mul_f32_e32 v115, v117, v135
	v_mul_f32_e32 v110, v110, v135
	v_cvt_pk_fp8_f32 v120, v114, v115 op_sel:[0,0,1]
	v_mul_f32_e32 v111, v111, v135
	v_mov_b32_e32 v114, v131
	v_cvt_pk_fp8_f32 v114, v110, v111
	v_mul_f32_e32 v110, v112, v135
	v_mul_f32_e32 v106, v106, v135
	v_mul_f32_e32 v107, v107, v135
	v_mov_b32_e32 v112, v131
	v_cvt_pk_fp8_f32 v112, v106, v107
	v_mul_f32_e32 v106, v108, v135
	v_mul_f32_e32 v107, v109, v135
	v_mul_f32_e32 v102, v102, v135
	v_cvt_pk_fp8_f32 v112, v106, v107 op_sel:[0,0,1]
	v_mul_f32_e32 v103, v103, v135
	v_mov_b32_e32 v106, v131
	v_cvt_pk_fp8_f32 v106, v102, v103
	v_mul_f32_e32 v102, v104, v135
	v_mul_f32_e32 v98, v98, v135
	v_mul_f32_e32 v99, v99, v135
	v_mov_b32_e32 v104, v131
	v_cvt_pk_fp8_f32 v104, v98, v99
	v_mul_f32_e32 v98, v100, v135
	v_mul_f32_e32 v99, v101, v135
	v_mul_f32_e32 v94, v94, v135
	v_cvt_pk_fp8_f32 v104, v98, v99 op_sel:[0,0,1]
	v_mul_f32_e32 v95, v95, v135
	v_mov_b32_e32 v98, v131
	v_cvt_pk_fp8_f32 v98, v94, v95
	v_mul_f32_e32 v94, v96, v135
	v_mul_f32_e32 v90, v90, v135
	v_mul_f32_e32 v91, v91, v135
	v_mov_b32_e32 v96, v131
	v_cvt_pk_fp8_f32 v96, v90, v91
	v_mul_f32_e32 v90, v92, v135
	v_mul_f32_e32 v91, v93, v135
	v_mul_f32_e32 v82, v82, v135
	v_cvt_pk_fp8_f32 v96, v90, v91 op_sel:[0,0,1]
	v_mul_f32_e32 v83, v83, v135
	v_mov_b32_e32 v90, v131
	v_cvt_pk_fp8_f32 v90, v82, v83
	v_mul_f32_e32 v82, v84, v135
	v_mul_f32_e32 v78, v78, v135
	v_mul_f32_e32 v79, v79, v135
	v_mov_b32_e32 v84, v131
	v_cvt_pk_fp8_f32 v84, v78, v79
	v_mul_f32_e32 v78, v80, v135
	v_mul_f32_e32 v79, v81, v135
	v_mul_f32_e32 v74, v74, v135
	v_cvt_pk_fp8_f32 v84, v78, v79 op_sel:[0,0,1]
	v_mul_f32_e32 v75, v75, v135
	v_mov_b32_e32 v78, v131
	v_cvt_pk_fp8_f32 v78, v74, v75
	v_mul_f32_e32 v74, v76, v135
	v_mul_f32_e32 v70, v70, v135
	v_mul_f32_e32 v71, v71, v135
	v_mov_b32_e32 v76, v131
	v_cvt_pk_fp8_f32 v76, v70, v71
	v_mul_f32_e32 v70, v72, v135
	v_mul_f32_e32 v71, v73, v135
	v_mul_f32_e32 v66, v66, v135
	v_cvt_pk_fp8_f32 v76, v70, v71 op_sel:[0,0,1]
	v_mul_f32_e32 v67, v67, v135
	v_mov_b32_e32 v70, v131
	v_cvt_pk_fp8_f32 v70, v66, v67
	v_mul_f32_e32 v66, v68, v135
	v_mul_f32_e32 v58, v58, v135
	v_mul_f32_e32 v59, v59, v135
	v_mov_b32_e32 v68, v131
	v_mul_f32_e32 v127, v129, v135
	v_mul_f32_e32 v111, v113, v135
	v_mul_f32_e32 v95, v97, v135
	v_mul_f32_e32 v75, v77, v135
	v_cvt_pk_fp8_f32 v68, v58, v59
	v_cvt_pk_fp8_f32 v137, v126, v127 op_sel:[0,0,1]
	v_cvt_pk_fp8_f32 v114, v110, v111 op_sel:[0,0,1]
	v_cvt_pk_fp8_f32 v98, v94, v95 op_sel:[0,0,1]
	v_cvt_pk_fp8_f32 v78, v74, v75 op_sel:[0,0,1]
	v_mul_f32_e32 v119, v121, v135
	v_mul_f32_e32 v103, v105, v135
	v_mul_f32_e32 v83, v85, v135
	v_mul_f32_e32 v67, v69, v135
	v_cvt_pk_fp8_f32 v122, v118, v119 op_sel:[0,0,1]
	v_cvt_pk_fp8_f32 v106, v102, v103 op_sel:[0,0,1]
	v_cvt_pk_fp8_f32 v90, v82, v83 op_sel:[0,0,1]
	v_cvt_pk_fp8_f32 v70, v66, v67 op_sel:[0,0,1]
	v_mul_f32_e32 v58, v60, v135
	v_mul_f32_e32 v59, v61, v135
	v_cvt_pk_fp8_f32 v68, v58, v59 op_sel:[0,0,1]
	global_store_dword v[138:139], v137, off
	global_store_dword v[138:139], v128, off offset:256
	global_store_dword v[138:139], v122, off offset:512
	global_store_dword v[138:139], v120, off offset:768
	global_store_dword v[138:139], v114, off offset:1024
	global_store_dword v[138:139], v112, off offset:1280
	global_store_dword v[138:139], v106, off offset:1536
	global_store_dword v[138:139], v104, off offset:1792
	global_store_dword v[138:139], v98, off offset:2048
	global_store_dword v[138:139], v96, off offset:2304
	global_store_dword v[138:139], v90, off offset:2560
	global_store_dword v[138:139], v84, off offset:2816
	global_store_dword v[138:139], v78, off offset:3072
	global_store_dword v[138:139], v76, off offset:3328
	global_store_dword v[138:139], v70, off offset:3584
	global_store_dword v[138:139], v68, off offset:3840
	s_and_saveexec_b64 s[8:9], s[0:1]
	s_cbranch_execz .LBB0_620
	s_lshl_b64 s[6:7], s[6:7], 2
	s_add_u32 s6, s17, s6
	s_addc_u32 s7, s18, s7
	v_mul_f32_e32 v58, 0x3b800000, v130
	global_store_dword v131, v58, s[6:7]
	s_branch .LBB0_620

;     ...
;     for (int chain = blockIdx.x; chain < NB * NHEAD; chain += G) {
;         const int b = chain >> 5, h = chain & 31;
;         const float* mu = in[8];
;         const f32x4 mur = *(const f32x4*)(mu + h * 64 + j4), muk = *(const f32x4*)(mu + 2048 + h * 64 + j4), muv = *(const f32x4*)(mu + 4096 + h * 64 + j4);
;         const f32x4 kk_ = *(const f32x4*)(in[14] + h * 64 + j4), ka_ = *(const f32x4*)(in[15] + h * 64 + j4), rk_ = *(const f32x4*)(in[16] + h * 64 + j4);
;         const f32x4 gng = *(const f32x4*)(in[17] + h * 64 + j4), gnb = *(const f32x4*)(in[18] + h * 64 + j4);
;         float S0[4], S1[4];
; #pragma unroll
;         for (int j = 0; j < 4; ++j) { S0[j] = 0.f; S1[j] = 0.f; }
;         const f32x4 w0v = *(const f32x4*)(in[9] + h * 64 + j4), a0v = *(const f32x4*)(in[11] + h * 64 + j4);
;         RwkvRegs R; rwkv_load(R, Z, WAG, b, h, tt, j4, w0v, a0v);
;         const int nchunk = (LSEQ + 31) / 32;
.LBB0_677:
	s_or_b64 exec, exec, s[20:21]
	s_lshl_b32 s18, s22, 1
	s_sub_i32 s56, s23, 17
	s_mov_b32 s13, s19
	s_cmp_lt_u32 s54, 32
	v_lshl_add_u64 v[148:149], v[110:111], 0, s[18:19]
	v_lshl_add_u64 v[150:151], v[114:115], 0, s[12:13]
	v_mov_b32_e32 v156, 0
	s_mov_b32 s57, 0
	s_cselect_b64 s[20:21], -1, 0
	s_mov_b32 s58, 0
	v_mov_b32_e32 v152, 0
	v_mov_b32_e32 v92, 0
	v_mov_b32_e32 v90, 0
	v_mov_b32_e32 v157, 0
	v_mov_b32_e32 v153, 0
	v_mov_b32_e32 v93, 0
	v_mov_b32_e32 v91, 0
	s_waitcnt vmcnt(0)
	s_branch .LBB0_679

; #define LAS __attribute__((address_space(3)))
; __device__ __forceinline__ float sum16(float x) { x = sum8(x); x += dppf<DPP_MIRROR>(x); return x; }
; __device__ __forceinline__ float sigmoidf_(float v) { return __builtin_amdgcn_rcpf(1.0f + __expf(-v)); }
; __device__ __forceinline__ f32x4 unpack4(u32x2 q) { return (f32x4){bflo(q.x), bfhi(q.x), bflo(q.y), bfhi(q.y)}; }
;     ...
;         for (int c = 0; c < nchunk; ++c) {
;             LAS float* buf = (LAS float*)(lds + (c & 1) * 65536);
;             LAS float* bon = bonus + (c & 1) * 96;
;             {
;                 const f32x4 zr = unpack4(R.zr), zk = unpack4(R.zk), zv = unpack4(R.zv), pr = unpack4(R.pr), pk = unpack4(R.pk), pv = unpack4(R.pv);
;                 f32x4 dec = R.dec + w0v, av = R.a + a0v;
; #pragma unroll
;                 for (int e = 0; e < 4; ++e) { dec[e] = decay_of(dec[e]); av[e] = sigmoidf_(av[e]); }
;                 const f32x4 r = zr + (pr - zr) * mur, k = zk + (pk - zk) * muk, v = zv + (pv - zv) * muv;
;                 const f32x4 kr = k * kk_;
;                 const float ss = sum16((kr[0] * kr[0] + kr[1] * kr[1]) + (kr[2] * kr[2] + kr[3] * kr[3]));
;                 const float inrm = rsqrtf(fmaxf(ss, 1e-24f));
;                 const f32x4 kk = kr * inrm;
;                 const f32x4 km = k * (1.0f + (av - 1.0f) * ka_);
;                 const f32x4 kka = kk * av;
;                 const f32x4 rb = r * km * rk_;
;                 const float bs = sum16((rb[0] + rb[1]) + (rb[2] + rb[3]));
;                 const f32x4 rka = r * kka, rkm = r * km;
;                 const float c1 = sum16((rka[0] + rka[1]) + (rka[2] + rka[3])), c2 = sum16((rkm[0] + rkm[1]) + (rkm[2] + rkm[3]));
;                 const int o = tt * 64 + j4;
;                 *(LAS f32x4*)(buf + 0 * 2048 + o) = r * dec; *(LAS f32x4*)(buf + 1 * 2048 + o) = dec; *(LAS f32x4*)(buf + 2 * 2048 + o) = km; *(LAS f32x4*)(buf + 3 * 2048 + o) = v;
;                 *(LAS f32x4*)(buf + 4 * 2048 + o) = kk; *(LAS f32x4*)(buf + 5 * 2048 + o) = kka; *(LAS f32x4*)(buf + 6 * 2048 + o) = R.g;
;                 if (q == 0) { bon[tt] = bs; bon[32 + tt] = c1; bon[64 + tt] = c2; }
.LBB0_679:
	s_waitcnt vmcnt(1)
	v_pk_add_f32 v[72:73], v[38:39], v[50:51]
	v_pk_add_f32 v[70:71], v[40:41], v[52:53]
	v_mul_f32_e32 v72, 0xbfb8aa3b, v72
	v_exp_f32_e32 v72, v72
	v_mul_f32_e32 v70, 0xbfb8aa3b, v70
	v_exp_f32_e32 v70, v70
	v_mul_f32_e32 v71, 0xbfb8aa3b, v71
	v_add_f32_e32 v72, 1.0, v72
	v_rcp_f32_e32 v76, v72
	v_mul_f32_e32 v72, 0xbfb8aa3b, v73
	v_exp_f32_e32 v72, v72
	v_exp_f32_e32 v71, v71
	v_add_f32_e32 v70, 1.0, v70
	v_lshlrev_b32_e32 v54, 16, v136
	v_and_b32_e32 v55, 0xffff0000, v136
	v_lshlrev_b32_e32 v56, 16, v137
	v_and_b32_e32 v57, 0xffff0000, v137
	v_lshlrev_b32_e32 v74, 16, v144
	v_and_b32_e32 v75, 0xffff0000, v144
	v_lshlrev_b32_e32 v80, 16, v145
	v_and_b32_e32 v81, 0xffff0000, v145
	v_add_f32_e32 v72, 1.0, v72
	v_rcp_f32_e32 v78, v70
	v_add_f32_e32 v70, 1.0, v71
	v_lshlrev_b32_e32 v58, 16, v138
	v_and_b32_e32 v59, 0xffff0000, v138
	v_lshlrev_b32_e32 v64, 16, v139
	v_and_b32_e32 v65, 0xffff0000, v139
	v_lshlrev_b32_e32 v82, 16, v142
	v_and_b32_e32 v83, 0xffff0000, v142
	v_lshlrev_b32_e32 v86, 16, v143
	v_and_b32_e32 v87, 0xffff0000, v143
	v_rcp_f32_e32 v77, v72
	v_rcp_f32_e32 v79, v70
	v_sub_f32_e32 v71, v75, v55
	v_sub_f32_e32 v70, v74, v54
	v_sub_f32_e32 v73, v81, v57
	v_sub_f32_e32 v72, v80, v56
	v_pk_fma_f32 v[80:81], v[4:5], v[72:73], v[56:57]
	v_pk_fma_f32 v[84:85], v[2:3], v[70:71], v[54:55]
	v_sub_f32_e32 v55, v83, v59
	v_sub_f32_e32 v54, v82, v58
	v_sub_f32_e32 v57, v87, v65
	v_sub_f32_e32 v56, v86, v64
	v_pk_fma_f32 v[56:57], v[8:9], v[56:57], v[64:65]
	v_pk_fma_f32 v[54:55], v[6:7], v[54:55], v[58:59]
	v_pk_mul_f32 v[70:71], v[16:17], v[56:57]
	v_pk_mul_f32 v[72:73], v[14:15], v[54:55]
	v_pk_mul_f32 v[74:75], v[70:71], v[70:71]
	v_pk_mul_f32 v[82:83], v[72:73], v[72:73]
	v_pk_add_f32 v[60:61], v[34:35], v[42:43]
	v_pk_mov_b32 v[86:87], v[82:83], v[74:75] op_sel:[1,0]
	v_mov_b32_e32 v83, v75
	v_pk_add_f32 v[74:75], v[86:87], v[82:83]
	v_pk_add_f32 v[62:63], v[36:37], v[44:45]
	v_add_f32_e32 v64, v74, v75
	v_mul_f32_e32 v60, 0xbfb8aa3b, v60
	v_mul_f32_e32 v61, 0xbfb8aa3b, v61
	v_add_f32_dpp v64, v64, v64 quad_perm:[1,0,3,2] row_mask:0xf bank_mask:0xf bound_ctrl:1
	v_mul_f32_e32 v62, 0xbfb8aa3b, v62
	v_mul_f32_e32 v63, 0xbfb8aa3b, v63
	v_add_f32_dpp v64, v64, v64 quad_perm:[2,3,0,1] row_mask:0xf bank_mask:0xf bound_ctrl:1
	v_lshlrev_b32_e32 v68, 16, v140
	v_and_b32_e32 v69, 0xffff0000, v140
	v_add_f32_dpp v64, v64, v64 row_half_mirror row_mask:0xf bank_mask:0xf bound_ctrl:1
	v_lshlrev_b32_e32 v66, 16, v141
	v_and_b32_e32 v67, 0xffff0000, v141
	v_add_f32_dpp v64, v64, v64 row_mirror row_mask:0xf bank_mask:0xf bound_ctrl:1
	v_max_f32_e32 v64, 0x179abe15, v64
	v_rsq_f32_e32 v74, v64
	v_lshlrev_b32_e32 v88, 16, v146
	v_and_b32_e32 v89, 0xffff0000, v146
	v_lshlrev_b32_e32 v94, 16, v147
	v_exp_f32_e32 v60, v60
	v_and_b32_e32 v95, 0xffff0000, v147
	v_exp_f32_e32 v61, v61
	v_exp_f32_e32 v62, v62
	v_exp_f32_e32 v63, v63
	v_sub_f32_e32 v59, v89, v69
	v_sub_f32_e32 v58, v88, v68
	v_sub_f32_e32 v65, v95, v67
	v_sub_f32_e32 v64, v94, v66
	v_pk_fma_f32 v[66:67], v[12:13], v[64:65], v[66:67]
	v_pk_fma_f32 v[64:65], v[10:11], v[58:59], v[68:69]
	v_pk_mul_f32 v[68:69], v[72:73], v[74:75] op_sel_hi:[1,0]
	v_pk_add_f32 v[58:59], v[78:79], -1.0 op_sel_hi:[1,0]
	v_pk_add_f32 v[72:73], v[76:77], -1.0 op_sel_hi:[1,0]
	v_pk_fma_f32 v[58:59], v[20:21], v[58:59], 1.0 op_sel_hi:[1,1,0]
	v_pk_fma_f32 v[72:73], v[18:19], v[72:73], 1.0 op_sel_hi:[1,1,0]
	v_add_f32_e32 v60, 1.0, v60
	v_add_f32_e32 v61, 1.0, v61
	v_add_f32_e32 v62, 1.0, v62
	v_add_f32_e32 v63, 1.0, v63
	v_pk_mul_f32 v[70:71], v[70:71], v[74:75] op_sel_hi:[1,0]
	v_pk_mul_f32 v[74:75], v[56:57], v[58:59]
	v_pk_mul_f32 v[72:73], v[54:55], v[72:73]
	v_rcp_f32_e32 v60, v60
	v_rcp_f32_e32 v61, v61
	v_rcp_f32_e32 v62, v62
	v_rcp_f32_e32 v63, v63
	v_pk_mul_f32 v[58:59], v[84:85], v[72:73]
	v_pk_mul_f32 v[82:83], v[80:81], v[74:75]
	v_pk_mul_f32 v[56:57], v[22:23], v[58:59]
	v_pk_mul_f32 v[54:55], v[24:25], v[82:83]
	v_pk_mul_f32 v[78:79], v[78:79], v[70:71]
	v_pk_mul_f32 v[76:77], v[76:77], v[68:69]
	v_add_f32_e32 v56, v56, v57
	v_add_f32_e32 v54, v54, v55
	v_add_f32_e32 v54, v56, v54
	v_pk_mul_f32 v[56:57], v[80:81], v[78:79]
	v_pk_mul_f32 v[86:87], v[84:85], v[76:77]
	v_mul_f32_e32 v60, 0xbf60028b, v60
	v_mul_f32_e32 v61, 0xbf60028b, v61
	v_mul_f32_e32 v62, 0xbf60028b, v62
	v_mul_f32_e32 v63, 0xbf60028b, v63
	v_add_f32_e32 v86, v86, v87
	v_add_f32_e32 v56, v56, v57
	v_add_f32_e32 v58, v58, v59
	v_add_f32_e32 v59, v82, v83
	s_and_b32 s12, s58, 1
	v_exp_f32_e32 v60, v60
	v_exp_f32_e32 v61, v61
	v_exp_f32_e32 v62, v62
	v_exp_f32_e32 v63, v63
	v_add_f32_e32 v56, v86, v56
	v_add_f32_e32 v58, v58, v59
	s_lshl_b32 s13, s12, 16
	s_mulk_i32 s12, 0x180
	v_add_f32_dpp v54, v54, v54 quad_perm:[1,0,3,2] row_mask:0xf bank_mask:0xf bound_ctrl:1
	v_add_f32_dpp v56, v56, v56 quad_perm:[1,0,3,2] row_mask:0xf bank_mask:0xf bound_ctrl:1
	v_add_f32_dpp v58, v58, v58 quad_perm:[1,0,3,2] row_mask:0xf bank_mask:0xf bound_ctrl:1
	s_add_i32 s59, s12, 0
	v_add_f32_dpp v54, v54, v54 quad_perm:[2,3,0,1] row_mask:0xf bank_mask:0xf bound_ctrl:1
	v_add_f32_dpp v56, v56, v56 quad_perm:[2,3,0,1] row_mask:0xf bank_mask:0xf bound_ctrl:1
	v_add_f32_dpp v58, v58, v58 quad_perm:[2,3,0,1] row_mask:0xf bank_mask:0xf bound_ctrl:1
	s_add_i32 s60, s13, 0
	s_add_i32 s59, s59, 0x20200
	v_add_f32_dpp v54, v54, v54 row_half_mirror row_mask:0xf bank_mask:0xf bound_ctrl:1
	v_add_f32_dpp v56, v56, v56 row_half_mirror row_mask:0xf bank_mask:0xf bound_ctrl:1
	v_add_f32_dpp v58, v58, v58 row_half_mirror row_mask:0xf bank_mask:0xf bound_ctrl:1
	v_mov_b32_dpp v55, v54 row_mirror row_mask:0xf bank_mask:0xf bound_ctrl:1
	v_mov_b32_dpp v57, v56 row_mirror row_mask:0xf bank_mask:0xf bound_ctrl:1
	v_mov_b32_dpp v59, v58 row_mirror row_mask:0xf bank_mask:0xf bound_ctrl:1
	v_pk_mul_f32 v[82:83], v[80:81], v[62:63]
	v_pk_mul_f32 v[80:81], v[84:85], v[60:61]
	v_lshl_add_u32 v163, v160, 2, s60
	v_lshl_add_u32 v164, v1, 2, s59
	ds_write_b128 v163, v[80:83]
	ds_write_b128 v163, v[60:63] offset:8192
	ds_write_b128 v163, v[72:75] offset:16384
	ds_write_b128 v163, v[64:67] offset:24576
	ds_write_b128 v163, v[68:71] offset:32768
	ds_write_b128 v163, v[76:79] offset:40960
	ds_write_b128 v163, v[46:49] offset:49152
	s_and_saveexec_b64 s[12:13], s[10:11]
	s_cbranch_execz .LBB0_681
	v_add_f32_e32 v54, v54, v55
	v_add_f32_e32 v55, v56, v57
	v_add_f32_e32 v56, v58, v59
	ds_write2_b32 v164, v54, v55 offset1:32
	ds_write_b32 v164, v56 offset:256

; #define LAS __attribute__((address_space(3)))
; __device__ __forceinline__ unsigned cvt_pk_bf16(float lo, float hi) { unsigned r; asm volatile("v_cvt_pk_bf16_f32 %0, %1, %2" : "=v"(r) : "v"(lo), "v"(hi)); return r; }
; __device__ __forceinline__ float sum16(float x) { x = sum8(x); x += dppf<DPP_MIRROR>(x); return x; }
; __device__ __forceinline__ void peer_row_load(f32x4 (&v)[16], const float* const (&in)[34], int it, int layer, int lane) {
;     const int tbl = it >= NEXP, r = it - tbl * NEXP + layer * NEXP;
;     const f32x4* src = (const f32x4*)((tbl ? in[33] : in[32]) + (size_t)r * D) + lane;
; #pragma unroll
;     for (int j = 0; j < 16; ++j) v[j] = src[64 * j];
; }
; __device__ __forceinline__ void peer_row_store(const f32x4 (&v)[16], unsigned char* ws, int it, int layer, int lane) {
;     const int tbl = it >= NEXP, r = it - tbl * NEXP + layer * NEXP;
;     float am = 0.f;
; #pragma unroll
;     for (int j = 0; j < 16; ++j) am = fmaxf(fmaxf(am, fmaxf(fabsf(v[j][0]), fabsf(v[j][1]))), fmaxf(fabsf(v[j][2]), fabsf(v[j][3])));
;     am = __uint_as_float(max64u(__float_as_uint(am)));
;     ...
;             __syncthreads();
;             {
;                 const int pos = c * 32 + tt;
;                 const int o = tt * 64 + j4;
;                 const f32x4 y = *(const LAS f32x4*)(buf + 7 * 2048 + o), v = *(const LAS f32x4*)(buf + 3 * 2048 + o), g = *(const LAS f32x4*)(buf + 6 * 2048 + o);
;                 const float mean = sum16((y[0] + y[1]) + (y[2] + y[3])) * (1.0f / 64.0f);
;                 const f32x4 dy = y - mean;
;                 const float var = sum16((dy[0] * dy[0] + dy[1] * dy[1]) + (dy[2] * dy[2] + dy[3] * dy[3])) * (1.0f / 64.0f);
;                 const float rs = rsqrtf(var + GN_EPS), bs = bon[tt];
;     ...
;                 const f32x4 out = (f32x4){0.f, 0.f, 0.f, 0.f};
;     ...
;                 const f32x4 out = (dy * rs * gng + gnb + v * bs) * g;
;     ...
;                 if (pos < LSEQ && (b == 0 || pos >= NMETA)) { u32x2 w; w.x = cvt_pk_bf16(out[0], out[1]); w.y = cvt_pk_bf16(out[2], out[3]);
;                     *(u32x2*)(Y + (size_t)rowof(b, pos) * D + 2048 + h * 64 + j4) = w; }
.LBB0_752:
.LBB0_753:
	s_waitcnt lgkmcnt(0)
	s_barrier
	ds_read_b128 v[54:57], v163 offset:57344
	v_add_u32_e32 v58, s57, v1
	v_cmp_lt_i32_e64 s[12:13], 15, v58
	v_cmp_gt_i32_e32 vcc, s3, v58
	s_or_b64 s[12:13], s[20:21], s[12:13]
	s_waitcnt lgkmcnt(0)
	v_mov_b32_e32 v60, v55
	v_mov_b32_e32 v61, v56
	v_mov_b32_e32 v62, v54
	v_mov_b32_e32 v63, v57
	v_pk_add_f32 v[60:61], v[60:61], v[62:63]
	s_and_b64 s[22:23], vcc, s[12:13]
	v_add_f32_e32 v59, v60, v61
	s_nop 1
	v_add_f32_dpp v59, v59, v59 quad_perm:[1,0,3,2] row_mask:0xf bank_mask:0xf bound_ctrl:1
	s_nop 1
	v_add_f32_dpp v59, v59, v59 quad_perm:[2,3,0,1] row_mask:0xf bank_mask:0xf bound_ctrl:1
	s_nop 1
	v_add_f32_dpp v59, v59, v59 row_half_mirror row_mask:0xf bank_mask:0xf bound_ctrl:1
	s_nop 1
	v_add_f32_dpp v59, v59, v59 row_mirror row_mask:0xf bank_mask:0xf bound_ctrl:1
	v_fmamk_f32 v57, v59, 0xbc800000, v57
	v_fmamk_f32 v55, v59, 0xbc800000, v55
	v_fmamk_f32 v56, v59, 0xbc800000, v56
	v_fmac_f32_e32 v54, 0xbc800000, v59
	v_mul_f32_e32 v59, v55, v55
	v_mul_f32_e32 v60, v57, v57
	v_fmac_f32_e32 v59, v54, v54
	v_fmac_f32_e32 v60, v56, v56
	v_add_f32_e32 v59, v59, v60
	s_nop 1
	v_add_f32_dpp v59, v59, v59 quad_perm:[1,0,3,2] row_mask:0xf bank_mask:0xf bound_ctrl:1
	s_nop 1
	v_add_f32_dpp v59, v59, v59 quad_perm:[2,3,0,1] row_mask:0xf bank_mask:0xf bound_ctrl:1
	s_nop 1
	v_add_f32_dpp v59, v59, v59 row_half_mirror row_mask:0xf bank_mask:0xf bound_ctrl:1
	s_nop 1
	v_mov_b32_dpp v60, v59 row_mirror row_mask:0xf bank_mask:0xf bound_ctrl:1
	s_and_saveexec_b64 s[12:13], s[22:23]
	v_add_f32_e32 v59, v59, v60
	v_fmamk_f32 v59, v59, 0x3c800000, v113
	v_mul_f32_e32 v60, 0x4b800000, v59
	v_cmp_gt_f32_e32 vcc, s53, v59
	s_nop 1
	v_cndmask_b32_e32 v59, v59, v60, vcc
	v_rsq_f32_e32 v59, v59
	ds_read_b128 v[60:63], v163 offset:49152
	ds_read_b128 v[64:67], v163 offset:24576
	ds_read_b32 v68, v164
	v_mul_f32_e32 v69, 0x45800000, v59
	v_cndmask_b32_e32 v70, v59, v69, vcc
	v_pk_mul_f32 v[54:55], v[54:55], v[70:71] op_sel_hi:[1,0]
	v_pk_mul_f32 v[56:57], v[56:57], v[70:71] op_sel_hi:[1,0]
	v_pk_fma_f32 v[54:55], v[26:27], v[54:55], v[30:31]
	v_pk_fma_f32 v[56:57], v[28:29], v[56:57], v[32:33]
	s_waitcnt lgkmcnt(0)
	v_pk_fma_f32 v[54:55], v[64:65], v[68:69], v[54:55] op_sel_hi:[1,0,1]
	v_pk_fma_f32 v[56:57], v[66:67], v[68:69], v[56:57] op_sel_hi:[1,0,1]
	v_pk_mul_f32 v[54:55], v[60:61], v[54:55]
	v_pk_mul_f32 v[56:57], v[62:63], v[56:57]
	v_cvt_pk_bf16_f32 v54, v54, v55
	v_cmp_lt_i32_e32 vcc, 15, v58
	v_cvt_pk_bf16_f32 v55, v56, v57
	v_mov_b32_e32 v56, s55
	s_nop 0
	v_cndmask_b32_e32 v56, v161, v56, vcc
	v_add3_u32 v56, v1, v56, s57
	v_ashrrev_i32_e32 v57, 31, v56
	v_lshlrev_b64 v[56:57], 13, v[56:57]
	v_lshl_add_u64 v[56:57], s[90:91], 0, v[56:57]
	v_lshl_add_u64 v[56:57], v[56:57], 0, s[18:19]
	v_lshl_add_u64 v[56:57], v[56:57], 0, v[108:109]
	v_add_co_u32_e32 v56, vcc, 0x3eb59000, v56
	s_nop 1
	v_addc_co_u32_e32 v57, vcc, 0, v57, vcc
	global_store_dwordx2 v[56:57], v[54:55], off
	s_branch .LBB0_678
.Lp4r_conv:
	s_waitcnt vmcnt(0) lgkmcnt(0)
	v_and_b32_e32 v11, 63, v0
	v_lshrrev_b32_e32 v7, 6, v0
	v_lshlrev_b32_e32 v1, 4, v11
	v_readfirstlane_b32 s0, v7
	v_lshlrev_b32_e32 v2, 2, v11
	v_add_u32_e32 v3, 0x1000, v1
	v_add_u32_e32 v4, 0x2000, v1
	v_add_u32_e32 v5, 0x3000, v1
	v_mov_b32_e32 v10, 0
	v_cmp_eq_u32_e64 s[12:13], 0, v11
	s_lshl_b32 s1, s2, 3
	s_add_i32 s4, s1, s0
	s_addk_i32 s4, 0x2000
	s_mov_b32 s14, 0x43800000
	s_lshl_b32 s1, s4, 14
	s_add_u32 s6, s84, s1
	s_addc_u32 s7, s85, 0
	global_load_dwordx4 v[40:43], v1, s[6:7]
	global_load_dwordx4 v[44:47], v1, s[6:7] offset:1024
	global_load_dwordx4 v[48:51], v1, s[6:7] offset:2048
	global_load_dwordx4 v[52:55], v1, s[6:7] offset:3072
	global_load_dwordx4 v[56:59], v3, s[6:7]
	global_load_dwordx4 v[60:63], v3, s[6:7] offset:1024
	global_load_dwordx4 v[64:67], v3, s[6:7] offset:2048
	global_load_dwordx4 v[68:71], v3, s[6:7] offset:3072
	global_load_dwordx4 v[72:75], v4, s[6:7]
	global_load_dwordx4 v[76:79], v4, s[6:7] offset:1024
	global_load_dwordx4 v[80:83], v4, s[6:7] offset:2048
	global_load_dwordx4 v[84:87], v4, s[6:7] offset:3072
	global_load_dwordx4 v[88:91], v5, s[6:7]
	global_load_dwordx4 v[92:95], v5, s[6:7] offset:1024
	global_load_dwordx4 v[96:99], v5, s[6:7] offset:2048
	global_load_dwordx4 v[100:103], v5, s[6:7] offset:3072
	s_add_i32 s5, s4, 1024
	s_lshl_b32 s1, s5, 14
	s_add_u32 s6, s84, s1
	s_addc_u32 s7, s85, 0
	global_load_dwordx4 v[104:107], v1, s[6:7]
	global_load_dwordx4 v[108:111], v1, s[6:7] offset:1024
	global_load_dwordx4 v[112:115], v1, s[6:7] offset:2048
	global_load_dwordx4 v[116:119], v1, s[6:7] offset:3072
	global_load_dwordx4 v[120:123], v3, s[6:7]
	global_load_dwordx4 v[124:127], v3, s[6:7] offset:1024
	global_load_dwordx4 v[128:131], v3, s[6:7] offset:2048
	global_load_dwordx4 v[132:135], v3, s[6:7] offset:3072
	global_load_dwordx4 v[136:139], v4, s[6:7]
	global_load_dwordx4 v[140:143], v4, s[6:7] offset:1024
	global_load_dwordx4 v[144:147], v4, s[6:7] offset:2048
	global_load_dwordx4 v[148:151], v4, s[6:7] offset:3072
	global_load_dwordx4 v[152:155], v5, s[6:7]
	global_load_dwordx4 v[156:159], v5, s[6:7] offset:1024
	global_load_dwordx4 v[160:163], v5, s[6:7] offset:2048
	global_load_dwordx4 v[164:167], v5, s[6:7] offset:3072
	s_waitcnt vmcnt(31)
	v_max3_f32 v6, |v40|, |v41|, 0
	v_max3_f32 v6, |v42|, |v43|, v6
	s_waitcnt vmcnt(30)
	v_max3_f32 v6, |v44|, |v45|, v6
	v_max3_f32 v6, |v46|, |v47|, v6
	s_waitcnt vmcnt(29)
	v_max3_f32 v6, |v48|, |v49|, v6
	v_max3_f32 v6, |v50|, |v51|, v6
	s_waitcnt vmcnt(28)
	v_max3_f32 v6, |v52|, |v53|, v6
	v_max3_f32 v6, |v54|, |v55|, v6
	s_waitcnt vmcnt(27)
; __device__ __forceinline__ void peer_row_store(const f32x4 (&v)[16], unsigned char* ws, int it, int layer, int lane) {
;     const int tbl = it >= NEXP, r = it - tbl * NEXP + layer * NEXP;
;     float am = 0.f;
; #pragma unroll
;     for (int j = 0; j < 16; ++j) am = fmaxf(fmaxf(am, fmaxf(fabsf(v[j][0]), fabsf(v[j][1]))), fmaxf(fabsf(v[j][2]), fabsf(v[j][3])));
;     am = __uint_as_float(max64u(__float_as_uint(am)));
;     const float q = am > 0.f ? 256.0f / am : 0.f;
;     unsigned* dst = (unsigned*)(ws + (tbl ? WS_PV : WS_PU) + (size_t)r * D) + lane;
;     if (tbl) {
;         const int rl = it - NEXP;
;         unsigned char* pvl = ws + WS_PV + (size_t)layer * NEXP * D + (size_t)rl * 8 + (lane & 1) * 4;
;         unsigned char* pvg = ws + WS_PV + (size_t)layer * NEXP * D + (size_t)NEXP * 2048 + (size_t)rl * 2048 + 4 * lane;
; #pragma unroll
;         for (int j = 0; j < 16; ++j) { int w = __builtin_amdgcn_cvt_pk_bf8_f32(v[j][0] * q, v[j][1] * q, 0, false); w = __builtin_amdgcn_cvt_pk_bf8_f32(v[j][2] * q, v[j][3] * q, w, true);
;             if (j < 8) *(unsigned*)(pvl + (size_t)((lane >> 1) + 32 * j) * (NEXP * 8)) = (unsigned)w;
;             else *(unsigned*)(pvg + 256 * (j - 8)) = (unsigned)w; }
;     } else {
; #pragma unroll
;         for (int j = 0; j < 16; ++j) { int w = __builtin_amdgcn_cvt_pk_fp8_f32(v[j][0] * q, v[j][1] * q, 0, false); w = __builtin_amdgcn_cvt_pk_fp8_f32(v[j][2] * q, v[j][3] * q, w, true); dst[64 * j] = (unsigned)w; }
;     }
;     if (lane == 0) ((float*)(ws + (tbl ? WS_SV : WS_SU)))[r] = am * (1.0f / 256.0f);
	v_max3_f32 v6, |v56|, |v57|, v6
	v_max3_f32 v6, |v58|, |v59|, v6
	s_waitcnt vmcnt(26)
	v_max3_f32 v6, |v60|, |v61|, v6
	v_max3_f32 v6, |v62|, |v63|, v6
	s_waitcnt vmcnt(25)
	v_max3_f32 v6, |v64|, |v65|, v6
	v_max3_f32 v6, |v66|, |v67|, v6
	s_waitcnt vmcnt(24)
	v_max3_f32 v6, |v68|, |v69|, v6
	v_max3_f32 v6, |v70|, |v71|, v6
	s_waitcnt vmcnt(23)
	v_max3_f32 v6, |v72|, |v73|, v6
	v_max3_f32 v6, |v74|, |v75|, v6
	s_waitcnt vmcnt(22)
	v_max3_f32 v6, |v76|, |v77|, v6
	v_max3_f32 v6, |v78|, |v79|, v6
	s_waitcnt vmcnt(21)
	v_max3_f32 v6, |v80|, |v81|, v6
	v_max3_f32 v6, |v82|, |v83|, v6
	s_waitcnt vmcnt(20)
	v_max3_f32 v6, |v84|, |v85|, v6
	v_max3_f32 v6, |v86|, |v87|, v6
	s_waitcnt vmcnt(19)
	v_max3_f32 v6, |v88|, |v89|, v6
	v_max3_f32 v6, |v90|, |v91|, v6
	s_waitcnt vmcnt(18)
	v_max3_f32 v6, |v92|, |v93|, v6
	v_max3_f32 v6, |v94|, |v95|, v6
	s_waitcnt vmcnt(17)
	v_max3_f32 v6, |v96|, |v97|, v6
	v_max3_f32 v6, |v98|, |v99|, v6
	s_waitcnt vmcnt(16)
	v_max3_f32 v6, |v100|, |v101|, v6
	v_max3_f32 v6, |v102|, |v103|, v6
	s_nop 1
	v_max_u32_dpp v6, v6, v6 quad_perm:[1,0,3,2] row_mask:0xf bank_mask:0xf bound_ctrl:1
	s_nop 1
	v_max_u32_dpp v6, v6, v6 quad_perm:[2,3,0,1] row_mask:0xf bank_mask:0xf bound_ctrl:1
	s_nop 1
	v_max_u32_dpp v6, v6, v6 row_half_mirror row_mask:0xf bank_mask:0xf bound_ctrl:1
	s_nop 1
	v_max_u32_dpp v6, v6, v6 row_mirror row_mask:0xf bank_mask:0xf bound_ctrl:1
	s_nop 1
	v_mov_b32_e32 v7, v6
	s_nop 1
	v_permlane16_swap_b32_e32 v6, v7
	v_max_u32_e32 v6, v6, v7
	v_mov_b32_e32 v7, v6
	s_nop 1
	v_permlane32_swap_b32_e32 v6, v7
	v_max_u32_e32 v6, v6, v7
	v_div_scale_f32 v12, s[16:17], v6, v6, s14
	v_rcp_f32_e32 v13, v12
	s_nop 0
	v_fma_f32 v14, -v12, v13, 1.0
	v_fmac_f32_e32 v13, v14, v13
	v_div_scale_f32 v14, vcc, s14, v6, s14
	v_mul_f32_e32 v15, v14, v13
	v_fma_f32 v16, -v12, v15, v14
	v_fmac_f32_e32 v15, v16, v13
	v_fma_f32 v12, -v12, v15, v14
	v_div_fmas_f32 v12, v12, v13, v15
	v_div_fixup_f32 v9, v12, v6, s14
	v_cmp_lt_f32_e32 vcc, 0, v6
	s_nop 1
	v_cndmask_b32_e32 v9, 0, v9, vcc
	s_lshl_b32 s1, s4, 12
	s_add_u32 s8, s90, 0xba00000
	s_addc_u32 s9, s91, 0
	s_add_u32 s8, s8, s1
	s_addc_u32 s9, s9, 0
	s_lshl_b32 s1, s4, 2
	s_add_u32 s10, s90, 0x1ba00000
	s_addc_u32 s11, s91, 0
	s_add_u32 s10, s10, s1
	s_addc_u32 s11, s11, 0
	v_mul_f32_e32 v40, v40, v9
	v_mul_f32_e32 v41, v41, v9
	v_mul_f32_e32 v42, v42, v9
	v_mul_f32_e32 v43, v43, v9
	v_mov_b32_e32 v20, v10
	v_cvt_pk_fp8_f32 v20, v40, v41
	v_mul_f32_e32 v44, v44, v9
	v_mul_f32_e32 v45, v45, v9
	v_mul_f32_e32 v46, v46, v9
	v_mul_f32_e32 v47, v47, v9
	v_mov_b32_e32 v21, v10
	v_cvt_pk_fp8_f32 v21, v44, v45
	v_cvt_pk_fp8_f32 v20, v42, v43 op_sel:[0,0,1]
	v_mul_f32_e32 v48, v48, v9
	v_mul_f32_e32 v49, v49, v9
	v_mul_f32_e32 v50, v50, v9
	v_mul_f32_e32 v51, v51, v9
	v_mov_b32_e32 v22, v10
	v_cvt_pk_fp8_f32 v22, v48, v49
	v_cvt_pk_fp8_f32 v21, v46, v47 op_sel:[0,0,1]
	v_mul_f32_e32 v52, v52, v9
	v_mul_f32_e32 v53, v53, v9
	v_mul_f32_e32 v54, v54, v9
	v_mul_f32_e32 v55, v55, v9
	v_mov_b32_e32 v23, v10
	v_cvt_pk_fp8_f32 v23, v52, v53
	v_cvt_pk_fp8_f32 v22, v50, v51 op_sel:[0,0,1]
	v_mul_f32_e32 v56, v56, v9
	v_mul_f32_e32 v57, v57, v9
	v_mul_f32_e32 v58, v58, v9
	v_mul_f32_e32 v59, v59, v9
	v_mov_b32_e32 v24, v10
	v_cvt_pk_fp8_f32 v24, v56, v57
	v_cvt_pk_fp8_f32 v23, v54, v55 op_sel:[0,0,1]
	v_mul_f32_e32 v60, v60, v9
	v_mul_f32_e32 v61, v61, v9
	v_mul_f32_e32 v62, v62, v9
	v_mul_f32_e32 v63, v63, v9
	v_mov_b32_e32 v25, v10
	v_cvt_pk_fp8_f32 v25, v60, v61
	v_cvt_pk_fp8_f32 v24, v58, v59 op_sel:[0,0,1]
	v_mul_f32_e32 v64, v64, v9
	v_mul_f32_e32 v65, v65, v9
	v_mul_f32_e32 v66, v66, v9
	v_mul_f32_e32 v67, v67, v9
	v_mov_b32_e32 v26, v10
	v_cvt_pk_fp8_f32 v26, v64, v65
	v_cvt_pk_fp8_f32 v25, v62, v63 op_sel:[0,0,1]
	v_mul_f32_e32 v68, v68, v9
	v_mul_f32_e32 v69, v69, v9
	v_mul_f32_e32 v70, v70, v9
	v_mul_f32_e32 v71, v71, v9
	v_mov_b32_e32 v27, v10
	v_cvt_pk_fp8_f32 v27, v68, v69
	v_cvt_pk_fp8_f32 v26, v66, v67 op_sel:[0,0,1]
	v_mul_f32_e32 v72, v72, v9
	v_mul_f32_e32 v73, v73, v9
	v_mul_f32_e32 v74, v74, v9
	v_mul_f32_e32 v75, v75, v9
	v_mov_b32_e32 v28, v10
	v_cvt_pk_fp8_f32 v28, v72, v73
	v_cvt_pk_fp8_f32 v27, v70, v71 op_sel:[0,0,1]
	v_mul_f32_e32 v76, v76, v9
	v_mul_f32_e32 v77, v77, v9
	v_mul_f32_e32 v78, v78, v9
	v_mul_f32_e32 v79, v79, v9
	v_mov_b32_e32 v29, v10
	v_cvt_pk_fp8_f32 v29, v76, v77
	v_cvt_pk_fp8_f32 v28, v74, v75 op_sel:[0,0,1]
	v_mul_f32_e32 v80, v80, v9
	v_mul_f32_e32 v81, v81, v9
	v_mul_f32_e32 v82, v82, v9
	v_mul_f32_e32 v83, v83, v9
	v_mov_b32_e32 v30, v10
	v_cvt_pk_fp8_f32 v30, v80, v81
	v_cvt_pk_fp8_f32 v29, v78, v79 op_sel:[0,0,1]
	v_mul_f32_e32 v84, v84, v9
	v_mul_f32_e32 v85, v85, v9
	v_mul_f32_e32 v86, v86, v9
	v_mul_f32_e32 v87, v87, v9
	v_mov_b32_e32 v31, v10
	v_cvt_pk_fp8_f32 v31, v84, v85
	v_cvt_pk_fp8_f32 v30, v82, v83 op_sel:[0,0,1]
	v_mul_f32_e32 v88, v88, v9
	v_mul_f32_e32 v89, v89, v9
	v_mul_f32_e32 v90, v90, v9
	v_mul_f32_e32 v91, v91, v9
	v_mov_b32_e32 v32, v10
	v_cvt_pk_fp8_f32 v32, v88, v89
	v_cvt_pk_fp8_f32 v31, v86, v87 op_sel:[0,0,1]
	v_mul_f32_e32 v92, v92, v9
	v_mul_f32_e32 v93, v93, v9
	v_mul_f32_e32 v94, v94, v9
	v_mul_f32_e32 v95, v95, v9
	v_mov_b32_e32 v33, v10
	v_cvt_pk_fp8_f32 v33, v92, v93
	v_cvt_pk_fp8_f32 v32, v90, v91 op_sel:[0,0,1]
	v_mul_f32_e32 v96, v96, v9
	v_mul_f32_e32 v97, v97, v9
	v_mul_f32_e32 v98, v98, v9
	v_mul_f32_e32 v99, v99, v9
	v_mov_b32_e32 v34, v10
	v_cvt_pk_fp8_f32 v34, v96, v97
	v_cvt_pk_fp8_f32 v33, v94, v95 op_sel:[0,0,1]
	v_mul_f32_e32 v100, v100, v9
	v_mul_f32_e32 v101, v101, v9
	v_mul_f32_e32 v102, v102, v9
	v_mul_f32_e32 v103, v103, v9
	v_mov_b32_e32 v35, v10
	v_cvt_pk_fp8_f32 v35, v100, v101
; __device__ __forceinline__ void peer_row_load(f32x4 (&v)[16], const float* const (&in)[34], int it, int layer, int lane) {
;     const int tbl = it >= NEXP, r = it - tbl * NEXP + layer * NEXP;
;     const f32x4* src = (const f32x4*)((tbl ? in[33] : in[32]) + (size_t)r * D) + lane;
; #pragma unroll
;     for (int j = 0; j < 16; ++j) v[j] = src[64 * j];
; }
; __device__ __forceinline__ void peer_row_store(const f32x4 (&v)[16], unsigned char* ws, int it, int layer, int lane) {
;     const int tbl = it >= NEXP, r = it - tbl * NEXP + layer * NEXP;
;     float am = 0.f;
; #pragma unroll
;     for (int j = 0; j < 16; ++j) am = fmaxf(fmaxf(am, fmaxf(fabsf(v[j][0]), fabsf(v[j][1]))), fmaxf(fabsf(v[j][2]), fabsf(v[j][3])));
;     am = __uint_as_float(max64u(__float_as_uint(am)));
;     const float q = am > 0.f ? 256.0f / am : 0.f;
;     unsigned* dst = (unsigned*)(ws + (tbl ? WS_PV : WS_PU) + (size_t)r * D) + lane;
;     if (tbl) {
;         const int rl = it - NEXP;
;         unsigned char* pvl = ws + WS_PV + (size_t)layer * NEXP * D + (size_t)rl * 8 + (lane & 1) * 4;
;         unsigned char* pvg = ws + WS_PV + (size_t)layer * NEXP * D + (size_t)NEXP * 2048 + (size_t)rl * 2048 + 4 * lane;
; #pragma unroll
;         for (int j = 0; j < 16; ++j) { int w = __builtin_amdgcn_cvt_pk_bf8_f32(v[j][0] * q, v[j][1] * q, 0, false); w = __builtin_amdgcn_cvt_pk_bf8_f32(v[j][2] * q, v[j][3] * q, w, true);
;             if (j < 8) *(unsigned*)(pvl + (size_t)((lane >> 1) + 32 * j) * (NEXP * 8)) = (unsigned)w;
;             else *(unsigned*)(pvg + 256 * (j - 8)) = (unsigned)w; }
;     } else {
; #pragma unroll
;         for (int j = 0; j < 16; ++j) { int w = __builtin_amdgcn_cvt_pk_fp8_f32(v[j][0] * q, v[j][1] * q, 0, false); w = __builtin_amdgcn_cvt_pk_fp8_f32(v[j][2] * q, v[j][3] * q, w, true); dst[64 * j] = (unsigned)w; }
;     }
;     if (lane == 0) ((float*)(ws + (tbl ? WS_SV : WS_SU)))[r] = am * (1.0f / 256.0f);
	v_cvt_pk_fp8_f32 v34, v98, v99 op_sel:[0,0,1]
	v_cvt_pk_fp8_f32 v35, v102, v103 op_sel:[0,0,1]
	s_nop 0
	v_mul_f32_e32 v8, 0x3b800000, v6
	global_store_dword v2, v20, s[8:9]
	global_store_dword v2, v21, s[8:9] offset:256
	global_store_dword v2, v22, s[8:9] offset:512
	global_store_dword v2, v23, s[8:9] offset:768
	global_store_dword v2, v24, s[8:9] offset:1024
	global_store_dword v2, v25, s[8:9] offset:1280
	global_store_dword v2, v26, s[8:9] offset:1536
	global_store_dword v2, v27, s[8:9] offset:1792
	global_store_dword v2, v28, s[8:9] offset:2048
	global_store_dword v2, v29, s[8:9] offset:2304
	global_store_dword v2, v30, s[8:9] offset:2560
	global_store_dword v2, v31, s[8:9] offset:2816
	global_store_dword v2, v32, s[8:9] offset:3072
	global_store_dword v2, v33, s[8:9] offset:3328
	global_store_dword v2, v34, s[8:9] offset:3584
	global_store_dword v2, v35, s[8:9] offset:3840
	s_mov_b64 s[18:19], exec
	s_mov_b64 exec, s[12:13]
	global_store_dword v10, v8, s[10:11]
	s_mov_b64 exec, s[18:19]
	s_mov_b32 s4, s5
	s_add_i32 s5, s4, 1024
	s_lshl_b32 s1, s5, 14
	s_add_u32 s6, s84, s1
	s_addc_u32 s7, s85, 0
	global_load_dwordx4 v[40:43], v1, s[6:7]
	global_load_dwordx4 v[44:47], v1, s[6:7] offset:1024
	global_load_dwordx4 v[48:51], v1, s[6:7] offset:2048
	global_load_dwordx4 v[52:55], v1, s[6:7] offset:3072
	global_load_dwordx4 v[56:59], v3, s[6:7]
	global_load_dwordx4 v[60:63], v3, s[6:7] offset:1024
	global_load_dwordx4 v[64:67], v3, s[6:7] offset:2048
	global_load_dwordx4 v[68:71], v3, s[6:7] offset:3072
	global_load_dwordx4 v[72:75], v4, s[6:7]
	global_load_dwordx4 v[76:79], v4, s[6:7] offset:1024
	global_load_dwordx4 v[80:83], v4, s[6:7] offset:2048
	global_load_dwordx4 v[84:87], v4, s[6:7] offset:3072
	global_load_dwordx4 v[88:91], v5, s[6:7]
	global_load_dwordx4 v[92:95], v5, s[6:7] offset:1024
	global_load_dwordx4 v[96:99], v5, s[6:7] offset:2048
	global_load_dwordx4 v[100:103], v5, s[6:7] offset:3072
	s_waitcnt vmcnt(48)
	v_max3_f32 v6, |v104|, |v105|, 0
	v_max3_f32 v6, |v106|, |v107|, v6
	s_waitcnt vmcnt(47)
	v_max3_f32 v6, |v108|, |v109|, v6
	v_max3_f32 v6, |v110|, |v111|, v6
	s_waitcnt vmcnt(46)
	v_max3_f32 v6, |v112|, |v113|, v6
	v_max3_f32 v6, |v114|, |v115|, v6
	s_waitcnt vmcnt(45)
	v_max3_f32 v6, |v116|, |v117|, v6
	v_max3_f32 v6, |v118|, |v119|, v6
	s_waitcnt vmcnt(44)
	v_max3_f32 v6, |v120|, |v121|, v6
	v_max3_f32 v6, |v122|, |v123|, v6
	s_waitcnt vmcnt(43)
	v_max3_f32 v6, |v124|, |v125|, v6
	v_max3_f32 v6, |v126|, |v127|, v6
	s_waitcnt vmcnt(42)
	v_max3_f32 v6, |v128|, |v129|, v6
	v_max3_f32 v6, |v130|, |v131|, v6
	s_waitcnt vmcnt(41)
	v_max3_f32 v6, |v132|, |v133|, v6
	v_max3_f32 v6, |v134|, |v135|, v6
	s_waitcnt vmcnt(40)
	v_max3_f32 v6, |v136|, |v137|, v6
	v_max3_f32 v6, |v138|, |v139|, v6
	s_waitcnt vmcnt(39)
	v_max3_f32 v6, |v140|, |v141|, v6
	v_max3_f32 v6, |v142|, |v143|, v6
	s_waitcnt vmcnt(38)
	v_max3_f32 v6, |v144|, |v145|, v6
	v_max3_f32 v6, |v146|, |v147|, v6
	s_waitcnt vmcnt(37)
	v_max3_f32 v6, |v148|, |v149|, v6
	v_max3_f32 v6, |v150|, |v151|, v6
	s_waitcnt vmcnt(36)
	v_max3_f32 v6, |v152|, |v153|, v6
	v_max3_f32 v6, |v154|, |v155|, v6
	s_waitcnt vmcnt(35)
	v_max3_f32 v6, |v156|, |v157|, v6
	v_max3_f32 v6, |v158|, |v159|, v6
	s_waitcnt vmcnt(34)
	v_max3_f32 v6, |v160|, |v161|, v6
	v_max3_f32 v6, |v162|, |v163|, v6
	s_waitcnt vmcnt(33)
	v_max3_f32 v6, |v164|, |v165|, v6
	v_max3_f32 v6, |v166|, |v167|, v6
	s_nop 1
	v_max_u32_dpp v6, v6, v6 quad_perm:[1,0,3,2] row_mask:0xf bank_mask:0xf bound_ctrl:1
	s_nop 1
	v_max_u32_dpp v6, v6, v6 quad_perm:[2,3,0,1] row_mask:0xf bank_mask:0xf bound_ctrl:1
	s_nop 1
	v_max_u32_dpp v6, v6, v6 row_half_mirror row_mask:0xf bank_mask:0xf bound_ctrl:1
	s_nop 1
	v_max_u32_dpp v6, v6, v6 row_mirror row_mask:0xf bank_mask:0xf bound_ctrl:1
	s_nop 1
	v_mov_b32_e32 v7, v6
	s_nop 1
	v_permlane16_swap_b32_e32 v6, v7
	v_max_u32_e32 v6, v6, v7
	v_mov_b32_e32 v7, v6
	s_nop 1
	v_permlane32_swap_b32_e32 v6, v7
	v_max_u32_e32 v6, v6, v7
	v_div_scale_f32 v12, s[16:17], v6, v6, s14
	v_rcp_f32_e32 v13, v12
	s_nop 0
	v_fma_f32 v14, -v12, v13, 1.0
	v_fmac_f32_e32 v13, v14, v13
	v_div_scale_f32 v14, vcc, s14, v6, s14
	v_mul_f32_e32 v15, v14, v13
	v_fma_f32 v16, -v12, v15, v14
	v_fmac_f32_e32 v15, v16, v13
	v_fma_f32 v12, -v12, v15, v14
	v_div_fmas_f32 v12, v12, v13, v15
	v_div_fixup_f32 v9, v12, v6, s14
	v_cmp_lt_f32_e32 vcc, 0, v6
	s_nop 1
	v_cndmask_b32_e32 v9, 0, v9, vcc
	s_lshl_b32 s1, s4, 12
	s_add_u32 s8, s90, 0xba00000
	s_addc_u32 s9, s91, 0
	s_add_u32 s8, s8, s1
	s_addc_u32 s9, s9, 0
	s_lshl_b32 s1, s4, 2
	s_add_u32 s10, s90, 0x1ba00000
	s_addc_u32 s11, s91, 0
	s_add_u32 s10, s10, s1
	s_addc_u32 s11, s11, 0
	v_mul_f32_e32 v104, v104, v9
	v_mul_f32_e32 v105, v105, v9
	v_mul_f32_e32 v106, v106, v9
	v_mul_f32_e32 v107, v107, v9
	v_mov_b32_e32 v20, v10
	v_cvt_pk_fp8_f32 v20, v104, v105
	v_mul_f32_e32 v108, v108, v9
	v_mul_f32_e32 v109, v109, v9
	v_mul_f32_e32 v110, v110, v9
	v_mul_f32_e32 v111, v111, v9
	v_mov_b32_e32 v21, v10
	v_cvt_pk_fp8_f32 v21, v108, v109
	v_cvt_pk_fp8_f32 v20, v106, v107 op_sel:[0,0,1]
	v_mul_f32_e32 v112, v112, v9
	v_mul_f32_e32 v113, v113, v9
	v_mul_f32_e32 v114, v114, v9
	v_mul_f32_e32 v115, v115, v9
	v_mov_b32_e32 v22, v10
	v_cvt_pk_fp8_f32 v22, v112, v113
	v_cvt_pk_fp8_f32 v21, v110, v111 op_sel:[0,0,1]
	v_mul_f32_e32 v116, v116, v9
	v_mul_f32_e32 v117, v117, v9
	v_mul_f32_e32 v118, v118, v9
	v_mul_f32_e32 v119, v119, v9
	v_mov_b32_e32 v23, v10
	v_cvt_pk_fp8_f32 v23, v116, v117
	v_cvt_pk_fp8_f32 v22, v114, v115 op_sel:[0,0,1]
	v_mul_f32_e32 v120, v120, v9
	v_mul_f32_e32 v121, v121, v9
	v_mul_f32_e32 v122, v122, v9
	v_mul_f32_e32 v123, v123, v9
	v_mov_b32_e32 v24, v10
; __device__ __forceinline__ void peer_row_load(f32x4 (&v)[16], const float* const (&in)[34], int it, int layer, int lane) {
;     const int tbl = it >= NEXP, r = it - tbl * NEXP + layer * NEXP;
;     const f32x4* src = (const f32x4*)((tbl ? in[33] : in[32]) + (size_t)r * D) + lane;
; #pragma unroll
;     for (int j = 0; j < 16; ++j) v[j] = src[64 * j];
; }
; __device__ __forceinline__ void peer_row_store(const f32x4 (&v)[16], unsigned char* ws, int it, int layer, int lane) {
;     const int tbl = it >= NEXP, r = it - tbl * NEXP + layer * NEXP;
;     float am = 0.f;
; #pragma unroll
;     for (int j = 0; j < 16; ++j) am = fmaxf(fmaxf(am, fmaxf(fabsf(v[j][0]), fabsf(v[j][1]))), fmaxf(fabsf(v[j][2]), fabsf(v[j][3])));
;     am = __uint_as_float(max64u(__float_as_uint(am)));
;     const float q = am > 0.f ? 256.0f / am : 0.f;
;     unsigned* dst = (unsigned*)(ws + (tbl ? WS_PV : WS_PU) + (size_t)r * D) + lane;
;     if (tbl) {
;         const int rl = it - NEXP;
;         unsigned char* pvl = ws + WS_PV + (size_t)layer * NEXP * D + (size_t)rl * 8 + (lane & 1) * 4;
;         unsigned char* pvg = ws + WS_PV + (size_t)layer * NEXP * D + (size_t)NEXP * 2048 + (size_t)rl * 2048 + 4 * lane;
; #pragma unroll
;         for (int j = 0; j < 16; ++j) { int w = __builtin_amdgcn_cvt_pk_bf8_f32(v[j][0] * q, v[j][1] * q, 0, false); w = __builtin_amdgcn_cvt_pk_bf8_f32(v[j][2] * q, v[j][3] * q, w, true);
;             if (j < 8) *(unsigned*)(pvl + (size_t)((lane >> 1) + 32 * j) * (NEXP * 8)) = (unsigned)w;
;             else *(unsigned*)(pvg + 256 * (j - 8)) = (unsigned)w; }
;     } else {
; #pragma unroll
;         for (int j = 0; j < 16; ++j) { int w = __builtin_amdgcn_cvt_pk_fp8_f32(v[j][0] * q, v[j][1] * q, 0, false); w = __builtin_amdgcn_cvt_pk_fp8_f32(v[j][2] * q, v[j][3] * q, w, true); dst[64 * j] = (unsigned)w; }
;     }
;     if (lane == 0) ((float*)(ws + (tbl ? WS_SV : WS_SU)))[r] = am * (1.0f / 256.0f);
	v_cvt_pk_fp8_f32 v24, v120, v121
	v_cvt_pk_fp8_f32 v23, v118, v119 op_sel:[0,0,1]
	v_mul_f32_e32 v124, v124, v9
	v_mul_f32_e32 v125, v125, v9
	v_mul_f32_e32 v126, v126, v9
	v_mul_f32_e32 v127, v127, v9
	v_mov_b32_e32 v25, v10
	v_cvt_pk_fp8_f32 v25, v124, v125
	v_cvt_pk_fp8_f32 v24, v122, v123 op_sel:[0,0,1]
	v_mul_f32_e32 v128, v128, v9
	v_mul_f32_e32 v129, v129, v9
	v_mul_f32_e32 v130, v130, v9
	v_mul_f32_e32 v131, v131, v9
	v_mov_b32_e32 v26, v10
	v_cvt_pk_fp8_f32 v26, v128, v129
	v_cvt_pk_fp8_f32 v25, v126, v127 op_sel:[0,0,1]
	v_mul_f32_e32 v132, v132, v9
	v_mul_f32_e32 v133, v133, v9
	v_mul_f32_e32 v134, v134, v9
	v_mul_f32_e32 v135, v135, v9
	v_mov_b32_e32 v27, v10
	v_cvt_pk_fp8_f32 v27, v132, v133
	v_cvt_pk_fp8_f32 v26, v130, v131 op_sel:[0,0,1]
	v_mul_f32_e32 v136, v136, v9
	v_mul_f32_e32 v137, v137, v9
	v_mul_f32_e32 v138, v138, v9
	v_mul_f32_e32 v139, v139, v9
	v_mov_b32_e32 v28, v10
	v_cvt_pk_fp8_f32 v28, v136, v137
	v_cvt_pk_fp8_f32 v27, v134, v135 op_sel:[0,0,1]
	v_mul_f32_e32 v140, v140, v9
	v_mul_f32_e32 v141, v141, v9
	v_mul_f32_e32 v142, v142, v9
	v_mul_f32_e32 v143, v143, v9
	v_mov_b32_e32 v29, v10
	v_cvt_pk_fp8_f32 v29, v140, v141
	v_cvt_pk_fp8_f32 v28, v138, v139 op_sel:[0,0,1]
	v_mul_f32_e32 v144, v144, v9
	v_mul_f32_e32 v145, v145, v9
	v_mul_f32_e32 v146, v146, v9
	v_mul_f32_e32 v147, v147, v9
	v_mov_b32_e32 v30, v10
	v_cvt_pk_fp8_f32 v30, v144, v145
	v_cvt_pk_fp8_f32 v29, v142, v143 op_sel:[0,0,1]
	v_mul_f32_e32 v148, v148, v9
	v_mul_f32_e32 v149, v149, v9
	v_mul_f32_e32 v150, v150, v9
	v_mul_f32_e32 v151, v151, v9
	v_mov_b32_e32 v31, v10
	v_cvt_pk_fp8_f32 v31, v148, v149
	v_cvt_pk_fp8_f32 v30, v146, v147 op_sel:[0,0,1]
	v_mul_f32_e32 v152, v152, v9
	v_mul_f32_e32 v153, v153, v9
	v_mul_f32_e32 v154, v154, v9
	v_mul_f32_e32 v155, v155, v9
	v_mov_b32_e32 v32, v10
	v_cvt_pk_fp8_f32 v32, v152, v153
	v_cvt_pk_fp8_f32 v31, v150, v151 op_sel:[0,0,1]
	v_mul_f32_e32 v156, v156, v9
	v_mul_f32_e32 v157, v157, v9
	v_mul_f32_e32 v158, v158, v9
	v_mul_f32_e32 v159, v159, v9
	v_mov_b32_e32 v33, v10
	v_cvt_pk_fp8_f32 v33, v156, v157
	v_cvt_pk_fp8_f32 v32, v154, v155 op_sel:[0,0,1]
	v_mul_f32_e32 v160, v160, v9
	v_mul_f32_e32 v161, v161, v9
	v_mul_f32_e32 v162, v162, v9
	v_mul_f32_e32 v163, v163, v9
	v_mov_b32_e32 v34, v10
	v_cvt_pk_fp8_f32 v34, v160, v161
	v_cvt_pk_fp8_f32 v33, v158, v159 op_sel:[0,0,1]
	v_mul_f32_e32 v164, v164, v9
	v_mul_f32_e32 v165, v165, v9
	v_mul_f32_e32 v166, v166, v9
	v_mul_f32_e32 v167, v167, v9
	v_mov_b32_e32 v35, v10
	v_cvt_pk_fp8_f32 v35, v164, v165
	v_cvt_pk_fp8_f32 v34, v162, v163 op_sel:[0,0,1]
	v_cvt_pk_fp8_f32 v35, v166, v167 op_sel:[0,0,1]
	s_nop 0
	v_mul_f32_e32 v8, 0x3b800000, v6
	global_store_dword v2, v20, s[8:9]
	global_store_dword v2, v21, s[8:9] offset:256
	global_store_dword v2, v22, s[8:9] offset:512
	global_store_dword v2, v23, s[8:9] offset:768
	global_store_dword v2, v24, s[8:9] offset:1024
	global_store_dword v2, v25, s[8:9] offset:1280
	global_store_dword v2, v26, s[8:9] offset:1536
	global_store_dword v2, v27, s[8:9] offset:1792
	global_store_dword v2, v28, s[8:9] offset:2048
	global_store_dword v2, v29, s[8:9] offset:2304
	global_store_dword v2, v30, s[8:9] offset:2560
	global_store_dword v2, v31, s[8:9] offset:2816
	global_store_dword v2, v32, s[8:9] offset:3072
	global_store_dword v2, v33, s[8:9] offset:3328
	global_store_dword v2, v34, s[8:9] offset:3584
	global_store_dword v2, v35, s[8:9] offset:3840
	s_mov_b64 s[18:19], exec
	s_mov_b64 exec, s[12:13]
	global_store_dword v10, v8, s[10:11]
	s_mov_b64 exec, s[18:19]
	s_mov_b32 s4, s5
	s_add_i32 s5, s4, 1024
	s_lshl_b32 s1, s5, 14
	s_add_u32 s6, s84, s1
	s_addc_u32 s7, s85, 0
	global_load_dwordx4 v[104:107], v1, s[6:7]
	global_load_dwordx4 v[108:111], v1, s[6:7] offset:1024
	global_load_dwordx4 v[112:115], v1, s[6:7] offset:2048
	global_load_dwordx4 v[116:119], v1, s[6:7] offset:3072
	global_load_dwordx4 v[120:123], v3, s[6:7]
	global_load_dwordx4 v[124:127], v3, s[6:7] offset:1024
	global_load_dwordx4 v[128:131], v3, s[6:7] offset:2048
	global_load_dwordx4 v[132:135], v3, s[6:7] offset:3072
	global_load_dwordx4 v[136:139], v4, s[6:7]
	global_load_dwordx4 v[140:143], v4, s[6:7] offset:1024
	global_load_dwordx4 v[144:147], v4, s[6:7] offset:2048
	global_load_dwordx4 v[148:151], v4, s[6:7] offset:3072
	global_load_dwordx4 v[152:155], v5, s[6:7]
	global_load_dwordx4 v[156:159], v5, s[6:7] offset:1024
	global_load_dwordx4 v[160:163], v5, s[6:7] offset:2048
	global_load_dwordx4 v[164:167], v5, s[6:7] offset:3072
	s_waitcnt vmcnt(48)
	v_max3_f32 v6, |v40|, |v41|, 0
	v_max3_f32 v6, |v42|, |v43|, v6
	s_waitcnt vmcnt(47)
	v_max3_f32 v6, |v44|, |v45|, v6
	v_max3_f32 v6, |v46|, |v47|, v6
	s_waitcnt vmcnt(46)
	v_max3_f32 v6, |v48|, |v49|, v6
	v_max3_f32 v6, |v50|, |v51|, v6
	s_waitcnt vmcnt(45)
	v_max3_f32 v6, |v52|, |v53|, v6
	v_max3_f32 v6, |v54|, |v55|, v6
	s_waitcnt vmcnt(44)
	v_max3_f32 v6, |v56|, |v57|, v6
	v_max3_f32 v6, |v58|, |v59|, v6
	s_waitcnt vmcnt(43)
	v_max3_f32 v6, |v60|, |v61|, v6
	v_max3_f32 v6, |v62|, |v63|, v6
	s_waitcnt vmcnt(42)
	v_max3_f32 v6, |v64|, |v65|, v6
	v_max3_f32 v6, |v66|, |v67|, v6
	s_waitcnt vmcnt(41)
	v_max3_f32 v6, |v68|, |v69|, v6
	v_max3_f32 v6, |v70|, |v71|, v6
	s_waitcnt vmcnt(40)
	v_max3_f32 v6, |v72|, |v73|, v6
	v_max3_f32 v6, |v74|, |v75|, v6
	s_waitcnt vmcnt(39)
	v_max3_f32 v6, |v76|, |v77|, v6
	v_max3_f32 v6, |v78|, |v79|, v6
	s_waitcnt vmcnt(38)
	v_max3_f32 v6, |v80|, |v81|, v6
	v_max3_f32 v6, |v82|, |v83|, v6
	s_waitcnt vmcnt(37)
	v_max3_f32 v6, |v84|, |v85|, v6
	v_max3_f32 v6, |v86|, |v87|, v6
	s_waitcnt vmcnt(36)
	v_max3_f32 v6, |v88|, |v89|, v6
	v_max3_f32 v6, |v90|, |v91|, v6
	s_waitcnt vmcnt(35)
; __device__ __forceinline__ void peer_row_load(f32x4 (&v)[16], const float* const (&in)[34], int it, int layer, int lane) {
;     const int tbl = it >= NEXP, r = it - tbl * NEXP + layer * NEXP;
;     const f32x4* src = (const f32x4*)((tbl ? in[33] : in[32]) + (size_t)r * D) + lane;
; #pragma unroll
;     for (int j = 0; j < 16; ++j) v[j] = src[64 * j];
; }
; __device__ __forceinline__ void peer_row_store(const f32x4 (&v)[16], unsigned char* ws, int it, int layer, int lane) {
;     const int tbl = it >= NEXP, r = it - tbl * NEXP + layer * NEXP;
;     float am = 0.f;
; #pragma unroll
;     for (int j = 0; j < 16; ++j) am = fmaxf(fmaxf(am, fmaxf(fabsf(v[j][0]), fabsf(v[j][1]))), fmaxf(fabsf(v[j][2]), fabsf(v[j][3])));
;     am = __uint_as_float(max64u(__float_as_uint(am)));
;     const float q = am > 0.f ? 256.0f / am : 0.f;
;     unsigned* dst = (unsigned*)(ws + (tbl ? WS_PV : WS_PU) + (size_t)r * D) + lane;
;     if (tbl) {
;         const int rl = it - NEXP;
;         unsigned char* pvl = ws + WS_PV + (size_t)layer * NEXP * D + (size_t)rl * 8 + (lane & 1) * 4;
;         unsigned char* pvg = ws + WS_PV + (size_t)layer * NEXP * D + (size_t)NEXP * 2048 + (size_t)rl * 2048 + 4 * lane;
; #pragma unroll
;         for (int j = 0; j < 16; ++j) { int w = __builtin_amdgcn_cvt_pk_bf8_f32(v[j][0] * q, v[j][1] * q, 0, false); w = __builtin_amdgcn_cvt_pk_bf8_f32(v[j][2] * q, v[j][3] * q, w, true);
;             if (j < 8) *(unsigned*)(pvl + (size_t)((lane >> 1) + 32 * j) * (NEXP * 8)) = (unsigned)w;
;             else *(unsigned*)(pvg + 256 * (j - 8)) = (unsigned)w; }
;     } else {
; #pragma unroll
;         for (int j = 0; j < 16; ++j) { int w = __builtin_amdgcn_cvt_pk_fp8_f32(v[j][0] * q, v[j][1] * q, 0, false); w = __builtin_amdgcn_cvt_pk_fp8_f32(v[j][2] * q, v[j][3] * q, w, true); dst[64 * j] = (unsigned)w; }
;     }
;     if (lane == 0) ((float*)(ws + (tbl ? WS_SV : WS_SU)))[r] = am * (1.0f / 256.0f);
	v_max3_f32 v6, |v92|, |v93|, v6
	v_max3_f32 v6, |v94|, |v95|, v6
	s_waitcnt vmcnt(34)
	v_max3_f32 v6, |v96|, |v97|, v6
	v_max3_f32 v6, |v98|, |v99|, v6
	s_waitcnt vmcnt(33)
	v_max3_f32 v6, |v100|, |v101|, v6
	v_max3_f32 v6, |v102|, |v103|, v6
	s_nop 1
	v_max_u32_dpp v6, v6, v6 quad_perm:[1,0,3,2] row_mask:0xf bank_mask:0xf bound_ctrl:1
	s_nop 1
	v_max_u32_dpp v6, v6, v6 quad_perm:[2,3,0,1] row_mask:0xf bank_mask:0xf bound_ctrl:1
	s_nop 1
	v_max_u32_dpp v6, v6, v6 row_half_mirror row_mask:0xf bank_mask:0xf bound_ctrl:1
	s_nop 1
	v_max_u32_dpp v6, v6, v6 row_mirror row_mask:0xf bank_mask:0xf bound_ctrl:1
	s_nop 1
	v_mov_b32_e32 v7, v6
	s_nop 1
	v_permlane16_swap_b32_e32 v6, v7
	v_max_u32_e32 v6, v6, v7
	v_mov_b32_e32 v7, v6
	s_nop 1
	v_permlane32_swap_b32_e32 v6, v7
	v_max_u32_e32 v6, v6, v7
	v_div_scale_f32 v12, s[16:17], v6, v6, s14
	v_rcp_f32_e32 v13, v12
	s_nop 0
	v_fma_f32 v14, -v12, v13, 1.0
	v_fmac_f32_e32 v13, v14, v13
	v_div_scale_f32 v14, vcc, s14, v6, s14
	v_mul_f32_e32 v15, v14, v13
	v_fma_f32 v16, -v12, v15, v14
	v_fmac_f32_e32 v15, v16, v13
	v_fma_f32 v12, -v12, v15, v14
	v_div_fmas_f32 v12, v12, v13, v15
	v_div_fixup_f32 v9, v12, v6, s14
	v_cmp_lt_f32_e32 vcc, 0, v6
	s_nop 1
	v_cndmask_b32_e32 v9, 0, v9, vcc
	s_lshl_b32 s1, s4, 12
	s_add_u32 s8, s90, 0xba00000
	s_addc_u32 s9, s91, 0
	s_add_u32 s8, s8, s1
	s_addc_u32 s9, s9, 0
	s_lshl_b32 s1, s4, 2
	s_add_u32 s10, s90, 0x1ba00000
	s_addc_u32 s11, s91, 0
	s_add_u32 s10, s10, s1
	s_addc_u32 s11, s11, 0
	v_mul_f32_e32 v40, v40, v9
	v_mul_f32_e32 v41, v41, v9
	v_mul_f32_e32 v42, v42, v9
	v_mul_f32_e32 v43, v43, v9
	v_mov_b32_e32 v20, v10
	v_cvt_pk_fp8_f32 v20, v40, v41
	v_mul_f32_e32 v44, v44, v9
	v_mul_f32_e32 v45, v45, v9
	v_mul_f32_e32 v46, v46, v9
	v_mul_f32_e32 v47, v47, v9
	v_mov_b32_e32 v21, v10
	v_cvt_pk_fp8_f32 v21, v44, v45
	v_cvt_pk_fp8_f32 v20, v42, v43 op_sel:[0,0,1]
	v_mul_f32_e32 v48, v48, v9
	v_mul_f32_e32 v49, v49, v9
	v_mul_f32_e32 v50, v50, v9
	v_mul_f32_e32 v51, v51, v9
	v_mov_b32_e32 v22, v10
	v_cvt_pk_fp8_f32 v22, v48, v49
	v_cvt_pk_fp8_f32 v21, v46, v47 op_sel:[0,0,1]
	v_mul_f32_e32 v52, v52, v9
	v_mul_f32_e32 v53, v53, v9
	v_mul_f32_e32 v54, v54, v9
	v_mul_f32_e32 v55, v55, v9
	v_mov_b32_e32 v23, v10
	v_cvt_pk_fp8_f32 v23, v52, v53
	v_cvt_pk_fp8_f32 v22, v50, v51 op_sel:[0,0,1]
	v_mul_f32_e32 v56, v56, v9
	v_mul_f32_e32 v57, v57, v9
	v_mul_f32_e32 v58, v58, v9
	v_mul_f32_e32 v59, v59, v9
	v_mov_b32_e32 v24, v10
	v_cvt_pk_fp8_f32 v24, v56, v57
	v_cvt_pk_fp8_f32 v23, v54, v55 op_sel:[0,0,1]
	v_mul_f32_e32 v60, v60, v9
	v_mul_f32_e32 v61, v61, v9
	v_mul_f32_e32 v62, v62, v9
	v_mul_f32_e32 v63, v63, v9
	v_mov_b32_e32 v25, v10
	v_cvt_pk_fp8_f32 v25, v60, v61
	v_cvt_pk_fp8_f32 v24, v58, v59 op_sel:[0,0,1]
	v_mul_f32_e32 v64, v64, v9
	v_mul_f32_e32 v65, v65, v9
	v_mul_f32_e32 v66, v66, v9
	v_mul_f32_e32 v67, v67, v9
	v_mov_b32_e32 v26, v10
	v_cvt_pk_fp8_f32 v26, v64, v65
	v_cvt_pk_fp8_f32 v25, v62, v63 op_sel:[0,0,1]
	v_mul_f32_e32 v68, v68, v9
	v_mul_f32_e32 v69, v69, v9
	v_mul_f32_e32 v70, v70, v9
	v_mul_f32_e32 v71, v71, v9
	v_mov_b32_e32 v27, v10
	v_cvt_pk_fp8_f32 v27, v68, v69
	v_cvt_pk_fp8_f32 v26, v66, v67 op_sel:[0,0,1]
	v_mul_f32_e32 v72, v72, v9
	v_mul_f32_e32 v73, v73, v9
	v_mul_f32_e32 v74, v74, v9
	v_mul_f32_e32 v75, v75, v9
	v_mov_b32_e32 v28, v10
	v_cvt_pk_fp8_f32 v28, v72, v73
	v_cvt_pk_fp8_f32 v27, v70, v71 op_sel:[0,0,1]
	v_mul_f32_e32 v76, v76, v9
	v_mul_f32_e32 v77, v77, v9
	v_mul_f32_e32 v78, v78, v9
	v_mul_f32_e32 v79, v79, v9
	v_mov_b32_e32 v29, v10
	v_cvt_pk_fp8_f32 v29, v76, v77
	v_cvt_pk_fp8_f32 v28, v74, v75 op_sel:[0,0,1]
	v_mul_f32_e32 v80, v80, v9
	v_mul_f32_e32 v81, v81, v9
	v_mul_f32_e32 v82, v82, v9
	v_mul_f32_e32 v83, v83, v9
	v_mov_b32_e32 v30, v10
	v_cvt_pk_fp8_f32 v30, v80, v81
	v_cvt_pk_fp8_f32 v29, v78, v79 op_sel:[0,0,1]
	v_mul_f32_e32 v84, v84, v9
	v_mul_f32_e32 v85, v85, v9
	v_mul_f32_e32 v86, v86, v9
	v_mul_f32_e32 v87, v87, v9
	v_mov_b32_e32 v31, v10
	v_cvt_pk_fp8_f32 v31, v84, v85
	v_cvt_pk_fp8_f32 v30, v82, v83 op_sel:[0,0,1]
	v_mul_f32_e32 v88, v88, v9
	v_mul_f32_e32 v89, v89, v9
	v_mul_f32_e32 v90, v90, v9
	v_mul_f32_e32 v91, v91, v9
	v_mov_b32_e32 v32, v10
	v_cvt_pk_fp8_f32 v32, v88, v89
	v_cvt_pk_fp8_f32 v31, v86, v87 op_sel:[0,0,1]
	v_mul_f32_e32 v92, v92, v9
	v_mul_f32_e32 v93, v93, v9
	v_mul_f32_e32 v94, v94, v9
	v_mul_f32_e32 v95, v95, v9
	v_mov_b32_e32 v33, v10
	v_cvt_pk_fp8_f32 v33, v92, v93
	v_cvt_pk_fp8_f32 v32, v90, v91 op_sel:[0,0,1]
	v_mul_f32_e32 v96, v96, v9
	v_mul_f32_e32 v97, v97, v9
	v_mul_f32_e32 v98, v98, v9
	v_mul_f32_e32 v99, v99, v9
	v_mov_b32_e32 v34, v10
	v_cvt_pk_fp8_f32 v34, v96, v97
	v_cvt_pk_fp8_f32 v33, v94, v95 op_sel:[0,0,1]
	v_mul_f32_e32 v100, v100, v9
	v_mul_f32_e32 v101, v101, v9
	v_mul_f32_e32 v102, v102, v9
	v_mul_f32_e32 v103, v103, v9
	v_mov_b32_e32 v35, v10
	v_cvt_pk_fp8_f32 v35, v100, v101
	v_cvt_pk_fp8_f32 v34, v98, v99 op_sel:[0,0,1]
	v_cvt_pk_fp8_f32 v35, v102, v103 op_sel:[0,0,1]
	s_nop 0
	v_mul_f32_e32 v8, 0x3b800000, v6
	global_store_dword v2, v20, s[8:9]
	global_store_dword v2, v21, s[8:9] offset:256
	global_store_dword v2, v22, s[8:9] offset:512
	global_store_dword v2, v23, s[8:9] offset:768
	global_store_dword v2, v24, s[8:9] offset:1024
	global_store_dword v2, v25, s[8:9] offset:1280
	global_store_dword v2, v26, s[8:9] offset:1536
	global_store_dword v2, v27, s[8:9] offset:1792
	global_store_dword v2, v28, s[8:9] offset:2048
	global_store_dword v2, v29, s[8:9] offset:2304
	global_store_dword v2, v30, s[8:9] offset:2560
	global_store_dword v2, v31, s[8:9] offset:2816
	global_store_dword v2, v32, s[8:9] offset:3072
	global_store_dword v2, v33, s[8:9] offset:3328
	global_store_dword v2, v34, s[8:9] offset:3584
	global_store_dword v2, v35, s[8:9] offset:3840
	s_mov_b64 s[18:19], exec
	s_mov_b64 exec, s[12:13]
	global_store_dword v10, v8, s[10:11]
	s_mov_b64 exec, s[18:19]
	s_mov_b32 s4, s5
	s_add_i32 s5, s4, 1024
	s_lshl_b32 s1, s5, 14
	s_add_u32 s6, s84, s1
	s_addc_u32 s7, s85, 0
	global_load_dwordx4 v[40:43], v1, s[6:7]
	global_load_dwordx4 v[44:47], v1, s[6:7] offset:1024
	global_load_dwordx4 v[48:51], v1, s[6:7] offset:2048
	global_load_dwordx4 v[52:55], v1, s[6:7] offset:3072
	global_load_dwordx4 v[56:59], v3, s[6:7]
	global_load_dwordx4 v[60:63], v3, s[6:7] offset:1024
	global_load_dwordx4 v[64:67], v3, s[6:7] offset:2048
	global_load_dwordx4 v[68:71], v3, s[6:7] offset:3072
	global_load_dwordx4 v[72:75], v4, s[6:7]
	global_load_dwordx4 v[76:79], v4, s[6:7] offset:1024
	global_load_dwordx4 v[80:83], v4, s[6:7] offset:2048
	global_load_dwordx4 v[84:87], v4, s[6:7] offset:3072
	global_load_dwordx4 v[88:91], v5, s[6:7]
	global_load_dwordx4 v[92:95], v5, s[6:7] offset:1024
	global_load_dwordx4 v[96:99], v5, s[6:7] offset:2048
	global_load_dwordx4 v[100:103], v5, s[6:7] offset:3072
	s_waitcnt vmcnt(48)
; __device__ __forceinline__ void peer_row_load(f32x4 (&v)[16], const float* const (&in)[34], int it, int layer, int lane) {
;     const int tbl = it >= NEXP, r = it - tbl * NEXP + layer * NEXP;
;     const f32x4* src = (const f32x4*)((tbl ? in[33] : in[32]) + (size_t)r * D) + lane;
; #pragma unroll
;     for (int j = 0; j < 16; ++j) v[j] = src[64 * j];
; }
; __device__ __forceinline__ void peer_row_store(const f32x4 (&v)[16], unsigned char* ws, int it, int layer, int lane) {
;     const int tbl = it >= NEXP, r = it - tbl * NEXP + layer * NEXP;
;     float am = 0.f;
; #pragma unroll
;     for (int j = 0; j < 16; ++j) am = fmaxf(fmaxf(am, fmaxf(fabsf(v[j][0]), fabsf(v[j][1]))), fmaxf(fabsf(v[j][2]), fabsf(v[j][3])));
;     am = __uint_as_float(max64u(__float_as_uint(am)));
;     const float q = am > 0.f ? 256.0f / am : 0.f;
;     unsigned* dst = (unsigned*)(ws + (tbl ? WS_PV : WS_PU) + (size_t)r * D) + lane;
;     if (tbl) {
;         const int rl = it - NEXP;
;         unsigned char* pvl = ws + WS_PV + (size_t)layer * NEXP * D + (size_t)rl * 8 + (lane & 1) * 4;
;         unsigned char* pvg = ws + WS_PV + (size_t)layer * NEXP * D + (size_t)NEXP * 2048 + (size_t)rl * 2048 + 4 * lane;
; #pragma unroll
;         for (int j = 0; j < 16; ++j) { int w = __builtin_amdgcn_cvt_pk_bf8_f32(v[j][0] * q, v[j][1] * q, 0, false); w = __builtin_amdgcn_cvt_pk_bf8_f32(v[j][2] * q, v[j][3] * q, w, true);
;             if (j < 8) *(unsigned*)(pvl + (size_t)((lane >> 1) + 32 * j) * (NEXP * 8)) = (unsigned)w;
;             else *(unsigned*)(pvg + 256 * (j - 8)) = (unsigned)w; }
;     } else {
; #pragma unroll
;         for (int j = 0; j < 16; ++j) { int w = __builtin_amdgcn_cvt_pk_fp8_f32(v[j][0] * q, v[j][1] * q, 0, false); w = __builtin_amdgcn_cvt_pk_fp8_f32(v[j][2] * q, v[j][3] * q, w, true); dst[64 * j] = (unsigned)w; }
;     }
;     if (lane == 0) ((float*)(ws + (tbl ? WS_SV : WS_SU)))[r] = am * (1.0f / 256.0f);
	v_max3_f32 v6, |v104|, |v105|, 0
	v_max3_f32 v6, |v106|, |v107|, v6
	s_waitcnt vmcnt(47)
	v_max3_f32 v6, |v108|, |v109|, v6
	v_max3_f32 v6, |v110|, |v111|, v6
	s_waitcnt vmcnt(46)
	v_max3_f32 v6, |v112|, |v113|, v6
	v_max3_f32 v6, |v114|, |v115|, v6
	s_waitcnt vmcnt(45)
	v_max3_f32 v6, |v116|, |v117|, v6
	v_max3_f32 v6, |v118|, |v119|, v6
	s_waitcnt vmcnt(44)
	v_max3_f32 v6, |v120|, |v121|, v6
	v_max3_f32 v6, |v122|, |v123|, v6
	s_waitcnt vmcnt(43)
	v_max3_f32 v6, |v124|, |v125|, v6
	v_max3_f32 v6, |v126|, |v127|, v6
	s_waitcnt vmcnt(42)
	v_max3_f32 v6, |v128|, |v129|, v6
	v_max3_f32 v6, |v130|, |v131|, v6
	s_waitcnt vmcnt(41)
	v_max3_f32 v6, |v132|, |v133|, v6
	v_max3_f32 v6, |v134|, |v135|, v6
	s_waitcnt vmcnt(40)
	v_max3_f32 v6, |v136|, |v137|, v6
	v_max3_f32 v6, |v138|, |v139|, v6
	s_waitcnt vmcnt(39)
	v_max3_f32 v6, |v140|, |v141|, v6
	v_max3_f32 v6, |v142|, |v143|, v6
	s_waitcnt vmcnt(38)
	v_max3_f32 v6, |v144|, |v145|, v6
	v_max3_f32 v6, |v146|, |v147|, v6
	s_waitcnt vmcnt(37)
	v_max3_f32 v6, |v148|, |v149|, v6
	v_max3_f32 v6, |v150|, |v151|, v6
	s_waitcnt vmcnt(36)
	v_max3_f32 v6, |v152|, |v153|, v6
	v_max3_f32 v6, |v154|, |v155|, v6
	s_waitcnt vmcnt(35)
	v_max3_f32 v6, |v156|, |v157|, v6
	v_max3_f32 v6, |v158|, |v159|, v6
	s_waitcnt vmcnt(34)
	v_max3_f32 v6, |v160|, |v161|, v6
	v_max3_f32 v6, |v162|, |v163|, v6
	s_waitcnt vmcnt(33)
	v_max3_f32 v6, |v164|, |v165|, v6
	v_max3_f32 v6, |v166|, |v167|, v6
	s_nop 1
	v_max_u32_dpp v6, v6, v6 quad_perm:[1,0,3,2] row_mask:0xf bank_mask:0xf bound_ctrl:1
	s_nop 1
	v_max_u32_dpp v6, v6, v6 quad_perm:[2,3,0,1] row_mask:0xf bank_mask:0xf bound_ctrl:1
	s_nop 1
	v_max_u32_dpp v6, v6, v6 row_half_mirror row_mask:0xf bank_mask:0xf bound_ctrl:1
	s_nop 1
	v_max_u32_dpp v6, v6, v6 row_mirror row_mask:0xf bank_mask:0xf bound_ctrl:1
	s_nop 1
	v_mov_b32_e32 v7, v6
	s_nop 1
	v_permlane16_swap_b32_e32 v6, v7
	v_max_u32_e32 v6, v6, v7
	v_mov_b32_e32 v7, v6
	s_nop 1
	v_permlane32_swap_b32_e32 v6, v7
	v_max_u32_e32 v6, v6, v7
	v_div_scale_f32 v12, s[16:17], v6, v6, s14
	v_rcp_f32_e32 v13, v12
	s_nop 0
	v_fma_f32 v14, -v12, v13, 1.0
	v_fmac_f32_e32 v13, v14, v13
	v_div_scale_f32 v14, vcc, s14, v6, s14
	v_mul_f32_e32 v15, v14, v13
	v_fma_f32 v16, -v12, v15, v14
	v_fmac_f32_e32 v15, v16, v13
	v_fma_f32 v12, -v12, v15, v14
	v_div_fmas_f32 v12, v12, v13, v15
	v_div_fixup_f32 v9, v12, v6, s14
	v_cmp_lt_f32_e32 vcc, 0, v6
	s_nop 1
	v_cndmask_b32_e32 v9, 0, v9, vcc
	s_lshl_b32 s1, s4, 12
	s_add_u32 s8, s90, 0xba00000
	s_addc_u32 s9, s91, 0
	s_add_u32 s8, s8, s1
	s_addc_u32 s9, s9, 0
	s_lshl_b32 s1, s4, 2
	s_add_u32 s10, s90, 0x1ba00000
	s_addc_u32 s11, s91, 0
	s_add_u32 s10, s10, s1
	s_addc_u32 s11, s11, 0
	v_mul_f32_e32 v104, v104, v9
	v_mul_f32_e32 v105, v105, v9
	v_mul_f32_e32 v106, v106, v9
	v_mul_f32_e32 v107, v107, v9
	v_mov_b32_e32 v20, v10
	v_cvt_pk_fp8_f32 v20, v104, v105
	v_mul_f32_e32 v108, v108, v9
	v_mul_f32_e32 v109, v109, v9
	v_mul_f32_e32 v110, v110, v9
	v_mul_f32_e32 v111, v111, v9
	v_mov_b32_e32 v21, v10
	v_cvt_pk_fp8_f32 v21, v108, v109
	v_cvt_pk_fp8_f32 v20, v106, v107 op_sel:[0,0,1]
	v_mul_f32_e32 v112, v112, v9
	v_mul_f32_e32 v113, v113, v9
	v_mul_f32_e32 v114, v114, v9
	v_mul_f32_e32 v115, v115, v9
	v_mov_b32_e32 v22, v10
	v_cvt_pk_fp8_f32 v22, v112, v113
	v_cvt_pk_fp8_f32 v21, v110, v111 op_sel:[0,0,1]
	v_mul_f32_e32 v116, v116, v9
	v_mul_f32_e32 v117, v117, v9
	v_mul_f32_e32 v118, v118, v9
	v_mul_f32_e32 v119, v119, v9
	v_mov_b32_e32 v23, v10
	v_cvt_pk_fp8_f32 v23, v116, v117
	v_cvt_pk_fp8_f32 v22, v114, v115 op_sel:[0,0,1]
	v_mul_f32_e32 v120, v120, v9
	v_mul_f32_e32 v121, v121, v9
	v_mul_f32_e32 v122, v122, v9
	v_mul_f32_e32 v123, v123, v9
	v_mov_b32_e32 v24, v10
	v_cvt_pk_fp8_f32 v24, v120, v121
	v_cvt_pk_fp8_f32 v23, v118, v119 op_sel:[0,0,1]
	v_mul_f32_e32 v124, v124, v9
	v_mul_f32_e32 v125, v125, v9
	v_mul_f32_e32 v126, v126, v9
	v_mul_f32_e32 v127, v127, v9
	v_mov_b32_e32 v25, v10
	v_cvt_pk_fp8_f32 v25, v124, v125
	v_cvt_pk_fp8_f32 v24, v122, v123 op_sel:[0,0,1]
	v_mul_f32_e32 v128, v128, v9
	v_mul_f32_e32 v129, v129, v9
	v_mul_f32_e32 v130, v130, v9
	v_mul_f32_e32 v131, v131, v9
	v_mov_b32_e32 v26, v10
	v_cvt_pk_fp8_f32 v26, v128, v129
	v_cvt_pk_fp8_f32 v25, v126, v127 op_sel:[0,0,1]
	v_mul_f32_e32 v132, v132, v9
	v_mul_f32_e32 v133, v133, v9
	v_mul_f32_e32 v134, v134, v9
	v_mul_f32_e32 v135, v135, v9
	v_mov_b32_e32 v27, v10
	v_cvt_pk_fp8_f32 v27, v132, v133
	v_cvt_pk_fp8_f32 v26, v130, v131 op_sel:[0,0,1]
	v_mul_f32_e32 v136, v136, v9
	v_mul_f32_e32 v137, v137, v9
	v_mul_f32_e32 v138, v138, v9
	v_mul_f32_e32 v139, v139, v9
	v_mov_b32_e32 v28, v10
	v_cvt_pk_fp8_f32 v28, v136, v137
	v_cvt_pk_fp8_f32 v27, v134, v135 op_sel:[0,0,1]
	v_mul_f32_e32 v140, v140, v9
	v_mul_f32_e32 v141, v141, v9
	v_mul_f32_e32 v142, v142, v9
	v_mul_f32_e32 v143, v143, v9
	v_mov_b32_e32 v29, v10
	v_cvt_pk_fp8_f32 v29, v140, v141
	v_cvt_pk_fp8_f32 v28, v138, v139 op_sel:[0,0,1]
	v_mul_f32_e32 v144, v144, v9
	v_mul_f32_e32 v145, v145, v9
	v_mul_f32_e32 v146, v146, v9
	v_mul_f32_e32 v147, v147, v9
	v_mov_b32_e32 v30, v10
	v_cvt_pk_fp8_f32 v30, v144, v145
	v_cvt_pk_fp8_f32 v29, v142, v143 op_sel:[0,0,1]
	v_mul_f32_e32 v148, v148, v9
	v_mul_f32_e32 v149, v149, v9
	v_mul_f32_e32 v150, v150, v9
	v_mul_f32_e32 v151, v151, v9
	v_mov_b32_e32 v31, v10
	v_cvt_pk_fp8_f32 v31, v148, v149
	v_cvt_pk_fp8_f32 v30, v146, v147 op_sel:[0,0,1]
	v_mul_f32_e32 v152, v152, v9
	v_mul_f32_e32 v153, v153, v9
	v_mul_f32_e32 v154, v154, v9
	v_mul_f32_e32 v155, v155, v9
	v_mov_b32_e32 v32, v10
	v_cvt_pk_fp8_f32 v32, v152, v153
	v_cvt_pk_fp8_f32 v31, v150, v151 op_sel:[0,0,1]
	v_mul_f32_e32 v156, v156, v9
	v_mul_f32_e32 v157, v157, v9
; __device__ __forceinline__ unsigned max64u(unsigned x) {
;     x = umax_u(x, dppu<DPP_XOR1>(x)); x = umax_u(x, dppu<DPP_XOR2>(x)); x = umax_u(x, dppu<DPP_HMIRROR>(x)); x = umax_u(x, dppu<DPP_MIRROR>(x));
;     auto s = __builtin_amdgcn_permlane16_swap(x, x, false, false); x = umax_u(s[0], s[1]);
;     auto t = __builtin_amdgcn_permlane32_swap(x, x, false, false); return umax_u(t[0], t[1]);
; }
; __device__ __forceinline__ void peer_row_load(f32x4 (&v)[16], const float* const (&in)[34], int it, int layer, int lane) {
;     const int tbl = it >= NEXP, r = it - tbl * NEXP + layer * NEXP;
;     const f32x4* src = (const f32x4*)((tbl ? in[33] : in[32]) + (size_t)r * D) + lane;
; #pragma unroll
;     for (int j = 0; j < 16; ++j) v[j] = src[64 * j];
; }
; __device__ __forceinline__ void peer_row_store(const f32x4 (&v)[16], unsigned char* ws, int it, int layer, int lane) {
;     const int tbl = it >= NEXP, r = it - tbl * NEXP + layer * NEXP;
;     float am = 0.f;
; #pragma unroll
;     for (int j = 0; j < 16; ++j) am = fmaxf(fmaxf(am, fmaxf(fabsf(v[j][0]), fabsf(v[j][1]))), fmaxf(fabsf(v[j][2]), fabsf(v[j][3])));
;     am = __uint_as_float(max64u(__float_as_uint(am)));
;     const float q = am > 0.f ? 256.0f / am : 0.f;
;     unsigned* dst = (unsigned*)(ws + (tbl ? WS_PV : WS_PU) + (size_t)r * D) + lane;
;     if (tbl) {
;         const int rl = it - NEXP;
;         unsigned char* pvl = ws + WS_PV + (size_t)layer * NEXP * D + (size_t)rl * 8 + (lane & 1) * 4;
;         unsigned char* pvg = ws + WS_PV + (size_t)layer * NEXP * D + (size_t)NEXP * 2048 + (size_t)rl * 2048 + 4 * lane;
; #pragma unroll
;         for (int j = 0; j < 16; ++j) { int w = __builtin_amdgcn_cvt_pk_bf8_f32(v[j][0] * q, v[j][1] * q, 0, false); w = __builtin_amdgcn_cvt_pk_bf8_f32(v[j][2] * q, v[j][3] * q, w, true);
;             if (j < 8) *(unsigned*)(pvl + (size_t)((lane >> 1) + 32 * j) * (NEXP * 8)) = (unsigned)w;
;             else *(unsigned*)(pvg + 256 * (j - 8)) = (unsigned)w; }
;     } else {
; #pragma unroll
;         for (int j = 0; j < 16; ++j) { int w = __builtin_amdgcn_cvt_pk_fp8_f32(v[j][0] * q, v[j][1] * q, 0, false); w = __builtin_amdgcn_cvt_pk_fp8_f32(v[j][2] * q, v[j][3] * q, w, true); dst[64 * j] = (unsigned)w; }
;     }
;     if (lane == 0) ((float*)(ws + (tbl ? WS_SV : WS_SU)))[r] = am * (1.0f / 256.0f);
; }
	v_mul_f32_e32 v158, v158, v9
	v_mul_f32_e32 v159, v159, v9
	v_mov_b32_e32 v33, v10
	v_cvt_pk_fp8_f32 v33, v156, v157
	v_cvt_pk_fp8_f32 v32, v154, v155 op_sel:[0,0,1]
	v_mul_f32_e32 v160, v160, v9
	v_mul_f32_e32 v161, v161, v9
	v_mul_f32_e32 v162, v162, v9
	v_mul_f32_e32 v163, v163, v9
	v_mov_b32_e32 v34, v10
	v_cvt_pk_fp8_f32 v34, v160, v161
	v_cvt_pk_fp8_f32 v33, v158, v159 op_sel:[0,0,1]
	v_mul_f32_e32 v164, v164, v9
	v_mul_f32_e32 v165, v165, v9
	v_mul_f32_e32 v166, v166, v9
	v_mul_f32_e32 v167, v167, v9
	v_mov_b32_e32 v35, v10
	v_cvt_pk_fp8_f32 v35, v164, v165
	v_cvt_pk_fp8_f32 v34, v162, v163 op_sel:[0,0,1]
	v_cvt_pk_fp8_f32 v35, v166, v167 op_sel:[0,0,1]
	s_nop 0
	v_mul_f32_e32 v8, 0x3b800000, v6
	global_store_dword v2, v20, s[8:9]
	global_store_dword v2, v21, s[8:9] offset:256
	global_store_dword v2, v22, s[8:9] offset:512
	global_store_dword v2, v23, s[8:9] offset:768
	global_store_dword v2, v24, s[8:9] offset:1024
	global_store_dword v2, v25, s[8:9] offset:1280
	global_store_dword v2, v26, s[8:9] offset:1536
	global_store_dword v2, v27, s[8:9] offset:1792
	global_store_dword v2, v28, s[8:9] offset:2048
	global_store_dword v2, v29, s[8:9] offset:2304
	global_store_dword v2, v30, s[8:9] offset:2560
	global_store_dword v2, v31, s[8:9] offset:2816
	global_store_dword v2, v32, s[8:9] offset:3072
	global_store_dword v2, v33, s[8:9] offset:3328
	global_store_dword v2, v34, s[8:9] offset:3584
	global_store_dword v2, v35, s[8:9] offset:3840
	s_mov_b64 s[18:19], exec
	s_mov_b64 exec, s[12:13]
	global_store_dword v10, v8, s[10:11]
	s_mov_b64 exec, s[18:19]
	s_mov_b32 s4, s5
	s_add_i32 s5, s4, 1024
	s_lshl_b32 s1, s5, 14
	s_add_u32 s6, s84, s1
	s_addc_u32 s7, s85, 0
	global_load_dwordx4 v[104:107], v1, s[6:7]
	global_load_dwordx4 v[108:111], v1, s[6:7] offset:1024
	global_load_dwordx4 v[112:115], v1, s[6:7] offset:2048
	global_load_dwordx4 v[116:119], v1, s[6:7] offset:3072
	global_load_dwordx4 v[120:123], v3, s[6:7]
	global_load_dwordx4 v[124:127], v3, s[6:7] offset:1024
	global_load_dwordx4 v[128:131], v3, s[6:7] offset:2048
	global_load_dwordx4 v[132:135], v3, s[6:7] offset:3072
	global_load_dwordx4 v[136:139], v4, s[6:7]
	global_load_dwordx4 v[140:143], v4, s[6:7] offset:1024
	global_load_dwordx4 v[144:147], v4, s[6:7] offset:2048
	global_load_dwordx4 v[148:151], v4, s[6:7] offset:3072
	global_load_dwordx4 v[152:155], v5, s[6:7]
	global_load_dwordx4 v[156:159], v5, s[6:7] offset:1024
	global_load_dwordx4 v[160:163], v5, s[6:7] offset:2048
	global_load_dwordx4 v[164:167], v5, s[6:7] offset:3072
	s_waitcnt vmcnt(48)
	v_max3_f32 v6, |v40|, |v41|, 0
	v_max3_f32 v6, |v42|, |v43|, v6
	s_waitcnt vmcnt(47)
	v_max3_f32 v6, |v44|, |v45|, v6
	v_max3_f32 v6, |v46|, |v47|, v6
	s_waitcnt vmcnt(46)
	v_max3_f32 v6, |v48|, |v49|, v6
	v_max3_f32 v6, |v50|, |v51|, v6
	s_waitcnt vmcnt(45)
	v_max3_f32 v6, |v52|, |v53|, v6
	v_max3_f32 v6, |v54|, |v55|, v6
	s_waitcnt vmcnt(44)
	v_max3_f32 v6, |v56|, |v57|, v6
	v_max3_f32 v6, |v58|, |v59|, v6
	s_waitcnt vmcnt(43)
	v_max3_f32 v6, |v60|, |v61|, v6
	v_max3_f32 v6, |v62|, |v63|, v6
	s_waitcnt vmcnt(42)
	v_max3_f32 v6, |v64|, |v65|, v6
	v_max3_f32 v6, |v66|, |v67|, v6
	s_waitcnt vmcnt(41)
	v_max3_f32 v6, |v68|, |v69|, v6
	v_max3_f32 v6, |v70|, |v71|, v6
	s_waitcnt vmcnt(40)
	v_max3_f32 v6, |v72|, |v73|, v6
	v_max3_f32 v6, |v74|, |v75|, v6
	s_waitcnt vmcnt(39)
	v_max3_f32 v6, |v76|, |v77|, v6
	v_max3_f32 v6, |v78|, |v79|, v6
	s_waitcnt vmcnt(38)
	v_max3_f32 v6, |v80|, |v81|, v6
	v_max3_f32 v6, |v82|, |v83|, v6
	s_waitcnt vmcnt(37)
	v_max3_f32 v6, |v84|, |v85|, v6
	v_max3_f32 v6, |v86|, |v87|, v6
	s_waitcnt vmcnt(36)
	v_max3_f32 v6, |v88|, |v89|, v6
	v_max3_f32 v6, |v90|, |v91|, v6
	s_waitcnt vmcnt(35)
	v_max3_f32 v6, |v92|, |v93|, v6
	v_max3_f32 v6, |v94|, |v95|, v6
	s_waitcnt vmcnt(34)
	v_max3_f32 v6, |v96|, |v97|, v6
	v_max3_f32 v6, |v98|, |v99|, v6
	s_waitcnt vmcnt(33)
	v_max3_f32 v6, |v100|, |v101|, v6
	v_max3_f32 v6, |v102|, |v103|, v6
	s_nop 1
	v_max_u32_dpp v6, v6, v6 quad_perm:[1,0,3,2] row_mask:0xf bank_mask:0xf bound_ctrl:1
	s_nop 1
	v_max_u32_dpp v6, v6, v6 quad_perm:[2,3,0,1] row_mask:0xf bank_mask:0xf bound_ctrl:1
	s_nop 1
	v_max_u32_dpp v6, v6, v6 row_half_mirror row_mask:0xf bank_mask:0xf bound_ctrl:1
	s_nop 1
	v_max_u32_dpp v6, v6, v6 row_mirror row_mask:0xf bank_mask:0xf bound_ctrl:1
	s_nop 1
	v_mov_b32_e32 v7, v6
	s_nop 1
	v_permlane16_swap_b32_e32 v6, v7
	v_max_u32_e32 v6, v6, v7
	v_mov_b32_e32 v7, v6
	s_nop 1
	v_permlane32_swap_b32_e32 v6, v7
	v_max_u32_e32 v6, v6, v7
	v_div_scale_f32 v12, s[16:17], v6, v6, s14
	v_rcp_f32_e32 v13, v12
	s_nop 0
	v_fma_f32 v14, -v12, v13, 1.0
	v_fmac_f32_e32 v13, v14, v13
	v_div_scale_f32 v14, vcc, s14, v6, s14
	v_mul_f32_e32 v15, v14, v13
	v_fma_f32 v16, -v12, v15, v14
	v_fmac_f32_e32 v15, v16, v13
	v_fma_f32 v12, -v12, v15, v14
	v_div_fmas_f32 v12, v12, v13, v15
	v_div_fixup_f32 v9, v12, v6, s14
	v_cmp_lt_f32_e32 vcc, 0, v6
	s_nop 1
	v_cndmask_b32_e32 v9, 0, v9, vcc
	s_lshl_b32 s1, s4, 12
	s_add_u32 s8, s90, 0xba00000
	s_addc_u32 s9, s91, 0
	s_add_u32 s8, s8, s1
	s_addc_u32 s9, s9, 0
	s_lshl_b32 s1, s4, 2
	s_add_u32 s10, s90, 0x1ba00000
	s_addc_u32 s11, s91, 0
	s_add_u32 s10, s10, s1
	s_addc_u32 s11, s11, 0
	v_mul_f32_e32 v40, v40, v9
	v_mul_f32_e32 v41, v41, v9
	v_mul_f32_e32 v42, v42, v9
	v_mul_f32_e32 v43, v43, v9
	v_mov_b32_e32 v20, v10
	v_cvt_pk_fp8_f32 v20, v40, v41
	v_mul_f32_e32 v44, v44, v9
	v_mul_f32_e32 v45, v45, v9
	v_mul_f32_e32 v46, v46, v9
	v_mul_f32_e32 v47, v47, v9
	v_mov_b32_e32 v21, v10
	v_cvt_pk_fp8_f32 v21, v44, v45
	v_cvt_pk_fp8_f32 v20, v42, v43 op_sel:[0,0,1]
	v_mul_f32_e32 v48, v48, v9
	v_mul_f32_e32 v49, v49, v9
	v_mul_f32_e32 v50, v50, v9
; __device__ __forceinline__ unsigned max64u(unsigned x) {
;     x = umax_u(x, dppu<DPP_XOR1>(x)); x = umax_u(x, dppu<DPP_XOR2>(x)); x = umax_u(x, dppu<DPP_HMIRROR>(x)); x = umax_u(x, dppu<DPP_MIRROR>(x));
;     auto s = __builtin_amdgcn_permlane16_swap(x, x, false, false); x = umax_u(s[0], s[1]);
;     auto t = __builtin_amdgcn_permlane32_swap(x, x, false, false); return umax_u(t[0], t[1]);
; }
; __device__ __forceinline__ void peer_row_load(f32x4 (&v)[16], const float* const (&in)[34], int it, int layer, int lane) {
;     const int tbl = it >= NEXP, r = it - tbl * NEXP + layer * NEXP;
;     const f32x4* src = (const f32x4*)((tbl ? in[33] : in[32]) + (size_t)r * D) + lane;
; #pragma unroll
;     for (int j = 0; j < 16; ++j) v[j] = src[64 * j];
; }
; __device__ __forceinline__ void peer_row_store(const f32x4 (&v)[16], unsigned char* ws, int it, int layer, int lane) {
;     const int tbl = it >= NEXP, r = it - tbl * NEXP + layer * NEXP;
;     float am = 0.f;
; #pragma unroll
;     for (int j = 0; j < 16; ++j) am = fmaxf(fmaxf(am, fmaxf(fabsf(v[j][0]), fabsf(v[j][1]))), fmaxf(fabsf(v[j][2]), fabsf(v[j][3])));
;     am = __uint_as_float(max64u(__float_as_uint(am)));
;     const float q = am > 0.f ? 256.0f / am : 0.f;
;     unsigned* dst = (unsigned*)(ws + (tbl ? WS_PV : WS_PU) + (size_t)r * D) + lane;
;     if (tbl) {
;         const int rl = it - NEXP;
;         unsigned char* pvl = ws + WS_PV + (size_t)layer * NEXP * D + (size_t)rl * 8 + (lane & 1) * 4;
;         unsigned char* pvg = ws + WS_PV + (size_t)layer * NEXP * D + (size_t)NEXP * 2048 + (size_t)rl * 2048 + 4 * lane;
; #pragma unroll
;         for (int j = 0; j < 16; ++j) { int w = __builtin_amdgcn_cvt_pk_bf8_f32(v[j][0] * q, v[j][1] * q, 0, false); w = __builtin_amdgcn_cvt_pk_bf8_f32(v[j][2] * q, v[j][3] * q, w, true);
;             if (j < 8) *(unsigned*)(pvl + (size_t)((lane >> 1) + 32 * j) * (NEXP * 8)) = (unsigned)w;
;             else *(unsigned*)(pvg + 256 * (j - 8)) = (unsigned)w; }
;     } else {
; #pragma unroll
;         for (int j = 0; j < 16; ++j) { int w = __builtin_amdgcn_cvt_pk_fp8_f32(v[j][0] * q, v[j][1] * q, 0, false); w = __builtin_amdgcn_cvt_pk_fp8_f32(v[j][2] * q, v[j][3] * q, w, true); dst[64 * j] = (unsigned)w; }
;     }
;     if (lane == 0) ((float*)(ws + (tbl ? WS_SV : WS_SU)))[r] = am * (1.0f / 256.0f);
; }
	v_mul_f32_e32 v51, v51, v9
	v_mov_b32_e32 v22, v10
	v_cvt_pk_fp8_f32 v22, v48, v49
	v_cvt_pk_fp8_f32 v21, v46, v47 op_sel:[0,0,1]
	v_mul_f32_e32 v52, v52, v9
	v_mul_f32_e32 v53, v53, v9
	v_mul_f32_e32 v54, v54, v9
	v_mul_f32_e32 v55, v55, v9
	v_mov_b32_e32 v23, v10
	v_cvt_pk_fp8_f32 v23, v52, v53
	v_cvt_pk_fp8_f32 v22, v50, v51 op_sel:[0,0,1]
	v_mul_f32_e32 v56, v56, v9
	v_mul_f32_e32 v57, v57, v9
	v_mul_f32_e32 v58, v58, v9
	v_mul_f32_e32 v59, v59, v9
	v_mov_b32_e32 v24, v10
	v_cvt_pk_fp8_f32 v24, v56, v57
	v_cvt_pk_fp8_f32 v23, v54, v55 op_sel:[0,0,1]
	v_mul_f32_e32 v60, v60, v9
	v_mul_f32_e32 v61, v61, v9
	v_mul_f32_e32 v62, v62, v9
	v_mul_f32_e32 v63, v63, v9
	v_mov_b32_e32 v25, v10
	v_cvt_pk_fp8_f32 v25, v60, v61
	v_cvt_pk_fp8_f32 v24, v58, v59 op_sel:[0,0,1]
	v_mul_f32_e32 v64, v64, v9
	v_mul_f32_e32 v65, v65, v9
	v_mul_f32_e32 v66, v66, v9
	v_mul_f32_e32 v67, v67, v9
	v_mov_b32_e32 v26, v10
	v_cvt_pk_fp8_f32 v26, v64, v65
	v_cvt_pk_fp8_f32 v25, v62, v63 op_sel:[0,0,1]
	v_mul_f32_e32 v68, v68, v9
	v_mul_f32_e32 v69, v69, v9
	v_mul_f32_e32 v70, v70, v9
	v_mul_f32_e32 v71, v71, v9
	v_mov_b32_e32 v27, v10
	v_cvt_pk_fp8_f32 v27, v68, v69
	v_cvt_pk_fp8_f32 v26, v66, v67 op_sel:[0,0,1]
	v_mul_f32_e32 v72, v72, v9
	v_mul_f32_e32 v73, v73, v9
	v_mul_f32_e32 v74, v74, v9
	v_mul_f32_e32 v75, v75, v9
	v_mov_b32_e32 v28, v10
	v_cvt_pk_fp8_f32 v28, v72, v73
	v_cvt_pk_fp8_f32 v27, v70, v71 op_sel:[0,0,1]
	v_mul_f32_e32 v76, v76, v9
	v_mul_f32_e32 v77, v77, v9
	v_mul_f32_e32 v78, v78, v9
	v_mul_f32_e32 v79, v79, v9
	v_mov_b32_e32 v29, v10
	v_cvt_pk_fp8_f32 v29, v76, v77
	v_cvt_pk_fp8_f32 v28, v74, v75 op_sel:[0,0,1]
	v_mul_f32_e32 v80, v80, v9
	v_mul_f32_e32 v81, v81, v9
	v_mul_f32_e32 v82, v82, v9
	v_mul_f32_e32 v83, v83, v9
	v_mov_b32_e32 v30, v10
	v_cvt_pk_fp8_f32 v30, v80, v81
	v_cvt_pk_fp8_f32 v29, v78, v79 op_sel:[0,0,1]
	v_mul_f32_e32 v84, v84, v9
	v_mul_f32_e32 v85, v85, v9
	v_mul_f32_e32 v86, v86, v9
	v_mul_f32_e32 v87, v87, v9
	v_mov_b32_e32 v31, v10
	v_cvt_pk_fp8_f32 v31, v84, v85
	v_cvt_pk_fp8_f32 v30, v82, v83 op_sel:[0,0,1]
	v_mul_f32_e32 v88, v88, v9
	v_mul_f32_e32 v89, v89, v9
	v_mul_f32_e32 v90, v90, v9
	v_mul_f32_e32 v91, v91, v9
	v_mov_b32_e32 v32, v10
	v_cvt_pk_fp8_f32 v32, v88, v89
	v_cvt_pk_fp8_f32 v31, v86, v87 op_sel:[0,0,1]
	v_mul_f32_e32 v92, v92, v9
	v_mul_f32_e32 v93, v93, v9
	v_mul_f32_e32 v94, v94, v9
	v_mul_f32_e32 v95, v95, v9
	v_mov_b32_e32 v33, v10
	v_cvt_pk_fp8_f32 v33, v92, v93
	v_cvt_pk_fp8_f32 v32, v90, v91 op_sel:[0,0,1]
	v_mul_f32_e32 v96, v96, v9
	v_mul_f32_e32 v97, v97, v9
	v_mul_f32_e32 v98, v98, v9
	v_mul_f32_e32 v99, v99, v9
	v_mov_b32_e32 v34, v10
	v_cvt_pk_fp8_f32 v34, v96, v97
	v_cvt_pk_fp8_f32 v33, v94, v95 op_sel:[0,0,1]
	v_mul_f32_e32 v100, v100, v9
	v_mul_f32_e32 v101, v101, v9
	v_mul_f32_e32 v102, v102, v9
	v_mul_f32_e32 v103, v103, v9
	v_mov_b32_e32 v35, v10
	v_cvt_pk_fp8_f32 v35, v100, v101
	v_cvt_pk_fp8_f32 v34, v98, v99 op_sel:[0,0,1]
	v_cvt_pk_fp8_f32 v35, v102, v103 op_sel:[0,0,1]
	s_nop 0
	v_mul_f32_e32 v8, 0x3b800000, v6
	global_store_dword v2, v20, s[8:9]
	global_store_dword v2, v21, s[8:9] offset:256
	global_store_dword v2, v22, s[8:9] offset:512
	global_store_dword v2, v23, s[8:9] offset:768
	global_store_dword v2, v24, s[8:9] offset:1024
	global_store_dword v2, v25, s[8:9] offset:1280
	global_store_dword v2, v26, s[8:9] offset:1536
	global_store_dword v2, v27, s[8:9] offset:1792
	global_store_dword v2, v28, s[8:9] offset:2048
	global_store_dword v2, v29, s[8:9] offset:2304
	global_store_dword v2, v30, s[8:9] offset:2560
	global_store_dword v2, v31, s[8:9] offset:2816
	global_store_dword v2, v32, s[8:9] offset:3072
	global_store_dword v2, v33, s[8:9] offset:3328
	global_store_dword v2, v34, s[8:9] offset:3584
	global_store_dword v2, v35, s[8:9] offset:3840
	s_mov_b64 s[18:19], exec
	s_mov_b64 exec, s[12:13]
	global_store_dword v10, v8, s[10:11]
	s_mov_b64 exec, s[18:19]
	s_mov_b32 s4, s5
	s_add_i32 s5, s4, 1024
	s_lshl_b32 s1, s5, 14
	s_add_u32 s6, s84, s1
	s_addc_u32 s7, s85, 0
	global_load_dwordx4 v[40:43], v1, s[6:7]
	global_load_dwordx4 v[44:47], v1, s[6:7] offset:1024
	global_load_dwordx4 v[48:51], v1, s[6:7] offset:2048
	global_load_dwordx4 v[52:55], v1, s[6:7] offset:3072
	global_load_dwordx4 v[56:59], v3, s[6:7]
	global_load_dwordx4 v[60:63], v3, s[6:7] offset:1024
	global_load_dwordx4 v[64:67], v3, s[6:7] offset:2048
	global_load_dwordx4 v[68:71], v3, s[6:7] offset:3072
	global_load_dwordx4 v[72:75], v4, s[6:7]
	global_load_dwordx4 v[76:79], v4, s[6:7] offset:1024
	global_load_dwordx4 v[80:83], v4, s[6:7] offset:2048
	global_load_dwordx4 v[84:87], v4, s[6:7] offset:3072
	global_load_dwordx4 v[88:91], v5, s[6:7]
	global_load_dwordx4 v[92:95], v5, s[6:7] offset:1024
	global_load_dwordx4 v[96:99], v5, s[6:7] offset:2048
	global_load_dwordx4 v[100:103], v5, s[6:7] offset:3072
	s_waitcnt vmcnt(48)
	v_max3_f32 v6, |v104|, |v105|, 0
	v_max3_f32 v6, |v106|, |v107|, v6
	s_waitcnt vmcnt(47)
	v_max3_f32 v6, |v108|, |v109|, v6
	v_max3_f32 v6, |v110|, |v111|, v6
	s_waitcnt vmcnt(46)
	v_max3_f32 v6, |v112|, |v113|, v6
	v_max3_f32 v6, |v114|, |v115|, v6
	s_waitcnt vmcnt(45)
	v_max3_f32 v6, |v116|, |v117|, v6
	v_max3_f32 v6, |v118|, |v119|, v6
	s_waitcnt vmcnt(44)
	v_max3_f32 v6, |v120|, |v121|, v6
	v_max3_f32 v6, |v122|, |v123|, v6
	s_waitcnt vmcnt(43)
	v_max3_f32 v6, |v124|, |v125|, v6
	v_max3_f32 v6, |v126|, |v127|, v6
	s_waitcnt vmcnt(42)
	v_max3_f32 v6, |v128|, |v129|, v6
	v_max3_f32 v6, |v130|, |v131|, v6
	s_waitcnt vmcnt(41)
	v_max3_f32 v6, |v132|, |v133|, v6
	v_max3_f32 v6, |v134|, |v135|, v6
	s_waitcnt vmcnt(40)
	v_max3_f32 v6, |v136|, |v137|, v6
	v_max3_f32 v6, |v138|, |v139|, v6
	s_waitcnt vmcnt(39)
; __device__ __forceinline__ unsigned max64u(unsigned x) {
;     x = umax_u(x, dppu<DPP_XOR1>(x)); x = umax_u(x, dppu<DPP_XOR2>(x)); x = umax_u(x, dppu<DPP_HMIRROR>(x)); x = umax_u(x, dppu<DPP_MIRROR>(x));
;     auto s = __builtin_amdgcn_permlane16_swap(x, x, false, false); x = umax_u(s[0], s[1]);
;     auto t = __builtin_amdgcn_permlane32_swap(x, x, false, false); return umax_u(t[0], t[1]);
; }
; __device__ __forceinline__ void peer_row_load(f32x4 (&v)[16], const float* const (&in)[34], int it, int layer, int lane) {
;     const int tbl = it >= NEXP, r = it - tbl * NEXP + layer * NEXP;
;     const f32x4* src = (const f32x4*)((tbl ? in[33] : in[32]) + (size_t)r * D) + lane;
; #pragma unroll
;     for (int j = 0; j < 16; ++j) v[j] = src[64 * j];
; }
; __device__ __forceinline__ void peer_row_store(const f32x4 (&v)[16], unsigned char* ws, int it, int layer, int lane) {
;     const int tbl = it >= NEXP, r = it - tbl * NEXP + layer * NEXP;
;     float am = 0.f;
; #pragma unroll
;     for (int j = 0; j < 16; ++j) am = fmaxf(fmaxf(am, fmaxf(fabsf(v[j][0]), fabsf(v[j][1]))), fmaxf(fabsf(v[j][2]), fabsf(v[j][3])));
;     am = __uint_as_float(max64u(__float_as_uint(am)));
;     const float q = am > 0.f ? 256.0f / am : 0.f;
;     unsigned* dst = (unsigned*)(ws + (tbl ? WS_PV : WS_PU) + (size_t)r * D) + lane;
;     if (tbl) {
;         const int rl = it - NEXP;
;         unsigned char* pvl = ws + WS_PV + (size_t)layer * NEXP * D + (size_t)rl * 8 + (lane & 1) * 4;
;         unsigned char* pvg = ws + WS_PV + (size_t)layer * NEXP * D + (size_t)NEXP * 2048 + (size_t)rl * 2048 + 4 * lane;
; #pragma unroll
;         for (int j = 0; j < 16; ++j) { int w = __builtin_amdgcn_cvt_pk_bf8_f32(v[j][0] * q, v[j][1] * q, 0, false); w = __builtin_amdgcn_cvt_pk_bf8_f32(v[j][2] * q, v[j][3] * q, w, true);
;             if (j < 8) *(unsigned*)(pvl + (size_t)((lane >> 1) + 32 * j) * (NEXP * 8)) = (unsigned)w;
;             else *(unsigned*)(pvg + 256 * (j - 8)) = (unsigned)w; }
;     } else {
; #pragma unroll
;         for (int j = 0; j < 16; ++j) { int w = __builtin_amdgcn_cvt_pk_fp8_f32(v[j][0] * q, v[j][1] * q, 0, false); w = __builtin_amdgcn_cvt_pk_fp8_f32(v[j][2] * q, v[j][3] * q, w, true); dst[64 * j] = (unsigned)w; }
;     }
;     if (lane == 0) ((float*)(ws + (tbl ? WS_SV : WS_SU)))[r] = am * (1.0f / 256.0f);
; }
	v_max3_f32 v6, |v140|, |v141|, v6
	v_max3_f32 v6, |v142|, |v143|, v6
	s_waitcnt vmcnt(38)
	v_max3_f32 v6, |v144|, |v145|, v6
	v_max3_f32 v6, |v146|, |v147|, v6
	s_waitcnt vmcnt(37)
	v_max3_f32 v6, |v148|, |v149|, v6
	v_max3_f32 v6, |v150|, |v151|, v6
	s_waitcnt vmcnt(36)
	v_max3_f32 v6, |v152|, |v153|, v6
	v_max3_f32 v6, |v154|, |v155|, v6
	s_waitcnt vmcnt(35)
	v_max3_f32 v6, |v156|, |v157|, v6
	v_max3_f32 v6, |v158|, |v159|, v6
	s_waitcnt vmcnt(34)
	v_max3_f32 v6, |v160|, |v161|, v6
	v_max3_f32 v6, |v162|, |v163|, v6
	s_waitcnt vmcnt(33)
	v_max3_f32 v6, |v164|, |v165|, v6
	v_max3_f32 v6, |v166|, |v167|, v6
	s_nop 1
	v_max_u32_dpp v6, v6, v6 quad_perm:[1,0,3,2] row_mask:0xf bank_mask:0xf bound_ctrl:1
	s_nop 1
	v_max_u32_dpp v6, v6, v6 quad_perm:[2,3,0,1] row_mask:0xf bank_mask:0xf bound_ctrl:1
	s_nop 1
	v_max_u32_dpp v6, v6, v6 row_half_mirror row_mask:0xf bank_mask:0xf bound_ctrl:1
	s_nop 1
	v_max_u32_dpp v6, v6, v6 row_mirror row_mask:0xf bank_mask:0xf bound_ctrl:1
	s_nop 1
	v_mov_b32_e32 v7, v6
	s_nop 1
	v_permlane16_swap_b32_e32 v6, v7
	v_max_u32_e32 v6, v6, v7
	v_mov_b32_e32 v7, v6
	s_nop 1
	v_permlane32_swap_b32_e32 v6, v7
	v_max_u32_e32 v6, v6, v7
	v_div_scale_f32 v12, s[16:17], v6, v6, s14
	v_rcp_f32_e32 v13, v12
	s_nop 0
	v_fma_f32 v14, -v12, v13, 1.0
	v_fmac_f32_e32 v13, v14, v13
	v_div_scale_f32 v14, vcc, s14, v6, s14
	v_mul_f32_e32 v15, v14, v13
	v_fma_f32 v16, -v12, v15, v14
	v_fmac_f32_e32 v15, v16, v13
	v_fma_f32 v12, -v12, v15, v14
	v_div_fmas_f32 v12, v12, v13, v15
	v_div_fixup_f32 v9, v12, v6, s14
	v_cmp_lt_f32_e32 vcc, 0, v6
	s_nop 1
	v_cndmask_b32_e32 v9, 0, v9, vcc
	s_lshl_b32 s1, s4, 12
	s_add_u32 s8, s90, 0xba00000
	s_addc_u32 s9, s91, 0
	s_add_u32 s8, s8, s1
	s_addc_u32 s9, s9, 0
	s_lshl_b32 s1, s4, 2
	s_add_u32 s10, s90, 0x1ba00000
	s_addc_u32 s11, s91, 0
	s_add_u32 s10, s10, s1
	s_addc_u32 s11, s11, 0
	v_mul_f32_e32 v104, v104, v9
	v_mul_f32_e32 v105, v105, v9
	v_mul_f32_e32 v106, v106, v9
	v_mul_f32_e32 v107, v107, v9
	v_mov_b32_e32 v20, v10
	v_cvt_pk_fp8_f32 v20, v104, v105
	v_mul_f32_e32 v108, v108, v9
	v_mul_f32_e32 v109, v109, v9
	v_mul_f32_e32 v110, v110, v9
	v_mul_f32_e32 v111, v111, v9
	v_mov_b32_e32 v21, v10
	v_cvt_pk_fp8_f32 v21, v108, v109
	v_cvt_pk_fp8_f32 v20, v106, v107 op_sel:[0,0,1]
	v_mul_f32_e32 v112, v112, v9
	v_mul_f32_e32 v113, v113, v9
	v_mul_f32_e32 v114, v114, v9
	v_mul_f32_e32 v115, v115, v9
	v_mov_b32_e32 v22, v10
	v_cvt_pk_fp8_f32 v22, v112, v113
	v_cvt_pk_fp8_f32 v21, v110, v111 op_sel:[0,0,1]
	v_mul_f32_e32 v116, v116, v9
	v_mul_f32_e32 v117, v117, v9
	v_mul_f32_e32 v118, v118, v9
	v_mul_f32_e32 v119, v119, v9
	v_mov_b32_e32 v23, v10
	v_cvt_pk_fp8_f32 v23, v116, v117
	v_cvt_pk_fp8_f32 v22, v114, v115 op_sel:[0,0,1]
	v_mul_f32_e32 v120, v120, v9
	v_mul_f32_e32 v121, v121, v9
	v_mul_f32_e32 v122, v122, v9
	v_mul_f32_e32 v123, v123, v9
	v_mov_b32_e32 v24, v10
	v_cvt_pk_fp8_f32 v24, v120, v121
	v_cvt_pk_fp8_f32 v23, v118, v119 op_sel:[0,0,1]
	v_mul_f32_e32 v124, v124, v9
	v_mul_f32_e32 v125, v125, v9
	v_mul_f32_e32 v126, v126, v9
	v_mul_f32_e32 v127, v127, v9
	v_mov_b32_e32 v25, v10
	v_cvt_pk_fp8_f32 v25, v124, v125
	v_cvt_pk_fp8_f32 v24, v122, v123 op_sel:[0,0,1]
	v_mul_f32_e32 v128, v128, v9
	v_mul_f32_e32 v129, v129, v9
	v_mul_f32_e32 v130, v130, v9
	v_mul_f32_e32 v131, v131, v9
	v_mov_b32_e32 v26, v10
	v_cvt_pk_fp8_f32 v26, v128, v129
	v_cvt_pk_fp8_f32 v25, v126, v127 op_sel:[0,0,1]
	v_mul_f32_e32 v132, v132, v9
	v_mul_f32_e32 v133, v133, v9
	v_mul_f32_e32 v134, v134, v9
	v_mul_f32_e32 v135, v135, v9
	v_mov_b32_e32 v27, v10
	v_cvt_pk_fp8_f32 v27, v132, v133
	v_cvt_pk_fp8_f32 v26, v130, v131 op_sel:[0,0,1]
	v_mul_f32_e32 v136, v136, v9
	v_mul_f32_e32 v137, v137, v9
	v_mul_f32_e32 v138, v138, v9
	v_mul_f32_e32 v139, v139, v9
	v_mov_b32_e32 v28, v10
	v_cvt_pk_fp8_f32 v28, v136, v137
	v_cvt_pk_fp8_f32 v27, v134, v135 op_sel:[0,0,1]
	v_mul_f32_e32 v140, v140, v9
	v_mul_f32_e32 v141, v141, v9
	v_mul_f32_e32 v142, v142, v9
	v_mul_f32_e32 v143, v143, v9
	v_mov_b32_e32 v29, v10
	v_cvt_pk_fp8_f32 v29, v140, v141
	v_cvt_pk_fp8_f32 v28, v138, v139 op_sel:[0,0,1]
	v_mul_f32_e32 v144, v144, v9
	v_mul_f32_e32 v145, v145, v9
	v_mul_f32_e32 v146, v146, v9
	v_mul_f32_e32 v147, v147, v9
	v_mov_b32_e32 v30, v10
	v_cvt_pk_fp8_f32 v30, v144, v145
	v_cvt_pk_fp8_f32 v29, v142, v143 op_sel:[0,0,1]
	v_mul_f32_e32 v148, v148, v9
	v_mul_f32_e32 v149, v149, v9
	v_mul_f32_e32 v150, v150, v9
	v_mul_f32_e32 v151, v151, v9
	v_mov_b32_e32 v31, v10
	v_cvt_pk_fp8_f32 v31, v148, v149
	v_cvt_pk_fp8_f32 v30, v146, v147 op_sel:[0,0,1]
	v_mul_f32_e32 v152, v152, v9
	v_mul_f32_e32 v153, v153, v9
	v_mul_f32_e32 v154, v154, v9
	v_mul_f32_e32 v155, v155, v9
	v_mov_b32_e32 v32, v10
	v_cvt_pk_fp8_f32 v32, v152, v153
	v_cvt_pk_fp8_f32 v31, v150, v151 op_sel:[0,0,1]
	v_mul_f32_e32 v156, v156, v9
	v_mul_f32_e32 v157, v157, v9
	v_mul_f32_e32 v158, v158, v9
	v_mul_f32_e32 v159, v159, v9
	v_mov_b32_e32 v33, v10
	v_cvt_pk_fp8_f32 v33, v156, v157
	v_cvt_pk_fp8_f32 v32, v154, v155 op_sel:[0,0,1]
	v_mul_f32_e32 v160, v160, v9
	v_mul_f32_e32 v161, v161, v9
	v_mul_f32_e32 v162, v162, v9
	v_mul_f32_e32 v163, v163, v9
	v_mov_b32_e32 v34, v10
	v_cvt_pk_fp8_f32 v34, v160, v161
	v_cvt_pk_fp8_f32 v33, v158, v159 op_sel:[0,0,1]
	v_mul_f32_e32 v164, v164, v9
	v_mul_f32_e32 v165, v165, v9
	v_mul_f32_e32 v166, v166, v9
	v_mul_f32_e32 v167, v167, v9
	v_mov_b32_e32 v35, v10
	v_cvt_pk_fp8_f32 v35, v164, v165
	v_cvt_pk_fp8_f32 v34, v162, v163 op_sel:[0,0,1]
	v_cvt_pk_fp8_f32 v35, v166, v167 op_sel:[0,0,1]
	s_nop 0
	v_mul_f32_e32 v8, 0x3b800000, v6
	global_store_dword v2, v20, s[8:9]
	global_store_dword v2, v21, s[8:9] offset:256
; __device__ __forceinline__ unsigned max64u(unsigned x) {
;     x = umax_u(x, dppu<DPP_XOR1>(x)); x = umax_u(x, dppu<DPP_XOR2>(x)); x = umax_u(x, dppu<DPP_HMIRROR>(x)); x = umax_u(x, dppu<DPP_MIRROR>(x));
;     auto s = __builtin_amdgcn_permlane16_swap(x, x, false, false); x = umax_u(s[0], s[1]);
;     auto t = __builtin_amdgcn_permlane32_swap(x, x, false, false); return umax_u(t[0], t[1]);
; }
; __device__ __forceinline__ void peer_row_load(f32x4 (&v)[16], const float* const (&in)[34], int it, int layer, int lane) {
;     const int tbl = it >= NEXP, r = it - tbl * NEXP + layer * NEXP;
;     const f32x4* src = (const f32x4*)((tbl ? in[33] : in[32]) + (size_t)r * D) + lane;
; #pragma unroll
;     for (int j = 0; j < 16; ++j) v[j] = src[64 * j];
; }
; __device__ __forceinline__ void peer_row_store(const f32x4 (&v)[16], unsigned char* ws, int it, int layer, int lane) {
;     const int tbl = it >= NEXP, r = it - tbl * NEXP + layer * NEXP;
;     float am = 0.f;
; #pragma unroll
;     for (int j = 0; j < 16; ++j) am = fmaxf(fmaxf(am, fmaxf(fabsf(v[j][0]), fabsf(v[j][1]))), fmaxf(fabsf(v[j][2]), fabsf(v[j][3])));
;     am = __uint_as_float(max64u(__float_as_uint(am)));
;     const float q = am > 0.f ? 256.0f / am : 0.f;
;     unsigned* dst = (unsigned*)(ws + (tbl ? WS_PV : WS_PU) + (size_t)r * D) + lane;
;     if (tbl) {
;         const int rl = it - NEXP;
;         unsigned char* pvl = ws + WS_PV + (size_t)layer * NEXP * D + (size_t)rl * 8 + (lane & 1) * 4;
;         unsigned char* pvg = ws + WS_PV + (size_t)layer * NEXP * D + (size_t)NEXP * 2048 + (size_t)rl * 2048 + 4 * lane;
; #pragma unroll
;         for (int j = 0; j < 16; ++j) { int w = __builtin_amdgcn_cvt_pk_bf8_f32(v[j][0] * q, v[j][1] * q, 0, false); w = __builtin_amdgcn_cvt_pk_bf8_f32(v[j][2] * q, v[j][3] * q, w, true);
;             if (j < 8) *(unsigned*)(pvl + (size_t)((lane >> 1) + 32 * j) * (NEXP * 8)) = (unsigned)w;
;             else *(unsigned*)(pvg + 256 * (j - 8)) = (unsigned)w; }
;     } else {
; #pragma unroll
;         for (int j = 0; j < 16; ++j) { int w = __builtin_amdgcn_cvt_pk_fp8_f32(v[j][0] * q, v[j][1] * q, 0, false); w = __builtin_amdgcn_cvt_pk_fp8_f32(v[j][2] * q, v[j][3] * q, w, true); dst[64 * j] = (unsigned)w; }
;     }
;     if (lane == 0) ((float*)(ws + (tbl ? WS_SV : WS_SU)))[r] = am * (1.0f / 256.0f);
; }
	global_store_dword v2, v22, s[8:9] offset:512
	global_store_dword v2, v23, s[8:9] offset:768
	global_store_dword v2, v24, s[8:9] offset:1024
	global_store_dword v2, v25, s[8:9] offset:1280
	global_store_dword v2, v26, s[8:9] offset:1536
	global_store_dword v2, v27, s[8:9] offset:1792
	global_store_dword v2, v28, s[8:9] offset:2048
	global_store_dword v2, v29, s[8:9] offset:2304
	global_store_dword v2, v30, s[8:9] offset:2560
	global_store_dword v2, v31, s[8:9] offset:2816
	global_store_dword v2, v32, s[8:9] offset:3072
	global_store_dword v2, v33, s[8:9] offset:3328
	global_store_dword v2, v34, s[8:9] offset:3584
	global_store_dword v2, v35, s[8:9] offset:3840
	s_mov_b64 s[18:19], exec
	s_mov_b64 exec, s[12:13]
	global_store_dword v10, v8, s[10:11]
	s_mov_b64 exec, s[18:19]
	s_mov_b32 s4, s5
	s_add_i32 s5, s4, 1024
	s_lshl_b32 s1, s5, 14
	s_add_u32 s6, s84, s1
	s_addc_u32 s7, s85, 0
	global_load_dwordx4 v[104:107], v1, s[6:7]
	global_load_dwordx4 v[108:111], v1, s[6:7] offset:1024
	global_load_dwordx4 v[112:115], v1, s[6:7] offset:2048
	global_load_dwordx4 v[116:119], v1, s[6:7] offset:3072
	global_load_dwordx4 v[120:123], v3, s[6:7]
	global_load_dwordx4 v[124:127], v3, s[6:7] offset:1024
	global_load_dwordx4 v[128:131], v3, s[6:7] offset:2048
	global_load_dwordx4 v[132:135], v3, s[6:7] offset:3072
	global_load_dwordx4 v[136:139], v4, s[6:7]
	global_load_dwordx4 v[140:143], v4, s[6:7] offset:1024
	global_load_dwordx4 v[144:147], v4, s[6:7] offset:2048
	global_load_dwordx4 v[148:151], v4, s[6:7] offset:3072
	global_load_dwordx4 v[152:155], v5, s[6:7]
	global_load_dwordx4 v[156:159], v5, s[6:7] offset:1024
	global_load_dwordx4 v[160:163], v5, s[6:7] offset:2048
	global_load_dwordx4 v[164:167], v5, s[6:7] offset:3072
	s_waitcnt vmcnt(48)
	v_max3_f32 v6, |v40|, |v41|, 0
	v_max3_f32 v6, |v42|, |v43|, v6
	s_waitcnt vmcnt(47)
	v_max3_f32 v6, |v44|, |v45|, v6
	v_max3_f32 v6, |v46|, |v47|, v6
	s_waitcnt vmcnt(46)
	v_max3_f32 v6, |v48|, |v49|, v6
	v_max3_f32 v6, |v50|, |v51|, v6
	s_waitcnt vmcnt(45)
	v_max3_f32 v6, |v52|, |v53|, v6
	v_max3_f32 v6, |v54|, |v55|, v6
	s_waitcnt vmcnt(44)
	v_max3_f32 v6, |v56|, |v57|, v6
	v_max3_f32 v6, |v58|, |v59|, v6
	s_waitcnt vmcnt(43)
	v_max3_f32 v6, |v60|, |v61|, v6
	v_max3_f32 v6, |v62|, |v63|, v6
	s_waitcnt vmcnt(42)
	v_max3_f32 v6, |v64|, |v65|, v6
	v_max3_f32 v6, |v66|, |v67|, v6
	s_waitcnt vmcnt(41)
	v_max3_f32 v6, |v68|, |v69|, v6
	v_max3_f32 v6, |v70|, |v71|, v6
	s_waitcnt vmcnt(40)
	v_max3_f32 v6, |v72|, |v73|, v6
	v_max3_f32 v6, |v74|, |v75|, v6
	s_waitcnt vmcnt(39)
	v_max3_f32 v6, |v76|, |v77|, v6
	v_max3_f32 v6, |v78|, |v79|, v6
	s_waitcnt vmcnt(38)
	v_max3_f32 v6, |v80|, |v81|, v6
	v_max3_f32 v6, |v82|, |v83|, v6
	s_waitcnt vmcnt(37)
	v_max3_f32 v6, |v84|, |v85|, v6
	v_max3_f32 v6, |v86|, |v87|, v6
	s_waitcnt vmcnt(36)
	v_max3_f32 v6, |v88|, |v89|, v6
	v_max3_f32 v6, |v90|, |v91|, v6
	s_waitcnt vmcnt(35)
	v_max3_f32 v6, |v92|, |v93|, v6
	v_max3_f32 v6, |v94|, |v95|, v6
	s_waitcnt vmcnt(34)
	v_max3_f32 v6, |v96|, |v97|, v6
	v_max3_f32 v6, |v98|, |v99|, v6
	s_waitcnt vmcnt(33)
	v_max3_f32 v6, |v100|, |v101|, v6
	v_max3_f32 v6, |v102|, |v103|, v6
	s_nop 1
	v_max_u32_dpp v6, v6, v6 quad_perm:[1,0,3,2] row_mask:0xf bank_mask:0xf bound_ctrl:1
	s_nop 1
	v_max_u32_dpp v6, v6, v6 quad_perm:[2,3,0,1] row_mask:0xf bank_mask:0xf bound_ctrl:1
	s_nop 1
	v_max_u32_dpp v6, v6, v6 row_half_mirror row_mask:0xf bank_mask:0xf bound_ctrl:1
	s_nop 1
	v_max_u32_dpp v6, v6, v6 row_mirror row_mask:0xf bank_mask:0xf bound_ctrl:1
	s_nop 1
	v_mov_b32_e32 v7, v6
	s_nop 1
	v_permlane16_swap_b32_e32 v6, v7
	v_max_u32_e32 v6, v6, v7
	v_mov_b32_e32 v7, v6
	s_nop 1
	v_permlane32_swap_b32_e32 v6, v7
	v_max_u32_e32 v6, v6, v7
	v_div_scale_f32 v12, s[16:17], v6, v6, s14
	v_rcp_f32_e32 v13, v12
	s_nop 0
	v_fma_f32 v14, -v12, v13, 1.0
	v_fmac_f32_e32 v13, v14, v13
	v_div_scale_f32 v14, vcc, s14, v6, s14
	v_mul_f32_e32 v15, v14, v13
	v_fma_f32 v16, -v12, v15, v14
	v_fmac_f32_e32 v15, v16, v13
	v_fma_f32 v12, -v12, v15, v14
	v_div_fmas_f32 v12, v12, v13, v15
	v_div_fixup_f32 v9, v12, v6, s14
	v_cmp_lt_f32_e32 vcc, 0, v6
	s_nop 1
	v_cndmask_b32_e32 v9, 0, v9, vcc
	s_lshl_b32 s1, s4, 12
	s_add_u32 s8, s90, 0xba00000
	s_addc_u32 s9, s91, 0
	s_add_u32 s8, s8, s1
	s_addc_u32 s9, s9, 0
	s_lshl_b32 s1, s4, 2
	s_add_u32 s10, s90, 0x1ba00000
	s_addc_u32 s11, s91, 0
	s_add_u32 s10, s10, s1
	s_addc_u32 s11, s11, 0
	v_mul_f32_e32 v40, v40, v9
	v_mul_f32_e32 v41, v41, v9
	v_mul_f32_e32 v42, v42, v9
	v_mul_f32_e32 v43, v43, v9
	v_mov_b32_e32 v20, v10
	v_cvt_pk_fp8_f32 v20, v40, v41
	v_mul_f32_e32 v44, v44, v9
	v_mul_f32_e32 v45, v45, v9
	v_mul_f32_e32 v46, v46, v9
	v_mul_f32_e32 v47, v47, v9
	v_mov_b32_e32 v21, v10
	v_cvt_pk_fp8_f32 v21, v44, v45
	v_cvt_pk_fp8_f32 v20, v42, v43 op_sel:[0,0,1]
	v_mul_f32_e32 v48, v48, v9
	v_mul_f32_e32 v49, v49, v9
	v_mul_f32_e32 v50, v50, v9
	v_mul_f32_e32 v51, v51, v9
	v_mov_b32_e32 v22, v10
	v_cvt_pk_fp8_f32 v22, v48, v49
	v_cvt_pk_fp8_f32 v21, v46, v47 op_sel:[0,0,1]
	v_mul_f32_e32 v52, v52, v9
	v_mul_f32_e32 v53, v53, v9
	v_mul_f32_e32 v54, v54, v9
	v_mul_f32_e32 v55, v55, v9
	v_mov_b32_e32 v23, v10
	v_cvt_pk_fp8_f32 v23, v52, v53
	v_cvt_pk_fp8_f32 v22, v50, v51 op_sel:[0,0,1]
	v_mul_f32_e32 v56, v56, v9
	v_mul_f32_e32 v57, v57, v9
	v_mul_f32_e32 v58, v58, v9
	v_mul_f32_e32 v59, v59, v9
	v_mov_b32_e32 v24, v10
	v_cvt_pk_fp8_f32 v24, v56, v57
	v_cvt_pk_fp8_f32 v23, v54, v55 op_sel:[0,0,1]
	v_mul_f32_e32 v60, v60, v9
	v_mul_f32_e32 v61, v61, v9
	v_mul_f32_e32 v62, v62, v9
	v_mul_f32_e32 v63, v63, v9
	v_mov_b32_e32 v25, v10
	v_cvt_pk_fp8_f32 v25, v60, v61
	v_cvt_pk_fp8_f32 v24, v58, v59 op_sel:[0,0,1]
; __device__ __forceinline__ unsigned max64u(unsigned x) {
;     x = umax_u(x, dppu<DPP_XOR1>(x)); x = umax_u(x, dppu<DPP_XOR2>(x)); x = umax_u(x, dppu<DPP_HMIRROR>(x)); x = umax_u(x, dppu<DPP_MIRROR>(x));
;     auto s = __builtin_amdgcn_permlane16_swap(x, x, false, false); x = umax_u(s[0], s[1]);
;     auto t = __builtin_amdgcn_permlane32_swap(x, x, false, false); return umax_u(t[0], t[1]);
; }
; __device__ __forceinline__ void peer_row_load(f32x4 (&v)[16], const float* const (&in)[34], int it, int layer, int lane) {
;     const int tbl = it >= NEXP, r = it - tbl * NEXP + layer * NEXP;
;     const f32x4* src = (const f32x4*)((tbl ? in[33] : in[32]) + (size_t)r * D) + lane;
; #pragma unroll
;     for (int j = 0; j < 16; ++j) v[j] = src[64 * j];
; }
; __device__ __forceinline__ void peer_row_store(const f32x4 (&v)[16], unsigned char* ws, int it, int layer, int lane) {
;     const int tbl = it >= NEXP, r = it - tbl * NEXP + layer * NEXP;
;     float am = 0.f;
; #pragma unroll
;     for (int j = 0; j < 16; ++j) am = fmaxf(fmaxf(am, fmaxf(fabsf(v[j][0]), fabsf(v[j][1]))), fmaxf(fabsf(v[j][2]), fabsf(v[j][3])));
;     am = __uint_as_float(max64u(__float_as_uint(am)));
;     const float q = am > 0.f ? 256.0f / am : 0.f;
;     unsigned* dst = (unsigned*)(ws + (tbl ? WS_PV : WS_PU) + (size_t)r * D) + lane;
;     if (tbl) {
;         const int rl = it - NEXP;
;         unsigned char* pvl = ws + WS_PV + (size_t)layer * NEXP * D + (size_t)rl * 8 + (lane & 1) * 4;
;         unsigned char* pvg = ws + WS_PV + (size_t)layer * NEXP * D + (size_t)NEXP * 2048 + (size_t)rl * 2048 + 4 * lane;
; #pragma unroll
;         for (int j = 0; j < 16; ++j) { int w = __builtin_amdgcn_cvt_pk_bf8_f32(v[j][0] * q, v[j][1] * q, 0, false); w = __builtin_amdgcn_cvt_pk_bf8_f32(v[j][2] * q, v[j][3] * q, w, true);
;             if (j < 8) *(unsigned*)(pvl + (size_t)((lane >> 1) + 32 * j) * (NEXP * 8)) = (unsigned)w;
;             else *(unsigned*)(pvg + 256 * (j - 8)) = (unsigned)w; }
;     } else {
; #pragma unroll
;         for (int j = 0; j < 16; ++j) { int w = __builtin_amdgcn_cvt_pk_fp8_f32(v[j][0] * q, v[j][1] * q, 0, false); w = __builtin_amdgcn_cvt_pk_fp8_f32(v[j][2] * q, v[j][3] * q, w, true); dst[64 * j] = (unsigned)w; }
;     }
;     if (lane == 0) ((float*)(ws + (tbl ? WS_SV : WS_SU)))[r] = am * (1.0f / 256.0f);
; }
	v_mul_f32_e32 v64, v64, v9
	v_mul_f32_e32 v65, v65, v9
	v_mul_f32_e32 v66, v66, v9
	v_mul_f32_e32 v67, v67, v9
	v_mov_b32_e32 v26, v10
	v_cvt_pk_fp8_f32 v26, v64, v65
	v_cvt_pk_fp8_f32 v25, v62, v63 op_sel:[0,0,1]
	v_mul_f32_e32 v68, v68, v9
	v_mul_f32_e32 v69, v69, v9
	v_mul_f32_e32 v70, v70, v9
	v_mul_f32_e32 v71, v71, v9
	v_mov_b32_e32 v27, v10
	v_cvt_pk_fp8_f32 v27, v68, v69
	v_cvt_pk_fp8_f32 v26, v66, v67 op_sel:[0,0,1]
	v_mul_f32_e32 v72, v72, v9
	v_mul_f32_e32 v73, v73, v9
	v_mul_f32_e32 v74, v74, v9
	v_mul_f32_e32 v75, v75, v9
	v_mov_b32_e32 v28, v10
	v_cvt_pk_fp8_f32 v28, v72, v73
	v_cvt_pk_fp8_f32 v27, v70, v71 op_sel:[0,0,1]
	v_mul_f32_e32 v76, v76, v9
	v_mul_f32_e32 v77, v77, v9
	v_mul_f32_e32 v78, v78, v9
	v_mul_f32_e32 v79, v79, v9
	v_mov_b32_e32 v29, v10
	v_cvt_pk_fp8_f32 v29, v76, v77
	v_cvt_pk_fp8_f32 v28, v74, v75 op_sel:[0,0,1]
	v_mul_f32_e32 v80, v80, v9
	v_mul_f32_e32 v81, v81, v9
	v_mul_f32_e32 v82, v82, v9
	v_mul_f32_e32 v83, v83, v9
	v_mov_b32_e32 v30, v10
	v_cvt_pk_fp8_f32 v30, v80, v81
	v_cvt_pk_fp8_f32 v29, v78, v79 op_sel:[0,0,1]
	v_mul_f32_e32 v84, v84, v9
	v_mul_f32_e32 v85, v85, v9
	v_mul_f32_e32 v86, v86, v9
	v_mul_f32_e32 v87, v87, v9
	v_mov_b32_e32 v31, v10
	v_cvt_pk_fp8_f32 v31, v84, v85
	v_cvt_pk_fp8_f32 v30, v82, v83 op_sel:[0,0,1]
	v_mul_f32_e32 v88, v88, v9
	v_mul_f32_e32 v89, v89, v9
	v_mul_f32_e32 v90, v90, v9
	v_mul_f32_e32 v91, v91, v9
	v_mov_b32_e32 v32, v10
	v_cvt_pk_fp8_f32 v32, v88, v89
	v_cvt_pk_fp8_f32 v31, v86, v87 op_sel:[0,0,1]
	v_mul_f32_e32 v92, v92, v9
	v_mul_f32_e32 v93, v93, v9
	v_mul_f32_e32 v94, v94, v9
	v_mul_f32_e32 v95, v95, v9
	v_mov_b32_e32 v33, v10
	v_cvt_pk_fp8_f32 v33, v92, v93
	v_cvt_pk_fp8_f32 v32, v90, v91 op_sel:[0,0,1]
	v_mul_f32_e32 v96, v96, v9
	v_mul_f32_e32 v97, v97, v9
	v_mul_f32_e32 v98, v98, v9
	v_mul_f32_e32 v99, v99, v9
	v_mov_b32_e32 v34, v10
	v_cvt_pk_fp8_f32 v34, v96, v97
	v_cvt_pk_fp8_f32 v33, v94, v95 op_sel:[0,0,1]
	v_mul_f32_e32 v100, v100, v9
	v_mul_f32_e32 v101, v101, v9
	v_mul_f32_e32 v102, v102, v9
	v_mul_f32_e32 v103, v103, v9
	v_mov_b32_e32 v35, v10
	v_cvt_pk_fp8_f32 v35, v100, v101
	v_cvt_pk_fp8_f32 v34, v98, v99 op_sel:[0,0,1]
	v_cvt_pk_fp8_f32 v35, v102, v103 op_sel:[0,0,1]
	s_nop 0
	v_mul_f32_e32 v8, 0x3b800000, v6
	global_store_dword v2, v20, s[8:9]
	global_store_dword v2, v21, s[8:9] offset:256
	global_store_dword v2, v22, s[8:9] offset:512
	global_store_dword v2, v23, s[8:9] offset:768
	global_store_dword v2, v24, s[8:9] offset:1024
	global_store_dword v2, v25, s[8:9] offset:1280
	global_store_dword v2, v26, s[8:9] offset:1536
	global_store_dword v2, v27, s[8:9] offset:1792
	global_store_dword v2, v28, s[8:9] offset:2048
	global_store_dword v2, v29, s[8:9] offset:2304
	global_store_dword v2, v30, s[8:9] offset:2560
	global_store_dword v2, v31, s[8:9] offset:2816
	global_store_dword v2, v32, s[8:9] offset:3072
	global_store_dword v2, v33, s[8:9] offset:3328
	global_store_dword v2, v34, s[8:9] offset:3584
	global_store_dword v2, v35, s[8:9] offset:3840
	s_mov_b64 s[18:19], exec
	s_mov_b64 exec, s[12:13]
	global_store_dword v10, v8, s[10:11]
	s_mov_b64 exec, s[18:19]
	s_mov_b32 s4, s5
	s_waitcnt vmcnt(32)
	v_max3_f32 v6, |v104|, |v105|, 0
	v_max3_f32 v6, |v106|, |v107|, v6
	s_waitcnt vmcnt(31)
	v_max3_f32 v6, |v108|, |v109|, v6
	v_max3_f32 v6, |v110|, |v111|, v6
	s_waitcnt vmcnt(30)
	v_max3_f32 v6, |v112|, |v113|, v6
	v_max3_f32 v6, |v114|, |v115|, v6
	s_waitcnt vmcnt(29)
	v_max3_f32 v6, |v116|, |v117|, v6
	v_max3_f32 v6, |v118|, |v119|, v6
	s_waitcnt vmcnt(28)
	v_max3_f32 v6, |v120|, |v121|, v6
	v_max3_f32 v6, |v122|, |v123|, v6
	s_waitcnt vmcnt(27)
	v_max3_f32 v6, |v124|, |v125|, v6
	v_max3_f32 v6, |v126|, |v127|, v6
	s_waitcnt vmcnt(26)
	v_max3_f32 v6, |v128|, |v129|, v6
	v_max3_f32 v6, |v130|, |v131|, v6
	s_waitcnt vmcnt(25)
	v_max3_f32 v6, |v132|, |v133|, v6
	v_max3_f32 v6, |v134|, |v135|, v6
	s_waitcnt vmcnt(24)
	v_max3_f32 v6, |v136|, |v137|, v6
	v_max3_f32 v6, |v138|, |v139|, v6
	s_waitcnt vmcnt(23)
	v_max3_f32 v6, |v140|, |v141|, v6
	v_max3_f32 v6, |v142|, |v143|, v6
	s_waitcnt vmcnt(22)
	v_max3_f32 v6, |v144|, |v145|, v6
	v_max3_f32 v6, |v146|, |v147|, v6
	s_waitcnt vmcnt(21)
	v_max3_f32 v6, |v148|, |v149|, v6
	v_max3_f32 v6, |v150|, |v151|, v6
	s_waitcnt vmcnt(20)
	v_max3_f32 v6, |v152|, |v153|, v6
	v_max3_f32 v6, |v154|, |v155|, v6
	s_waitcnt vmcnt(19)
	v_max3_f32 v6, |v156|, |v157|, v6
	v_max3_f32 v6, |v158|, |v159|, v6
	s_waitcnt vmcnt(18)
	v_max3_f32 v6, |v160|, |v161|, v6
	v_max3_f32 v6, |v162|, |v163|, v6
	s_waitcnt vmcnt(17)
; template <int CTRL> __device__ __forceinline__ unsigned dppu(unsigned x) { return (unsigned)__builtin_amdgcn_mov_dpp((int)x, CTRL, 0xf, 0xf, true); }
; __device__ __forceinline__ unsigned max64u(unsigned x) {
;     x = umax_u(x, dppu<DPP_XOR1>(x)); x = umax_u(x, dppu<DPP_XOR2>(x)); x = umax_u(x, dppu<DPP_HMIRROR>(x)); x = umax_u(x, dppu<DPP_MIRROR>(x));
;     auto s = __builtin_amdgcn_permlane16_swap(x, x, false, false); x = umax_u(s[0], s[1]);
;     auto t = __builtin_amdgcn_permlane32_swap(x, x, false, false); return umax_u(t[0], t[1]);
; }
; __device__ __forceinline__ void peer_row_store(const f32x4 (&v)[16], unsigned char* ws, int it, int layer, int lane) {
;     const int tbl = it >= NEXP, r = it - tbl * NEXP + layer * NEXP;
;     float am = 0.f;
; #pragma unroll
;     for (int j = 0; j < 16; ++j) am = fmaxf(fmaxf(am, fmaxf(fabsf(v[j][0]), fabsf(v[j][1]))), fmaxf(fabsf(v[j][2]), fabsf(v[j][3])));
;     am = __uint_as_float(max64u(__float_as_uint(am)));
;     const float q = am > 0.f ? 256.0f / am : 0.f;
;     unsigned* dst = (unsigned*)(ws + (tbl ? WS_PV : WS_PU) + (size_t)r * D) + lane;
;     if (tbl) {
;         const int rl = it - NEXP;
;         unsigned char* pvl = ws + WS_PV + (size_t)layer * NEXP * D + (size_t)rl * 8 + (lane & 1) * 4;
;         unsigned char* pvg = ws + WS_PV + (size_t)layer * NEXP * D + (size_t)NEXP * 2048 + (size_t)rl * 2048 + 4 * lane;
; #pragma unroll
;         for (int j = 0; j < 16; ++j) { int w = __builtin_amdgcn_cvt_pk_bf8_f32(v[j][0] * q, v[j][1] * q, 0, false); w = __builtin_amdgcn_cvt_pk_bf8_f32(v[j][2] * q, v[j][3] * q, w, true);
;             if (j < 8) *(unsigned*)(pvl + (size_t)((lane >> 1) + 32 * j) * (NEXP * 8)) = (unsigned)w;
;             else *(unsigned*)(pvg + 256 * (j - 8)) = (unsigned)w; }
;     } else {
; #pragma unroll
;         for (int j = 0; j < 16; ++j) { int w = __builtin_amdgcn_cvt_pk_fp8_f32(v[j][0] * q, v[j][1] * q, 0, false); w = __builtin_amdgcn_cvt_pk_fp8_f32(v[j][2] * q, v[j][3] * q, w, true); dst[64 * j] = (unsigned)w; }
;     }
;     if (lane == 0) ((float*)(ws + (tbl ? WS_SV : WS_SU)))[r] = am * (1.0f / 256.0f);
; }
	v_max3_f32 v6, |v164|, |v165|, v6
	v_max3_f32 v6, |v166|, |v167|, v6
	s_nop 1
	v_max_u32_dpp v6, v6, v6 quad_perm:[1,0,3,2] row_mask:0xf bank_mask:0xf bound_ctrl:1
	s_nop 1
	v_max_u32_dpp v6, v6, v6 quad_perm:[2,3,0,1] row_mask:0xf bank_mask:0xf bound_ctrl:1
	s_nop 1
	v_max_u32_dpp v6, v6, v6 row_half_mirror row_mask:0xf bank_mask:0xf bound_ctrl:1
	s_nop 1
	v_max_u32_dpp v6, v6, v6 row_mirror row_mask:0xf bank_mask:0xf bound_ctrl:1
	s_nop 1
	v_mov_b32_e32 v7, v6
	s_nop 1
	v_permlane16_swap_b32_e32 v6, v7
	v_max_u32_e32 v6, v6, v7
	v_mov_b32_e32 v7, v6
	s_nop 1
	v_permlane32_swap_b32_e32 v6, v7
	v_max_u32_e32 v6, v6, v7
	v_div_scale_f32 v12, s[16:17], v6, v6, s14
	v_rcp_f32_e32 v13, v12
	s_nop 0
	v_fma_f32 v14, -v12, v13, 1.0
	v_fmac_f32_e32 v13, v14, v13
	v_div_scale_f32 v14, vcc, s14, v6, s14
	v_mul_f32_e32 v15, v14, v13
	v_fma_f32 v16, -v12, v15, v14
	v_fmac_f32_e32 v15, v16, v13
	v_fma_f32 v12, -v12, v15, v14
	v_div_fmas_f32 v12, v12, v13, v15
	v_div_fixup_f32 v9, v12, v6, s14
	v_cmp_lt_f32_e32 vcc, 0, v6
	s_nop 1
	v_cndmask_b32_e32 v9, 0, v9, vcc
	s_lshl_b32 s1, s4, 12
	s_add_u32 s8, s90, 0xba00000
	s_addc_u32 s9, s91, 0
	s_add_u32 s8, s8, s1
	s_addc_u32 s9, s9, 0
	s_lshl_b32 s1, s4, 2
	s_add_u32 s10, s90, 0x1ba00000
	s_addc_u32 s11, s91, 0
	s_add_u32 s10, s10, s1
	s_addc_u32 s11, s11, 0
	v_mul_f32_e32 v104, v104, v9
	v_mul_f32_e32 v105, v105, v9
	v_mul_f32_e32 v106, v106, v9
	v_mul_f32_e32 v107, v107, v9
	v_mov_b32_e32 v20, v10
	v_cvt_pk_fp8_f32 v20, v104, v105
	v_mul_f32_e32 v108, v108, v9
	v_mul_f32_e32 v109, v109, v9
	v_mul_f32_e32 v110, v110, v9
	v_mul_f32_e32 v111, v111, v9
	v_mov_b32_e32 v21, v10
	v_cvt_pk_fp8_f32 v21, v108, v109
	v_cvt_pk_fp8_f32 v20, v106, v107 op_sel:[0,0,1]
	v_mul_f32_e32 v112, v112, v9
	v_mul_f32_e32 v113, v113, v9
	v_mul_f32_e32 v114, v114, v9
	v_mul_f32_e32 v115, v115, v9
	v_mov_b32_e32 v22, v10
	v_cvt_pk_fp8_f32 v22, v112, v113
	v_cvt_pk_fp8_f32 v21, v110, v111 op_sel:[0,0,1]
	v_mul_f32_e32 v116, v116, v9
	v_mul_f32_e32 v117, v117, v9
	v_mul_f32_e32 v118, v118, v9
	v_mul_f32_e32 v119, v119, v9
	v_mov_b32_e32 v23, v10
	v_cvt_pk_fp8_f32 v23, v116, v117
	v_cvt_pk_fp8_f32 v22, v114, v115 op_sel:[0,0,1]
	v_mul_f32_e32 v120, v120, v9
	v_mul_f32_e32 v121, v121, v9
	v_mul_f32_e32 v122, v122, v9
	v_mul_f32_e32 v123, v123, v9
	v_mov_b32_e32 v24, v10
	v_cvt_pk_fp8_f32 v24, v120, v121
	v_cvt_pk_fp8_f32 v23, v118, v119 op_sel:[0,0,1]
	v_mul_f32_e32 v124, v124, v9
	v_mul_f32_e32 v125, v125, v9
	v_mul_f32_e32 v126, v126, v9
	v_mul_f32_e32 v127, v127, v9
	v_mov_b32_e32 v25, v10
	v_cvt_pk_fp8_f32 v25, v124, v125
	v_cvt_pk_fp8_f32 v24, v122, v123 op_sel:[0,0,1]
	v_mul_f32_e32 v128, v128, v9
	v_mul_f32_e32 v129, v129, v9
	v_mul_f32_e32 v130, v130, v9
	v_mul_f32_e32 v131, v131, v9
	v_mov_b32_e32 v26, v10
	v_cvt_pk_fp8_f32 v26, v128, v129
	v_cvt_pk_fp8_f32 v25, v126, v127 op_sel:[0,0,1]
	v_mul_f32_e32 v132, v132, v9
	v_mul_f32_e32 v133, v133, v9
	v_mul_f32_e32 v134, v134, v9
	v_mul_f32_e32 v135, v135, v9
	v_mov_b32_e32 v27, v10
	v_cvt_pk_fp8_f32 v27, v132, v133
	v_cvt_pk_fp8_f32 v26, v130, v131 op_sel:[0,0,1]
	v_mul_f32_e32 v136, v136, v9
	v_mul_f32_e32 v137, v137, v9
	v_mul_f32_e32 v138, v138, v9
	v_mul_f32_e32 v139, v139, v9
	v_mov_b32_e32 v28, v10
	v_cvt_pk_fp8_f32 v28, v136, v137
	v_cvt_pk_fp8_f32 v27, v134, v135 op_sel:[0,0,1]
	v_mul_f32_e32 v140, v140, v9
	v_mul_f32_e32 v141, v141, v9
	v_mul_f32_e32 v142, v142, v9
	v_mul_f32_e32 v143, v143, v9
	v_mov_b32_e32 v29, v10
	v_cvt_pk_fp8_f32 v29, v140, v141
	v_cvt_pk_fp8_f32 v28, v138, v139 op_sel:[0,0,1]
	v_mul_f32_e32 v144, v144, v9
	v_mul_f32_e32 v145, v145, v9
	v_mul_f32_e32 v146, v146, v9
	v_mul_f32_e32 v147, v147, v9
	v_mov_b32_e32 v30, v10
	v_cvt_pk_fp8_f32 v30, v144, v145
	v_cvt_pk_fp8_f32 v29, v142, v143 op_sel:[0,0,1]
	v_mul_f32_e32 v148, v148, v9
	v_mul_f32_e32 v149, v149, v9
	v_mul_f32_e32 v150, v150, v9
	v_mul_f32_e32 v151, v151, v9
	v_mov_b32_e32 v31, v10
	v_cvt_pk_fp8_f32 v31, v148, v149
	v_cvt_pk_fp8_f32 v30, v146, v147 op_sel:[0,0,1]
	v_mul_f32_e32 v152, v152, v9
	v_mul_f32_e32 v153, v153, v9
	v_mul_f32_e32 v154, v154, v9
	v_mul_f32_e32 v155, v155, v9
	v_mov_b32_e32 v32, v10
	v_cvt_pk_fp8_f32 v32, v152, v153
	v_cvt_pk_fp8_f32 v31, v150, v151 op_sel:[0,0,1]
	v_mul_f32_e32 v156, v156, v9
	v_mul_f32_e32 v157, v157, v9
	v_mul_f32_e32 v158, v158, v9
	v_mul_f32_e32 v159, v159, v9
	v_mov_b32_e32 v33, v10
	v_cvt_pk_fp8_f32 v33, v156, v157
	v_cvt_pk_fp8_f32 v32, v154, v155 op_sel:[0,0,1]
	v_mul_f32_e32 v160, v160, v9
	v_mul_f32_e32 v161, v161, v9
	v_mul_f32_e32 v162, v162, v9
	v_mul_f32_e32 v163, v163, v9
	v_mov_b32_e32 v34, v10
	v_cvt_pk_fp8_f32 v34, v160, v161
	v_cvt_pk_fp8_f32 v33, v158, v159 op_sel:[0,0,1]
	v_mul_f32_e32 v164, v164, v9
	v_mul_f32_e32 v165, v165, v9
	v_mul_f32_e32 v166, v166, v9
	v_mul_f32_e32 v167, v167, v9
	v_mov_b32_e32 v35, v10
	v_cvt_pk_fp8_f32 v35, v164, v165
	v_cvt_pk_fp8_f32 v34, v162, v163 op_sel:[0,0,1]
	v_cvt_pk_fp8_f32 v35, v166, v167 op_sel:[0,0,1]
	s_nop 0
	v_mul_f32_e32 v8, 0x3b800000, v6
	global_store_dword v2, v20, s[8:9]
	global_store_dword v2, v21, s[8:9] offset:256
	global_store_dword v2, v22, s[8:9] offset:512
	global_store_dword v2, v23, s[8:9] offset:768
	global_store_dword v2, v24, s[8:9] offset:1024
	global_store_dword v2, v25, s[8:9] offset:1280
	global_store_dword v2, v26, s[8:9] offset:1536
	global_store_dword v2, v27, s[8:9] offset:1792
	global_store_dword v2, v28, s[8:9] offset:2048
	global_store_dword v2, v29, s[8:9] offset:2304
	global_store_dword v2, v30, s[8:9] offset:2560
	global_store_dword v2, v31, s[8:9] offset:2816
	global_store_dword v2, v32, s[8:9] offset:3072
	global_store_dword v2, v33, s[8:9] offset:3328
	global_store_dword v2, v34, s[8:9] offset:3584
	global_store_dword v2, v35, s[8:9] offset:3840
	s_mov_b64 s[18:19], exec
	s_mov_b64 exec, s[12:13]
	global_store_dword v10, v8, s[10:11]
	s_mov_b64 exec, s[18:19]
	s_waitcnt vmcnt(0)
